# v046 + vmcnt/lgkmcnt waits in front of each K-loop load-segment barrier merged into one s_waitcnt
# speedup vs baseline: 1.0029x; 1.0029x over previous
.LBB0_260:
	s_ashr_i32 s69, s68, 31
	s_lshl_b64 s[26:27], s[68:69], 20
	v_readlane_b32 s8, v254, 56
	v_readlane_b32 s9, v254, 57
	s_add_u32 s70, s8, s26
	s_addc_u32 s71, s9, s27
	s_and_b64 s[26:27], s[0:1], exec
	s_cselect_b32 s69, s71, s83
	s_cselect_b32 s75, s70, s82
	s_ashr_i32 s57, s56, 31
	s_lshl_b64 s[26:27], s[56:57], 20
	s_add_u32 s72, s84, s26
	s_addc_u32 s73, s85, s27
	s_and_b64 s[26:27], s[0:1], exec
	s_cselect_b32 s57, s73, s81
	s_cselect_b32 s96, s72, s80
	s_add_u32 s97, s80, 0x10000
	s_addc_u32 vcc_lo, s81, 0
	s_add_u32 s80, s82, 0x80080
	s_addc_u32 s81, s83, 0
	s_mov_b32 vcc_hi, -2
	ds_read_b128 v[144:147], v170
	ds_read_b128 v[148:151], v170 offset:1024
	ds_read_b128 v[174:177], v170 offset:2048
	ds_read_b128 v[178:181], v170 offset:3072
	ds_read_b128 v[182:185], v171
	ds_read_b128 v[186:189], v171 offset:1024
	ds_read_b128 v[190:193], v171 offset:2048
	ds_read_b128 v[194:197], v171 offset:3072
	s_add_u32 s26, s80, 0xfff80080
	s_addc_u32 s27, s81, -1
	s_cmp_eq_u32 vcc_hi, 28
	s_cselect_b32 s83, s69, s27
	s_cselect_b32 s82, s75, s26
	s_cselect_b32 s27, s57, vcc_lo
	s_cselect_b32 s26, s96, s97
	v_lshl_add_u64 v[152:153], s[80:81], 0, v[134:135]
	s_add_i32 m0, s87, 0xc000
	ds_read_b128 v[198:201], v172
	ds_read_b128 v[202:205], v172 offset:1024
	ds_read_b128 v[206:209], v172 offset:2048
	ds_read_b128 v[210:213], v172 offset:3072
	ds_read_b128 v[214:217], v172 offset:4096
	ds_read_b128 v[220:223], v172 offset:5120
	ds_read_b128 v[224:227], v172 offset:6144
	ds_read_b128 v[228:231], v172 offset:7168
	global_load_lds_dwordx4 v[152:153], off
	v_lshl_add_u64 v[152:153], s[80:81], 0, v[138:139]
	s_add_i32 m0, s87, 0xe000
	s_nop 0
	global_load_lds_dwordx4 v[152:153], off
	s_waitcnt vmcnt(8) lgkmcnt(0)
	s_barrier
	v_mfma_f32_16x16x32_bf16 v[122:125], v[144:147], v[198:201], 0
	v_mfma_f32_16x16x32_bf16 v[118:121], v[174:177], v[198:201], 0
	v_mfma_f32_16x16x32_bf16 v[106:109], v[144:147], v[206:209], 0
	v_mfma_f32_16x16x32_bf16 v[102:105], v[174:177], v[206:209], 0
	v_mfma_f32_16x16x32_bf16 v[90:93], v[144:147], v[214:217], 0
	v_mfma_f32_16x16x32_bf16 v[86:89], v[174:177], v[214:217], 0
	v_mfma_f32_16x16x32_bf16 v[74:77], v[144:147], v[224:227], 0
	v_mfma_f32_16x16x32_bf16 v[70:73], v[174:177], v[224:227], 0
	v_mfma_f32_16x16x32_bf16 v[122:125], v[148:151], v[202:205], v[122:125]
	v_mfma_f32_16x16x32_bf16 v[118:121], v[178:181], v[202:205], v[118:121]
	v_mfma_f32_16x16x32_bf16 v[106:109], v[148:151], v[210:213], v[106:109]
	v_mfma_f32_16x16x32_bf16 v[102:105], v[178:181], v[210:213], v[102:105]
	v_mfma_f32_16x16x32_bf16 v[90:93], v[148:151], v[220:223], v[90:93]
	v_mfma_f32_16x16x32_bf16 v[86:89], v[178:181], v[220:223], v[86:89]
	v_mfma_f32_16x16x32_bf16 v[74:77], v[148:151], v[228:231], v[74:77]
	v_mfma_f32_16x16x32_bf16 v[70:73], v[178:181], v[228:231], v[70:73]
	v_mfma_f32_16x16x32_bf16 v[126:129], v[182:185], v[198:201], 0
	v_mfma_f32_16x16x32_bf16 v[114:117], v[190:193], v[198:201], 0
	v_mfma_f32_16x16x32_bf16 v[110:113], v[182:185], v[206:209], 0
	v_mfma_f32_16x16x32_bf16 v[98:101], v[190:193], v[206:209], 0
	v_mfma_f32_16x16x32_bf16 v[94:97], v[182:185], v[214:217], 0
	v_mfma_f32_16x16x32_bf16 v[82:85], v[190:193], v[214:217], 0
	v_mfma_f32_16x16x32_bf16 v[78:81], v[182:185], v[224:227], 0
	v_mfma_f32_16x16x32_bf16 v[66:69], v[190:193], v[224:227], 0
	v_mfma_f32_16x16x32_bf16 v[126:129], v[186:189], v[202:205], v[126:129]
	v_mfma_f32_16x16x32_bf16 v[114:117], v[194:197], v[202:205], v[114:117]
	v_mfma_f32_16x16x32_bf16 v[110:113], v[186:189], v[210:213], v[110:113]
	v_mfma_f32_16x16x32_bf16 v[98:101], v[194:197], v[210:213], v[98:101]
	v_mfma_f32_16x16x32_bf16 v[94:97], v[186:189], v[220:223], v[94:97]
	v_mfma_f32_16x16x32_bf16 v[82:85], v[194:197], v[220:223], v[82:85]
	v_mfma_f32_16x16x32_bf16 v[78:81], v[186:189], v[228:231], v[78:81]
	v_mfma_f32_16x16x32_bf16 v[66:69], v[194:197], v[228:231], v[66:69]
	s_barrier
	v_lshl_add_u64 v[152:153], s[26:27], 0, v[162:163]
	s_add_i32 s26, s94, s86
	s_mov_b32 m0, s26
	ds_read_b128 v[198:201], v172 offset:16384
	ds_read_b128 v[202:205], v172 offset:17408
	ds_read_b128 v[206:209], v172 offset:18432
	ds_read_b128 v[210:213], v172 offset:19456
	ds_read_b128 v[214:217], v172 offset:20480
	ds_read_b128 v[220:223], v172 offset:21504
	ds_read_b128 v[224:227], v172 offset:22528
	ds_read_b128 v[228:231], v172 offset:23552
	global_load_lds_dwordx4 v[152:153], off
	v_lshl_add_u64 v[232:233], v[152:153], 0, s[10:11]
	s_add_i32 m0, s26, 0x2000
	s_add_i32 s26, s95, s86
	global_load_lds_dwordx4 v[232:233], off
	v_lshl_add_u64 v[232:233], v[152:153], 0, s[12:13]
	s_mov_b32 m0, s26
	v_lshl_add_u64 v[234:235], s[82:83], 0, v[132:133]
	global_load_lds_dwordx4 v[232:233], off
	v_lshl_add_u64 v[232:233], v[152:153], 0, s[14:15]
	s_add_i32 m0, s26, 0x2000
	s_nop 0
	global_load_lds_dwordx4 v[232:233], off
	v_lshl_add_u64 v[232:233], s[82:83], 0, v[130:131]
	s_mov_b32 m0, s87
	s_nop 0
	global_load_lds_dwordx4 v[232:233], off
	s_mov_b32 m0, s88
	s_nop 0
	global_load_lds_dwordx4 v[234:235], off
	s_waitcnt vmcnt(8) lgkmcnt(0)
	s_barrier
	v_mfma_f32_16x16x32_bf16 v[58:61], v[144:147], v[198:201], 0
	v_mfma_f32_16x16x32_bf16 v[54:57], v[174:177], v[198:201], 0
	v_mfma_f32_16x16x32_bf16 v[42:45], v[144:147], v[206:209], 0
	v_mfma_f32_16x16x32_bf16 v[38:41], v[174:177], v[206:209], 0
	v_mfma_f32_16x16x32_bf16 v[26:29], v[144:147], v[214:217], 0
	v_mfma_f32_16x16x32_bf16 v[22:25], v[174:177], v[214:217], 0
	v_mfma_f32_16x16x32_bf16 v[10:13], v[144:147], v[224:227], 0
	v_mfma_f32_16x16x32_bf16 v[6:9], v[174:177], v[224:227], 0
	v_mfma_f32_16x16x32_bf16 v[58:61], v[148:151], v[202:205], v[58:61]
	v_mfma_f32_16x16x32_bf16 v[54:57], v[178:181], v[202:205], v[54:57]
	v_mfma_f32_16x16x32_bf16 v[42:45], v[148:151], v[210:213], v[42:45]
	v_mfma_f32_16x16x32_bf16 v[38:41], v[178:181], v[210:213], v[38:41]
	v_mfma_f32_16x16x32_bf16 v[26:29], v[148:151], v[220:223], v[26:29]
	v_mfma_f32_16x16x32_bf16 v[22:25], v[178:181], v[220:223], v[22:25]
	v_mfma_f32_16x16x32_bf16 v[10:13], v[148:151], v[228:231], v[10:13]
	v_mfma_f32_16x16x32_bf16 v[6:9], v[178:181], v[228:231], v[6:9]
	v_mfma_f32_16x16x32_bf16 v[62:65], v[182:185], v[198:201], 0
	v_mfma_f32_16x16x32_bf16 v[50:53], v[190:193], v[198:201], 0
	v_mfma_f32_16x16x32_bf16 v[46:49], v[182:185], v[206:209], 0
	v_mfma_f32_16x16x32_bf16 v[34:37], v[190:193], v[206:209], 0
	v_mfma_f32_16x16x32_bf16 v[30:33], v[182:185], v[214:217], 0
	v_mfma_f32_16x16x32_bf16 v[18:21], v[190:193], v[214:217], 0
	v_mfma_f32_16x16x32_bf16 v[14:17], v[182:185], v[224:227], 0
	v_mfma_f32_16x16x32_bf16 v[2:5], v[190:193], v[224:227], 0
	v_mfma_f32_16x16x32_bf16 v[62:65], v[186:189], v[202:205], v[62:65]
	v_mfma_f32_16x16x32_bf16 v[50:53], v[194:197], v[202:205], v[50:53]
	v_mfma_f32_16x16x32_bf16 v[46:49], v[186:189], v[210:213], v[46:49]
	v_mfma_f32_16x16x32_bf16 v[34:37], v[194:197], v[210:213], v[34:37]
	v_mfma_f32_16x16x32_bf16 v[30:33], v[186:189], v[220:223], v[30:33]
	v_mfma_f32_16x16x32_bf16 v[18:21], v[194:197], v[220:223], v[18:21]
	v_mfma_f32_16x16x32_bf16 v[14:17], v[186:189], v[228:231], v[14:17]
	v_mfma_f32_16x16x32_bf16 v[2:5], v[194:197], v[228:231], v[2:5]
	s_barrier
	s_add_i32 s33, 0, 0x18000
	v_add_u32_e32 v136, s33, v167
	s_add_i32 s8, 0, 0x1c000
	ds_read_b128 v[144:147], v136
	ds_read_b128 v[148:151], v136 offset:1024
	ds_read_b128 v[174:177], v136 offset:2048
	ds_read_b128 v[178:181], v136 offset:3072
	v_add_u32_e32 v136, s8, v167
	ds_read_b128 v[182:185], v136
	ds_read_b128 v[186:189], v136 offset:1024
	ds_read_b128 v[190:193], v136 offset:2048
	ds_read_b128 v[194:197], v136 offset:3072
	s_add_u32 s26, s82, 0x80000
	s_addc_u32 s27, s83, 0
	s_mov_b32 m0, s89
	v_lshl_add_u64 v[236:237], s[26:27], 0, v[130:131]
	ds_read_b128 v[198:201], v172 offset:32768
	ds_read_b128 v[202:205], v172 offset:33792
	ds_read_b128 v[206:209], v172 offset:34816
	ds_read_b128 v[210:213], v172 offset:35840
	ds_read_b128 v[214:217], v172 offset:36864
	ds_read_b128 v[220:223], v172 offset:37888
	ds_read_b128 v[224:227], v172 offset:38912
	ds_read_b128 v[228:231], v172 offset:39936
	global_load_lds_dwordx4 v[236:237], off
	v_lshl_add_u64 v[236:237], s[26:27], 0, v[132:133]
	s_mov_b32 m0, s90
	s_nop 0
	global_load_lds_dwordx4 v[236:237], off
	s_waitcnt vmcnt(8) lgkmcnt(0)
	s_barrier
	v_mfma_f32_16x16x32_bf16 v[122:125], v[144:147], v[198:201], v[122:125]
	v_mfma_f32_16x16x32_bf16 v[118:121], v[174:177], v[198:201], v[118:121]
	v_mfma_f32_16x16x32_bf16 v[106:109], v[144:147], v[206:209], v[106:109]
	v_mfma_f32_16x16x32_bf16 v[102:105], v[174:177], v[206:209], v[102:105]
	v_mfma_f32_16x16x32_bf16 v[90:93], v[144:147], v[214:217], v[90:93]
	v_mfma_f32_16x16x32_bf16 v[86:89], v[174:177], v[214:217], v[86:89]
	v_mfma_f32_16x16x32_bf16 v[74:77], v[144:147], v[224:227], v[74:77]
	v_mfma_f32_16x16x32_bf16 v[70:73], v[174:177], v[224:227], v[70:73]
	v_mfma_f32_16x16x32_bf16 v[122:125], v[148:151], v[202:205], v[122:125]
	v_mfma_f32_16x16x32_bf16 v[118:121], v[178:181], v[202:205], v[118:121]
	v_mfma_f32_16x16x32_bf16 v[106:109], v[148:151], v[210:213], v[106:109]
	v_mfma_f32_16x16x32_bf16 v[102:105], v[178:181], v[210:213], v[102:105]
	v_mfma_f32_16x16x32_bf16 v[90:93], v[148:151], v[220:223], v[90:93]
	v_mfma_f32_16x16x32_bf16 v[86:89], v[178:181], v[220:223], v[86:89]
	v_mfma_f32_16x16x32_bf16 v[74:77], v[148:151], v[228:231], v[74:77]
	v_mfma_f32_16x16x32_bf16 v[70:73], v[178:181], v[228:231], v[70:73]
	v_mfma_f32_16x16x32_bf16 v[126:129], v[182:185], v[198:201], v[126:129]
	v_mfma_f32_16x16x32_bf16 v[114:117], v[190:193], v[198:201], v[114:117]
	v_mfma_f32_16x16x32_bf16 v[110:113], v[182:185], v[206:209], v[110:113]
	v_mfma_f32_16x16x32_bf16 v[98:101], v[190:193], v[206:209], v[98:101]
	v_mfma_f32_16x16x32_bf16 v[94:97], v[182:185], v[214:217], v[94:97]
	v_mfma_f32_16x16x32_bf16 v[82:85], v[190:193], v[214:217], v[82:85]
	v_mfma_f32_16x16x32_bf16 v[78:81], v[182:185], v[224:227], v[78:81]
	v_mfma_f32_16x16x32_bf16 v[66:69], v[190:193], v[224:227], v[66:69]
	v_mfma_f32_16x16x32_bf16 v[126:129], v[186:189], v[202:205], v[126:129]
	v_mfma_f32_16x16x32_bf16 v[114:117], v[194:197], v[202:205], v[114:117]
	v_mfma_f32_16x16x32_bf16 v[110:113], v[186:189], v[210:213], v[110:113]
	v_mfma_f32_16x16x32_bf16 v[98:101], v[194:197], v[210:213], v[98:101]
	v_mfma_f32_16x16x32_bf16 v[94:97], v[186:189], v[220:223], v[94:97]
	v_mfma_f32_16x16x32_bf16 v[82:85], v[194:197], v[220:223], v[82:85]
	v_mfma_f32_16x16x32_bf16 v[78:81], v[186:189], v[228:231], v[78:81]
	v_mfma_f32_16x16x32_bf16 v[66:69], v[194:197], v[228:231], v[66:69]
	s_barrier
	s_add_i32 s9, s33, s86
	v_lshl_add_u64 v[236:237], v[152:153], 0, s[20:21]
	s_mov_b32 m0, s9
	ds_read_b128 v[198:201], v172 offset:49152
	ds_read_b128 v[202:205], v172 offset:50176
	ds_read_b128 v[206:209], v172 offset:51200
	ds_read_b128 v[210:213], v172 offset:52224
	ds_read_b128 v[214:217], v172 offset:53248
	ds_read_b128 v[220:223], v172 offset:54272
	ds_read_b128 v[224:227], v172 offset:55296
	ds_read_b128 v[228:231], v172 offset:56320
	global_load_lds_dwordx4 v[236:237], off
	v_lshl_add_u64 v[236:237], v[152:153], 0, s[22:23]
	s_add_i32 m0, s9, 0x2000
	s_add_i32 s8, s8, s86
	global_load_lds_dwordx4 v[236:237], off
	v_lshl_add_u64 v[236:237], v[152:153], 0, s[40:41]
	s_mov_b32 m0, s8
	v_lshl_add_u64 v[152:153], v[152:153], 0, s[44:45]
	global_load_lds_dwordx4 v[236:237], off
	s_add_i32 m0, s8, 0x2000
	s_nop 0
	global_load_lds_dwordx4 v[152:153], off
	v_lshl_add_u64 v[152:153], v[232:233], 0, s[24:25]
	s_mov_b32 m0, s91
	s_nop 0
	global_load_lds_dwordx4 v[152:153], off
	v_lshl_add_u64 v[152:153], v[234:235], 0, s[24:25]
	s_mov_b32 m0, s92
	s_nop 0
	global_load_lds_dwordx4 v[152:153], off
	s_waitcnt vmcnt(8) lgkmcnt(0)
	s_barrier
	v_mfma_f32_16x16x32_bf16 v[58:61], v[144:147], v[198:201], v[58:61]
	v_mfma_f32_16x16x32_bf16 v[54:57], v[174:177], v[198:201], v[54:57]
	v_mfma_f32_16x16x32_bf16 v[42:45], v[144:147], v[206:209], v[42:45]
	v_mfma_f32_16x16x32_bf16 v[38:41], v[174:177], v[206:209], v[38:41]
	v_mfma_f32_16x16x32_bf16 v[26:29], v[144:147], v[214:217], v[26:29]
	v_mfma_f32_16x16x32_bf16 v[22:25], v[174:177], v[214:217], v[22:25]
	v_mfma_f32_16x16x32_bf16 v[10:13], v[144:147], v[224:227], v[10:13]
	v_mfma_f32_16x16x32_bf16 v[6:9], v[174:177], v[224:227], v[6:9]
	v_mfma_f32_16x16x32_bf16 v[58:61], v[148:151], v[202:205], v[58:61]
	v_mfma_f32_16x16x32_bf16 v[54:57], v[178:181], v[202:205], v[54:57]
	v_mfma_f32_16x16x32_bf16 v[42:45], v[148:151], v[210:213], v[42:45]
	v_mfma_f32_16x16x32_bf16 v[38:41], v[178:181], v[210:213], v[38:41]
	v_mfma_f32_16x16x32_bf16 v[26:29], v[148:151], v[220:223], v[26:29]
	v_mfma_f32_16x16x32_bf16 v[22:25], v[178:181], v[220:223], v[22:25]
	v_mfma_f32_16x16x32_bf16 v[10:13], v[148:151], v[228:231], v[10:13]
	v_mfma_f32_16x16x32_bf16 v[6:9], v[178:181], v[228:231], v[6:9]
	v_mfma_f32_16x16x32_bf16 v[62:65], v[182:185], v[198:201], v[62:65]
	v_mfma_f32_16x16x32_bf16 v[50:53], v[190:193], v[198:201], v[50:53]
	v_mfma_f32_16x16x32_bf16 v[46:49], v[182:185], v[206:209], v[46:49]
	v_mfma_f32_16x16x32_bf16 v[34:37], v[190:193], v[206:209], v[34:37]
	v_mfma_f32_16x16x32_bf16 v[30:33], v[182:185], v[214:217], v[30:33]
	v_mfma_f32_16x16x32_bf16 v[18:21], v[190:193], v[214:217], v[18:21]
	v_mfma_f32_16x16x32_bf16 v[14:17], v[182:185], v[224:227], v[14:17]
	v_mfma_f32_16x16x32_bf16 v[2:5], v[190:193], v[224:227], v[2:5]
	v_mfma_f32_16x16x32_bf16 v[62:65], v[186:189], v[202:205], v[62:65]
	v_mfma_f32_16x16x32_bf16 v[50:53], v[194:197], v[202:205], v[50:53]
	v_mfma_f32_16x16x32_bf16 v[46:49], v[186:189], v[210:213], v[46:49]
	v_mfma_f32_16x16x32_bf16 v[34:37], v[194:197], v[210:213], v[34:37]
	v_mfma_f32_16x16x32_bf16 v[30:33], v[186:189], v[220:223], v[30:33]
	v_mfma_f32_16x16x32_bf16 v[18:21], v[194:197], v[220:223], v[18:21]
	v_mfma_f32_16x16x32_bf16 v[14:17], v[186:189], v[228:231], v[14:17]
	v_mfma_f32_16x16x32_bf16 v[2:5], v[194:197], v[228:231], v[2:5]
	s_barrier
	s_add_i32 vcc_hi, vcc_hi, 2
	s_add_u32 s97, s97, 0x10000
	s_addc_u32 vcc_lo, vcc_lo, 0
	s_add_u32 s80, s80, 0x100
	s_addc_u32 s81, s81, 0
	s_cmp_gt_u32 vcc_hi, 29
.LBB0_261:
	ds_read_b128 v[144:147], v170
	ds_read_b128 v[148:151], v170 offset:1024
	ds_read_b128 v[174:177], v170 offset:2048
	ds_read_b128 v[178:181], v170 offset:3072
	ds_read_b128 v[182:185], v171
	ds_read_b128 v[186:189], v171 offset:1024
	ds_read_b128 v[190:193], v171 offset:2048
	ds_read_b128 v[194:197], v171 offset:3072
	s_add_u32 s26, s80, 0xfff80080
	s_addc_u32 s27, s81, -1
	s_cmp_eq_u32 vcc_hi, 28
	s_cselect_b32 s83, s69, s27
	s_cselect_b32 s82, s75, s26
	s_cselect_b32 s27, s57, vcc_lo
	s_cselect_b32 s26, s96, s97
	v_lshl_add_u64 v[152:153], s[80:81], 0, v[134:135]
	s_add_i32 m0, s87, 0xc000
	ds_read_b128 v[198:201], v172
	ds_read_b128 v[202:205], v172 offset:1024
	ds_read_b128 v[206:209], v172 offset:2048
	ds_read_b128 v[210:213], v172 offset:3072
	ds_read_b128 v[214:217], v172 offset:4096
	ds_read_b128 v[220:223], v172 offset:5120
	ds_read_b128 v[224:227], v172 offset:6144
	ds_read_b128 v[228:231], v172 offset:7168
	global_load_lds_dwordx4 v[152:153], off
	v_lshl_add_u64 v[152:153], s[80:81], 0, v[138:139]
	s_add_i32 m0, s87, 0xe000
	s_nop 0
	global_load_lds_dwordx4 v[152:153], off
	s_waitcnt vmcnt(8) lgkmcnt(0)
	s_barrier
	v_mfma_f32_16x16x32_bf16 v[122:125], v[144:147], v[198:201], v[122:125]
	v_mfma_f32_16x16x32_bf16 v[118:121], v[174:177], v[198:201], v[118:121]
	v_mfma_f32_16x16x32_bf16 v[106:109], v[144:147], v[206:209], v[106:109]
	v_mfma_f32_16x16x32_bf16 v[102:105], v[174:177], v[206:209], v[102:105]
	v_mfma_f32_16x16x32_bf16 v[90:93], v[144:147], v[214:217], v[90:93]
	v_mfma_f32_16x16x32_bf16 v[86:89], v[174:177], v[214:217], v[86:89]
	v_mfma_f32_16x16x32_bf16 v[74:77], v[144:147], v[224:227], v[74:77]
	v_mfma_f32_16x16x32_bf16 v[70:73], v[174:177], v[224:227], v[70:73]
	v_mfma_f32_16x16x32_bf16 v[122:125], v[148:151], v[202:205], v[122:125]
	v_mfma_f32_16x16x32_bf16 v[118:121], v[178:181], v[202:205], v[118:121]
	v_mfma_f32_16x16x32_bf16 v[106:109], v[148:151], v[210:213], v[106:109]
	v_mfma_f32_16x16x32_bf16 v[102:105], v[178:181], v[210:213], v[102:105]
	v_mfma_f32_16x16x32_bf16 v[90:93], v[148:151], v[220:223], v[90:93]
	v_mfma_f32_16x16x32_bf16 v[86:89], v[178:181], v[220:223], v[86:89]
	v_mfma_f32_16x16x32_bf16 v[74:77], v[148:151], v[228:231], v[74:77]
	v_mfma_f32_16x16x32_bf16 v[70:73], v[178:181], v[228:231], v[70:73]
	v_mfma_f32_16x16x32_bf16 v[126:129], v[182:185], v[198:201], v[126:129]
	v_mfma_f32_16x16x32_bf16 v[114:117], v[190:193], v[198:201], v[114:117]
	v_mfma_f32_16x16x32_bf16 v[110:113], v[182:185], v[206:209], v[110:113]
	v_mfma_f32_16x16x32_bf16 v[98:101], v[190:193], v[206:209], v[98:101]
	v_mfma_f32_16x16x32_bf16 v[94:97], v[182:185], v[214:217], v[94:97]
	v_mfma_f32_16x16x32_bf16 v[82:85], v[190:193], v[214:217], v[82:85]
	v_mfma_f32_16x16x32_bf16 v[78:81], v[182:185], v[224:227], v[78:81]
	v_mfma_f32_16x16x32_bf16 v[66:69], v[190:193], v[224:227], v[66:69]
	v_mfma_f32_16x16x32_bf16 v[126:129], v[186:189], v[202:205], v[126:129]
	v_mfma_f32_16x16x32_bf16 v[114:117], v[194:197], v[202:205], v[114:117]
	v_mfma_f32_16x16x32_bf16 v[110:113], v[186:189], v[210:213], v[110:113]
	v_mfma_f32_16x16x32_bf16 v[98:101], v[194:197], v[210:213], v[98:101]
	v_mfma_f32_16x16x32_bf16 v[94:97], v[186:189], v[220:223], v[94:97]
	v_mfma_f32_16x16x32_bf16 v[82:85], v[194:197], v[220:223], v[82:85]
	v_mfma_f32_16x16x32_bf16 v[78:81], v[186:189], v[228:231], v[78:81]
	v_mfma_f32_16x16x32_bf16 v[66:69], v[194:197], v[228:231], v[66:69]
	s_barrier
	v_lshl_add_u64 v[152:153], s[26:27], 0, v[162:163]
	s_add_i32 s26, s94, s86
	s_mov_b32 m0, s26
	ds_read_b128 v[198:201], v172 offset:16384
	ds_read_b128 v[202:205], v172 offset:17408
	ds_read_b128 v[206:209], v172 offset:18432
	ds_read_b128 v[210:213], v172 offset:19456
	ds_read_b128 v[214:217], v172 offset:20480
	ds_read_b128 v[220:223], v172 offset:21504
	ds_read_b128 v[224:227], v172 offset:22528
	ds_read_b128 v[228:231], v172 offset:23552
	global_load_lds_dwordx4 v[152:153], off
	v_lshl_add_u64 v[232:233], v[152:153], 0, s[10:11]
	s_add_i32 m0, s26, 0x2000
	s_add_i32 s26, s95, s86
	global_load_lds_dwordx4 v[232:233], off
	v_lshl_add_u64 v[232:233], v[152:153], 0, s[12:13]
	s_mov_b32 m0, s26
	v_lshl_add_u64 v[234:235], s[82:83], 0, v[132:133]
	global_load_lds_dwordx4 v[232:233], off
	v_lshl_add_u64 v[232:233], v[152:153], 0, s[14:15]
	s_add_i32 m0, s26, 0x2000
	s_nop 0
	global_load_lds_dwordx4 v[232:233], off
	v_lshl_add_u64 v[232:233], s[82:83], 0, v[130:131]
	s_mov_b32 m0, s87
	s_nop 0
	global_load_lds_dwordx4 v[232:233], off
	s_mov_b32 m0, s88
	s_nop 0
	global_load_lds_dwordx4 v[234:235], off
	s_waitcnt vmcnt(8) lgkmcnt(0)
	s_barrier
	v_mfma_f32_16x16x32_bf16 v[58:61], v[144:147], v[198:201], v[58:61]
	v_mfma_f32_16x16x32_bf16 v[54:57], v[174:177], v[198:201], v[54:57]
	v_mfma_f32_16x16x32_bf16 v[42:45], v[144:147], v[206:209], v[42:45]
	v_mfma_f32_16x16x32_bf16 v[38:41], v[174:177], v[206:209], v[38:41]
	v_mfma_f32_16x16x32_bf16 v[26:29], v[144:147], v[214:217], v[26:29]
	v_mfma_f32_16x16x32_bf16 v[22:25], v[174:177], v[214:217], v[22:25]
	v_mfma_f32_16x16x32_bf16 v[10:13], v[144:147], v[224:227], v[10:13]
	v_mfma_f32_16x16x32_bf16 v[6:9], v[174:177], v[224:227], v[6:9]
	v_mfma_f32_16x16x32_bf16 v[58:61], v[148:151], v[202:205], v[58:61]
	v_mfma_f32_16x16x32_bf16 v[54:57], v[178:181], v[202:205], v[54:57]
	v_mfma_f32_16x16x32_bf16 v[42:45], v[148:151], v[210:213], v[42:45]
	v_mfma_f32_16x16x32_bf16 v[38:41], v[178:181], v[210:213], v[38:41]
	v_mfma_f32_16x16x32_bf16 v[26:29], v[148:151], v[220:223], v[26:29]
	v_mfma_f32_16x16x32_bf16 v[22:25], v[178:181], v[220:223], v[22:25]
	v_mfma_f32_16x16x32_bf16 v[10:13], v[148:151], v[228:231], v[10:13]
	v_mfma_f32_16x16x32_bf16 v[6:9], v[178:181], v[228:231], v[6:9]
	v_mfma_f32_16x16x32_bf16 v[62:65], v[182:185], v[198:201], v[62:65]
	v_mfma_f32_16x16x32_bf16 v[50:53], v[190:193], v[198:201], v[50:53]
	v_mfma_f32_16x16x32_bf16 v[46:49], v[182:185], v[206:209], v[46:49]
	v_mfma_f32_16x16x32_bf16 v[34:37], v[190:193], v[206:209], v[34:37]
	v_mfma_f32_16x16x32_bf16 v[30:33], v[182:185], v[214:217], v[30:33]
	v_mfma_f32_16x16x32_bf16 v[18:21], v[190:193], v[214:217], v[18:21]
	v_mfma_f32_16x16x32_bf16 v[14:17], v[182:185], v[224:227], v[14:17]
	v_mfma_f32_16x16x32_bf16 v[2:5], v[190:193], v[224:227], v[2:5]
	v_mfma_f32_16x16x32_bf16 v[62:65], v[186:189], v[202:205], v[62:65]
	v_mfma_f32_16x16x32_bf16 v[50:53], v[194:197], v[202:205], v[50:53]
	v_mfma_f32_16x16x32_bf16 v[46:49], v[186:189], v[210:213], v[46:49]
	v_mfma_f32_16x16x32_bf16 v[34:37], v[194:197], v[210:213], v[34:37]
	v_mfma_f32_16x16x32_bf16 v[30:33], v[186:189], v[220:223], v[30:33]
	v_mfma_f32_16x16x32_bf16 v[18:21], v[194:197], v[220:223], v[18:21]
	v_mfma_f32_16x16x32_bf16 v[14:17], v[186:189], v[228:231], v[14:17]
	v_mfma_f32_16x16x32_bf16 v[2:5], v[194:197], v[228:231], v[2:5]
	s_barrier
	s_add_i32 s33, 0, 0x18000
	v_add_u32_e32 v136, s33, v167
	s_add_i32 s8, 0, 0x1c000
	ds_read_b128 v[144:147], v136
	ds_read_b128 v[148:151], v136 offset:1024
	ds_read_b128 v[174:177], v136 offset:2048
	ds_read_b128 v[178:181], v136 offset:3072
	v_add_u32_e32 v136, s8, v167
	ds_read_b128 v[182:185], v136
	ds_read_b128 v[186:189], v136 offset:1024
	ds_read_b128 v[190:193], v136 offset:2048
	ds_read_b128 v[194:197], v136 offset:3072
	s_add_u32 s26, s82, 0x80000
	s_addc_u32 s27, s83, 0
	s_mov_b32 m0, s89
	v_lshl_add_u64 v[236:237], s[26:27], 0, v[130:131]
	ds_read_b128 v[198:201], v172 offset:32768
	ds_read_b128 v[202:205], v172 offset:33792
	ds_read_b128 v[206:209], v172 offset:34816
	ds_read_b128 v[210:213], v172 offset:35840
	ds_read_b128 v[214:217], v172 offset:36864
	ds_read_b128 v[220:223], v172 offset:37888
	ds_read_b128 v[224:227], v172 offset:38912
	ds_read_b128 v[228:231], v172 offset:39936
	global_load_lds_dwordx4 v[236:237], off
	v_lshl_add_u64 v[236:237], s[26:27], 0, v[132:133]
	s_mov_b32 m0, s90
	s_nop 0
	global_load_lds_dwordx4 v[236:237], off
	s_waitcnt vmcnt(8) lgkmcnt(0)
	s_barrier
	v_mfma_f32_16x16x32_bf16 v[122:125], v[144:147], v[198:201], v[122:125]
	v_mfma_f32_16x16x32_bf16 v[118:121], v[174:177], v[198:201], v[118:121]
	v_mfma_f32_16x16x32_bf16 v[106:109], v[144:147], v[206:209], v[106:109]
	v_mfma_f32_16x16x32_bf16 v[102:105], v[174:177], v[206:209], v[102:105]
	v_mfma_f32_16x16x32_bf16 v[90:93], v[144:147], v[214:217], v[90:93]
	v_mfma_f32_16x16x32_bf16 v[86:89], v[174:177], v[214:217], v[86:89]
	v_mfma_f32_16x16x32_bf16 v[74:77], v[144:147], v[224:227], v[74:77]
	v_mfma_f32_16x16x32_bf16 v[70:73], v[174:177], v[224:227], v[70:73]
	v_mfma_f32_16x16x32_bf16 v[122:125], v[148:151], v[202:205], v[122:125]
	v_mfma_f32_16x16x32_bf16 v[118:121], v[178:181], v[202:205], v[118:121]
	v_mfma_f32_16x16x32_bf16 v[106:109], v[148:151], v[210:213], v[106:109]
	v_mfma_f32_16x16x32_bf16 v[102:105], v[178:181], v[210:213], v[102:105]
	v_mfma_f32_16x16x32_bf16 v[90:93], v[148:151], v[220:223], v[90:93]
	v_mfma_f32_16x16x32_bf16 v[86:89], v[178:181], v[220:223], v[86:89]
	v_mfma_f32_16x16x32_bf16 v[74:77], v[148:151], v[228:231], v[74:77]
	v_mfma_f32_16x16x32_bf16 v[70:73], v[178:181], v[228:231], v[70:73]
	v_mfma_f32_16x16x32_bf16 v[126:129], v[182:185], v[198:201], v[126:129]
	v_mfma_f32_16x16x32_bf16 v[114:117], v[190:193], v[198:201], v[114:117]
	v_mfma_f32_16x16x32_bf16 v[110:113], v[182:185], v[206:209], v[110:113]
	v_mfma_f32_16x16x32_bf16 v[98:101], v[190:193], v[206:209], v[98:101]
	v_mfma_f32_16x16x32_bf16 v[94:97], v[182:185], v[214:217], v[94:97]
	v_mfma_f32_16x16x32_bf16 v[82:85], v[190:193], v[214:217], v[82:85]
	v_mfma_f32_16x16x32_bf16 v[78:81], v[182:185], v[224:227], v[78:81]
	v_mfma_f32_16x16x32_bf16 v[66:69], v[190:193], v[224:227], v[66:69]
	v_mfma_f32_16x16x32_bf16 v[126:129], v[186:189], v[202:205], v[126:129]
	v_mfma_f32_16x16x32_bf16 v[114:117], v[194:197], v[202:205], v[114:117]
	v_mfma_f32_16x16x32_bf16 v[110:113], v[186:189], v[210:213], v[110:113]
	v_mfma_f32_16x16x32_bf16 v[98:101], v[194:197], v[210:213], v[98:101]
	v_mfma_f32_16x16x32_bf16 v[94:97], v[186:189], v[220:223], v[94:97]
	v_mfma_f32_16x16x32_bf16 v[82:85], v[194:197], v[220:223], v[82:85]
	v_mfma_f32_16x16x32_bf16 v[78:81], v[186:189], v[228:231], v[78:81]
	v_mfma_f32_16x16x32_bf16 v[66:69], v[194:197], v[228:231], v[66:69]
	s_barrier
	s_add_i32 s9, s33, s86
	v_lshl_add_u64 v[236:237], v[152:153], 0, s[20:21]
	s_mov_b32 m0, s9
	ds_read_b128 v[198:201], v172 offset:49152
	ds_read_b128 v[202:205], v172 offset:50176
	ds_read_b128 v[206:209], v172 offset:51200
	ds_read_b128 v[210:213], v172 offset:52224
	ds_read_b128 v[214:217], v172 offset:53248
	ds_read_b128 v[220:223], v172 offset:54272
	ds_read_b128 v[224:227], v172 offset:55296
	ds_read_b128 v[228:231], v172 offset:56320
	global_load_lds_dwordx4 v[236:237], off
	v_lshl_add_u64 v[236:237], v[152:153], 0, s[22:23]
	s_add_i32 m0, s9, 0x2000
	s_add_i32 s8, s8, s86
	global_load_lds_dwordx4 v[236:237], off
	v_lshl_add_u64 v[236:237], v[152:153], 0, s[40:41]
	s_mov_b32 m0, s8
	v_lshl_add_u64 v[152:153], v[152:153], 0, s[44:45]
	global_load_lds_dwordx4 v[236:237], off
	s_add_i32 m0, s8, 0x2000
	s_nop 0
	global_load_lds_dwordx4 v[152:153], off
	v_lshl_add_u64 v[152:153], v[232:233], 0, s[24:25]
	s_mov_b32 m0, s91
	s_nop 0
	global_load_lds_dwordx4 v[152:153], off
	v_lshl_add_u64 v[152:153], v[234:235], 0, s[24:25]
	s_mov_b32 m0, s92
	s_nop 0
	global_load_lds_dwordx4 v[152:153], off
	s_waitcnt vmcnt(8) lgkmcnt(0)
	s_barrier
	v_mfma_f32_16x16x32_bf16 v[58:61], v[144:147], v[198:201], v[58:61]
	v_mfma_f32_16x16x32_bf16 v[54:57], v[174:177], v[198:201], v[54:57]
	v_mfma_f32_16x16x32_bf16 v[42:45], v[144:147], v[206:209], v[42:45]
	v_mfma_f32_16x16x32_bf16 v[38:41], v[174:177], v[206:209], v[38:41]
	v_mfma_f32_16x16x32_bf16 v[26:29], v[144:147], v[214:217], v[26:29]
	v_mfma_f32_16x16x32_bf16 v[22:25], v[174:177], v[214:217], v[22:25]
	v_mfma_f32_16x16x32_bf16 v[10:13], v[144:147], v[224:227], v[10:13]
	v_mfma_f32_16x16x32_bf16 v[6:9], v[174:177], v[224:227], v[6:9]
	v_mfma_f32_16x16x32_bf16 v[58:61], v[148:151], v[202:205], v[58:61]
	v_mfma_f32_16x16x32_bf16 v[54:57], v[178:181], v[202:205], v[54:57]
	v_mfma_f32_16x16x32_bf16 v[42:45], v[148:151], v[210:213], v[42:45]
	v_mfma_f32_16x16x32_bf16 v[38:41], v[178:181], v[210:213], v[38:41]
	v_mfma_f32_16x16x32_bf16 v[26:29], v[148:151], v[220:223], v[26:29]
	v_mfma_f32_16x16x32_bf16 v[22:25], v[178:181], v[220:223], v[22:25]
	v_mfma_f32_16x16x32_bf16 v[10:13], v[148:151], v[228:231], v[10:13]
	v_mfma_f32_16x16x32_bf16 v[6:9], v[178:181], v[228:231], v[6:9]
	v_mfma_f32_16x16x32_bf16 v[62:65], v[182:185], v[198:201], v[62:65]
	v_mfma_f32_16x16x32_bf16 v[50:53], v[190:193], v[198:201], v[50:53]
	v_mfma_f32_16x16x32_bf16 v[46:49], v[182:185], v[206:209], v[46:49]
	v_mfma_f32_16x16x32_bf16 v[34:37], v[190:193], v[206:209], v[34:37]
	v_mfma_f32_16x16x32_bf16 v[30:33], v[182:185], v[214:217], v[30:33]
	v_mfma_f32_16x16x32_bf16 v[18:21], v[190:193], v[214:217], v[18:21]
	v_mfma_f32_16x16x32_bf16 v[14:17], v[182:185], v[224:227], v[14:17]
	v_mfma_f32_16x16x32_bf16 v[2:5], v[190:193], v[224:227], v[2:5]
	v_mfma_f32_16x16x32_bf16 v[62:65], v[186:189], v[202:205], v[62:65]
	v_mfma_f32_16x16x32_bf16 v[50:53], v[194:197], v[202:205], v[50:53]
	v_mfma_f32_16x16x32_bf16 v[46:49], v[186:189], v[210:213], v[46:49]
	v_mfma_f32_16x16x32_bf16 v[34:37], v[194:197], v[210:213], v[34:37]
	v_mfma_f32_16x16x32_bf16 v[30:33], v[186:189], v[220:223], v[30:33]
	v_mfma_f32_16x16x32_bf16 v[18:21], v[194:197], v[220:223], v[18:21]
	v_mfma_f32_16x16x32_bf16 v[14:17], v[186:189], v[228:231], v[14:17]
	v_mfma_f32_16x16x32_bf16 v[2:5], v[194:197], v[228:231], v[2:5]
	s_barrier
	s_add_i32 vcc_hi, vcc_hi, 2
	s_add_u32 s97, s97, 0x10000
	s_addc_u32 vcc_lo, vcc_lo, 0
	s_add_u32 s80, s80, 0x100
	s_addc_u32 s81, s81, 0
	s_cmp_gt_u32 vcc_hi, 29
	s_cbranch_scc0 .LBB0_261
	s_and_b64 vcc, exec, s[50:51]
	s_cbranch_vccz .LBB0_264
	s_barrier

.LBB0_284:
	s_ashr_i32 s51, s50, 31
	s_lshl_b64 s[26:27], s[50:51], 19
	v_readlane_b32 s54, v254, 58
	v_readlane_b32 s55, v254, 59
	s_add_u32 s54, s54, s26
	s_addc_u32 s55, s55, s27
	s_and_b64 s[26:27], s[0:1], exec
	s_cselect_b32 s51, s55, s73
	s_cselect_b32 s90, s54, s72
	s_ashr_i32 s45, s44, 31
	s_lshl_b64 s[26:27], s[44:45], 19
	s_add_u32 s56, s81, s26
	s_addc_u32 s57, s82, s27
	s_and_b64 s[26:27], s[0:1], exec
	s_cselect_b32 s45, s57, s71
	s_cselect_b32 s91, s56, s70
	s_add_u32 s92, s70, 0x10000
	s_addc_u32 s93, s71, 0
	s_add_u32 s70, s72, 0x40080
	s_addc_u32 s71, s73, 0
	s_mov_b32 s94, -2
	ds_read_b128 v[26:29], v1
	ds_read_b128 v[30:33], v1 offset:1024
	ds_read_b128 v[18:21], v1 offset:2048
	ds_read_b128 v[22:25], v1 offset:3072
	ds_read_b128 v[10:13], v185
	ds_read_b128 v[14:17], v185 offset:1024
	ds_read_b128 v[2:5], v185 offset:2048
	ds_read_b128 v[6:9], v185 offset:3072
	s_add_u32 s26, s70, 0xfffc0080
	s_addc_u32 s27, s71, -1
	s_cmp_eq_u32 s94, 12
	s_cselect_b32 s73, s51, s27
	s_cselect_b32 s72, s90, s26
	s_cselect_b32 s75, s45, s93
	s_cselect_b32 s74, s91, s92
	v_lshl_add_u64 v[176:177], s[70:71], 0, v[168:169]
	s_add_i32 m0, s33, 0xc000
	ds_read_b128 v[190:193], v186
	ds_read_b128 v[194:197], v186 offset:1024
	ds_read_b128 v[198:201], v186 offset:2048
	ds_read_b128 v[202:205], v186 offset:3072
	ds_read_b128 v[206:209], v186 offset:4096
	ds_read_b128 v[210:213], v186 offset:5120
	ds_read_b128 v[220:223], v186 offset:6144
	ds_read_b128 v[224:227], v186 offset:7168
	global_load_lds_dwordx4 v[176:177], off
	v_lshl_add_u64 v[176:177], s[70:71], 0, v[170:171]
	s_add_i32 m0, s33, 0xe000
	s_nop 0
	global_load_lds_dwordx4 v[176:177], off
	s_waitcnt vmcnt(24) lgkmcnt(0)
	s_barrier
	v_mfma_scale_f32_16x16x128_f8f6f4 v[158:161], v[26:33], v[190:197], 0, v187, v188 op_sel_hi:[0,0,0]
	v_mfma_scale_f32_16x16x128_f8f6f4 v[154:157], v[18:25], v[190:197], 0, v187, v188 op_sel_hi:[0,0,0]
	v_mfma_scale_f32_16x16x128_f8f6f4 v[150:153], v[26:33], v[198:205], 0, v187, v188 op_sel_hi:[0,0,0]
	v_mfma_scale_f32_16x16x128_f8f6f4 v[142:145], v[18:25], v[198:205], 0, v187, v188 op_sel_hi:[0,0,0]
	v_mfma_scale_f32_16x16x128_f8f6f4 v[134:137], v[26:33], v[206:213], 0, v187, v188 op_sel_hi:[0,0,0]
	v_mfma_scale_f32_16x16x128_f8f6f4 v[126:129], v[18:25], v[206:213], 0, v187, v188 op_sel_hi:[0,0,0]
	v_mfma_scale_f32_16x16x128_f8f6f4 v[118:121], v[26:33], v[220:227], 0, v187, v188 op_sel_hi:[0,0,0]
	v_mfma_scale_f32_16x16x128_f8f6f4 v[110:113], v[18:25], v[220:227], 0, v187, v188 op_sel_hi:[0,0,0]
	v_mfma_scale_f32_16x16x128_f8f6f4 v[146:149], v[10:17], v[190:197], 0, v187, v188 op_sel_hi:[0,0,0]
	v_mfma_scale_f32_16x16x128_f8f6f4 v[138:141], v[2:9], v[190:197], 0, v187, v188 op_sel_hi:[0,0,0]
	v_mfma_scale_f32_16x16x128_f8f6f4 v[130:133], v[10:17], v[198:205], 0, v187, v188 op_sel_hi:[0,0,0]
	v_mfma_scale_f32_16x16x128_f8f6f4 v[122:125], v[2:9], v[198:205], 0, v187, v188 op_sel_hi:[0,0,0]
	v_mfma_scale_f32_16x16x128_f8f6f4 v[114:117], v[10:17], v[206:213], 0, v187, v188 op_sel_hi:[0,0,0]
	v_mfma_scale_f32_16x16x128_f8f6f4 v[106:109], v[2:9], v[206:213], 0, v187, v188 op_sel_hi:[0,0,0]
	v_mfma_scale_f32_16x16x128_f8f6f4 v[102:105], v[10:17], v[220:227], 0, v187, v188 op_sel_hi:[0,0,0]
	v_mfma_scale_f32_16x16x128_f8f6f4 v[98:101], v[2:9], v[220:227], 0, v187, v188 op_sel_hi:[0,0,0]
	s_barrier
	s_add_i32 s26, s88, s80
	v_lshl_add_u64 v[176:177], s[74:75], 0, v[162:163]
	s_mov_b32 m0, s26
	ds_read_b128 v[190:193], v186 offset:16384
	ds_read_b128 v[194:197], v186 offset:17408
	ds_read_b128 v[198:201], v186 offset:18432
	ds_read_b128 v[202:205], v186 offset:19456
	ds_read_b128 v[206:209], v186 offset:20480
	ds_read_b128 v[210:213], v186 offset:21504
	ds_read_b128 v[220:223], v186 offset:22528
	ds_read_b128 v[224:227], v186 offset:23552
	global_load_lds_dwordx4 v[176:177], off
	v_lshl_add_u64 v[178:179], v[176:177], 0, s[8:9]
	s_add_i32 m0, s26, 0x2000
	s_add_i32 s26, s89, s80
	global_load_lds_dwordx4 v[178:179], off
	v_lshl_add_u64 v[178:179], v[176:177], 0, s[10:11]
	s_mov_b32 m0, s26
	v_lshl_add_u64 v[180:181], s[72:73], 0, v[166:167]
	global_load_lds_dwordx4 v[178:179], off
	v_lshl_add_u64 v[178:179], v[176:177], 0, s[12:13]
	s_add_i32 m0, s26, 0x2000
	s_nop 0
	global_load_lds_dwordx4 v[178:179], off
	v_lshl_add_u64 v[178:179], s[72:73], 0, v[164:165]
	s_mov_b32 m0, s33
	s_nop 0
	global_load_lds_dwordx4 v[178:179], off
	s_mov_b32 m0, s69
	s_nop 0
	global_load_lds_dwordx4 v[180:181], off
	s_waitcnt vmcnt(24) lgkmcnt(0)
	s_barrier
	v_mfma_scale_f32_16x16x128_f8f6f4 v[94:97], v[26:33], v[190:197], 0, v187, v188 op_sel_hi:[0,0,0]
	v_mfma_scale_f32_16x16x128_f8f6f4 v[90:93], v[18:25], v[190:197], 0, v187, v188 op_sel_hi:[0,0,0]
	v_mfma_scale_f32_16x16x128_f8f6f4 v[86:89], v[26:33], v[198:205], 0, v187, v188 op_sel_hi:[0,0,0]
	v_mfma_scale_f32_16x16x128_f8f6f4 v[78:81], v[18:25], v[198:205], 0, v187, v188 op_sel_hi:[0,0,0]
	v_mfma_scale_f32_16x16x128_f8f6f4 v[70:73], v[26:33], v[206:213], 0, v187, v188 op_sel_hi:[0,0,0]
	v_mfma_scale_f32_16x16x128_f8f6f4 v[62:65], v[18:25], v[206:213], 0, v187, v188 op_sel_hi:[0,0,0]
	v_mfma_scale_f32_16x16x128_f8f6f4 v[54:57], v[26:33], v[220:227], 0, v187, v188 op_sel_hi:[0,0,0]
	v_mfma_scale_f32_16x16x128_f8f6f4 v[46:49], v[18:25], v[220:227], 0, v187, v188 op_sel_hi:[0,0,0]
	v_mfma_scale_f32_16x16x128_f8f6f4 v[82:85], v[10:17], v[190:197], 0, v187, v188 op_sel_hi:[0,0,0]
	v_mfma_scale_f32_16x16x128_f8f6f4 v[74:77], v[2:9], v[190:197], 0, v187, v188 op_sel_hi:[0,0,0]
	v_mfma_scale_f32_16x16x128_f8f6f4 v[66:69], v[10:17], v[198:205], 0, v187, v188 op_sel_hi:[0,0,0]
	v_mfma_scale_f32_16x16x128_f8f6f4 v[58:61], v[2:9], v[198:205], 0, v187, v188 op_sel_hi:[0,0,0]
	v_mfma_scale_f32_16x16x128_f8f6f4 v[50:53], v[10:17], v[206:213], 0, v187, v188 op_sel_hi:[0,0,0]
	v_mfma_scale_f32_16x16x128_f8f6f4 v[42:45], v[2:9], v[206:213], 0, v187, v188 op_sel_hi:[0,0,0]
	v_mfma_scale_f32_16x16x128_f8f6f4 v[38:41], v[10:17], v[220:227], 0, v187, v188 op_sel_hi:[0,0,0]
	v_mfma_scale_f32_16x16x128_f8f6f4 v[34:37], v[2:9], v[220:227], 0, v187, v188 op_sel_hi:[0,0,0]
	s_barrier
	s_add_i32 s74, 0, 0x18000
	s_add_i32 s75, 0, 0x1c000
	v_add_u32_e32 v14, s74, v183
	v_add_u32_e32 v30, s75, v183
	ds_read_b128 v[2:5], v14
	ds_read_b128 v[6:9], v14 offset:1024
	ds_read_b128 v[10:13], v14 offset:2048
	ds_read_b128 v[14:17], v14 offset:3072
	ds_read_b128 v[18:21], v30
	ds_read_b128 v[22:25], v30 offset:1024
	ds_read_b128 v[26:29], v30 offset:2048
	ds_read_b128 v[30:33], v30 offset:3072
	s_add_u32 s26, s72, 0x40000
	s_addc_u32 s27, s73, 0
	s_mov_b32 m0, s83
	v_lshl_add_u64 v[214:215], s[26:27], 0, v[164:165]
	ds_read_b128 v[190:193], v186 offset:32768
	ds_read_b128 v[194:197], v186 offset:33792
	ds_read_b128 v[198:201], v186 offset:34816
	ds_read_b128 v[202:205], v186 offset:35840
	ds_read_b128 v[206:209], v186 offset:36864
	ds_read_b128 v[210:213], v186 offset:37888
	ds_read_b128 v[220:223], v186 offset:38912
	ds_read_b128 v[224:227], v186 offset:39936
	global_load_lds_dwordx4 v[214:215], off
	v_lshl_add_u64 v[214:215], s[26:27], 0, v[166:167]
	s_mov_b32 m0, s84
	s_nop 0
	global_load_lds_dwordx4 v[214:215], off
	s_waitcnt vmcnt(8) lgkmcnt(0)
	s_barrier
	v_mfma_scale_f32_16x16x128_f8f6f4 v[158:161], v[2:9], v[190:197], v[158:161], v187, v188 op_sel_hi:[0,0,0]
	v_mfma_scale_f32_16x16x128_f8f6f4 v[154:157], v[10:17], v[190:197], v[154:157], v187, v188 op_sel_hi:[0,0,0]
	v_mfma_scale_f32_16x16x128_f8f6f4 v[150:153], v[2:9], v[198:205], v[150:153], v187, v188 op_sel_hi:[0,0,0]
	v_mfma_scale_f32_16x16x128_f8f6f4 v[142:145], v[10:17], v[198:205], v[142:145], v187, v188 op_sel_hi:[0,0,0]
	v_mfma_scale_f32_16x16x128_f8f6f4 v[134:137], v[2:9], v[206:213], v[134:137], v187, v188 op_sel_hi:[0,0,0]
	v_mfma_scale_f32_16x16x128_f8f6f4 v[126:129], v[10:17], v[206:213], v[126:129], v187, v188 op_sel_hi:[0,0,0]
	v_mfma_scale_f32_16x16x128_f8f6f4 v[118:121], v[2:9], v[220:227], v[118:121], v187, v188 op_sel_hi:[0,0,0]
	v_mfma_scale_f32_16x16x128_f8f6f4 v[110:113], v[10:17], v[220:227], v[110:113], v187, v188 op_sel_hi:[0,0,0]
	v_mfma_scale_f32_16x16x128_f8f6f4 v[146:149], v[18:25], v[190:197], v[146:149], v187, v188 op_sel_hi:[0,0,0]
	v_mfma_scale_f32_16x16x128_f8f6f4 v[138:141], v[26:33], v[190:197], v[138:141], v187, v188 op_sel_hi:[0,0,0]
	v_mfma_scale_f32_16x16x128_f8f6f4 v[130:133], v[18:25], v[198:205], v[130:133], v187, v188 op_sel_hi:[0,0,0]
	v_mfma_scale_f32_16x16x128_f8f6f4 v[122:125], v[26:33], v[198:205], v[122:125], v187, v188 op_sel_hi:[0,0,0]
	v_mfma_scale_f32_16x16x128_f8f6f4 v[114:117], v[18:25], v[206:213], v[114:117], v187, v188 op_sel_hi:[0,0,0]
	v_mfma_scale_f32_16x16x128_f8f6f4 v[106:109], v[26:33], v[206:213], v[106:109], v187, v188 op_sel_hi:[0,0,0]
	v_mfma_scale_f32_16x16x128_f8f6f4 v[102:105], v[18:25], v[220:227], v[102:105], v187, v188 op_sel_hi:[0,0,0]
	v_mfma_scale_f32_16x16x128_f8f6f4 v[98:101], v[26:33], v[220:227], v[98:101], v187, v188 op_sel_hi:[0,0,0]
	s_barrier
	s_add_i32 s26, s74, s80
	v_lshl_add_u64 v[214:215], v[176:177], 0, s[16:17]
	s_mov_b32 m0, s26
	ds_read_b128 v[190:193], v186 offset:49152
	ds_read_b128 v[194:197], v186 offset:50176
	ds_read_b128 v[198:201], v186 offset:51200
	ds_read_b128 v[202:205], v186 offset:52224
	ds_read_b128 v[206:209], v186 offset:53248
	ds_read_b128 v[210:213], v186 offset:54272
	ds_read_b128 v[220:223], v186 offset:55296
	ds_read_b128 v[224:227], v186 offset:56320
	global_load_lds_dwordx4 v[214:215], off
	v_lshl_add_u64 v[214:215], v[176:177], 0, s[18:19]
	s_add_i32 m0, s26, 0x2000
	s_add_i32 s26, s75, s80
	global_load_lds_dwordx4 v[214:215], off
	v_lshl_add_u64 v[214:215], v[176:177], 0, s[22:23]
	s_mov_b32 m0, s26
	v_lshl_add_u64 v[176:177], v[176:177], 0, s[24:25]
	global_load_lds_dwordx4 v[214:215], off
	s_add_i32 m0, s26, 0x2000
	s_nop 0
	global_load_lds_dwordx4 v[176:177], off
	v_lshl_add_u64 v[176:177], v[178:179], 0, s[20:21]
	s_mov_b32 m0, s86
	s_nop 0
	global_load_lds_dwordx4 v[176:177], off
	v_lshl_add_u64 v[176:177], v[180:181], 0, s[20:21]
	s_mov_b32 m0, s87
	s_nop 0
	global_load_lds_dwordx4 v[176:177], off
	s_waitcnt vmcnt(8) lgkmcnt(0)
	s_barrier
	v_mfma_scale_f32_16x16x128_f8f6f4 v[94:97], v[2:9], v[190:197], v[94:97], v187, v188 op_sel_hi:[0,0,0]
	v_mfma_scale_f32_16x16x128_f8f6f4 v[90:93], v[10:17], v[190:197], v[90:93], v187, v188 op_sel_hi:[0,0,0]
	v_mfma_scale_f32_16x16x128_f8f6f4 v[86:89], v[2:9], v[198:205], v[86:89], v187, v188 op_sel_hi:[0,0,0]
	v_mfma_scale_f32_16x16x128_f8f6f4 v[78:81], v[10:17], v[198:205], v[78:81], v187, v188 op_sel_hi:[0,0,0]
	v_mfma_scale_f32_16x16x128_f8f6f4 v[70:73], v[2:9], v[206:213], v[70:73], v187, v188 op_sel_hi:[0,0,0]
	v_mfma_scale_f32_16x16x128_f8f6f4 v[62:65], v[10:17], v[206:213], v[62:65], v187, v188 op_sel_hi:[0,0,0]
	v_mfma_scale_f32_16x16x128_f8f6f4 v[54:57], v[2:9], v[220:227], v[54:57], v187, v188 op_sel_hi:[0,0,0]
	v_mfma_scale_f32_16x16x128_f8f6f4 v[46:49], v[10:17], v[220:227], v[46:49], v187, v188 op_sel_hi:[0,0,0]
	v_mfma_scale_f32_16x16x128_f8f6f4 v[82:85], v[18:25], v[190:197], v[82:85], v187, v188 op_sel_hi:[0,0,0]
	v_mfma_scale_f32_16x16x128_f8f6f4 v[74:77], v[26:33], v[190:197], v[74:77], v187, v188 op_sel_hi:[0,0,0]
	v_mfma_scale_f32_16x16x128_f8f6f4 v[66:69], v[18:25], v[198:205], v[66:69], v187, v188 op_sel_hi:[0,0,0]
	v_mfma_scale_f32_16x16x128_f8f6f4 v[58:61], v[26:33], v[198:205], v[58:61], v187, v188 op_sel_hi:[0,0,0]
	v_mfma_scale_f32_16x16x128_f8f6f4 v[50:53], v[18:25], v[206:213], v[50:53], v187, v188 op_sel_hi:[0,0,0]
	v_mfma_scale_f32_16x16x128_f8f6f4 v[42:45], v[26:33], v[206:213], v[42:45], v187, v188 op_sel_hi:[0,0,0]
	v_mfma_scale_f32_16x16x128_f8f6f4 v[38:41], v[18:25], v[220:227], v[38:41], v187, v188 op_sel_hi:[0,0,0]
	v_mfma_scale_f32_16x16x128_f8f6f4 v[34:37], v[26:33], v[220:227], v[34:37], v187, v188 op_sel_hi:[0,0,0]
	s_barrier
	s_add_i32 s94, s94, 2
	s_add_u32 s92, s92, 0x10000
	s_addc_u32 s93, s93, 0
	s_add_u32 s70, s70, 0x100
	s_addc_u32 s71, s71, 0
	s_cmp_gt_u32 s94, 13
.LBB0_285:
	ds_read_b128 v[26:29], v1
	ds_read_b128 v[30:33], v1 offset:1024
	ds_read_b128 v[18:21], v1 offset:2048
	ds_read_b128 v[22:25], v1 offset:3072
	ds_read_b128 v[10:13], v185
	ds_read_b128 v[14:17], v185 offset:1024
	ds_read_b128 v[2:5], v185 offset:2048
	ds_read_b128 v[6:9], v185 offset:3072
	s_add_u32 s26, s70, 0xfffc0080
	s_addc_u32 s27, s71, -1
	s_cmp_eq_u32 s94, 12
	s_cselect_b32 s73, s51, s27
	s_cselect_b32 s72, s90, s26
	s_cselect_b32 s75, s45, s93
	s_cselect_b32 s74, s91, s92
	v_lshl_add_u64 v[176:177], s[70:71], 0, v[168:169]
	s_add_i32 m0, s33, 0xc000
	ds_read_b128 v[190:193], v186
	ds_read_b128 v[194:197], v186 offset:1024
	ds_read_b128 v[198:201], v186 offset:2048
	ds_read_b128 v[202:205], v186 offset:3072
	ds_read_b128 v[206:209], v186 offset:4096
	ds_read_b128 v[210:213], v186 offset:5120
	ds_read_b128 v[220:223], v186 offset:6144
	ds_read_b128 v[224:227], v186 offset:7168
	global_load_lds_dwordx4 v[176:177], off
	v_lshl_add_u64 v[176:177], s[70:71], 0, v[170:171]
	s_add_i32 m0, s33, 0xe000
	s_nop 0
	global_load_lds_dwordx4 v[176:177], off
	s_waitcnt vmcnt(8) lgkmcnt(0)
	s_barrier
	v_mfma_scale_f32_16x16x128_f8f6f4 v[158:161], v[26:33], v[190:197], v[158:161], v187, v188 op_sel_hi:[0,0,0]
	v_mfma_scale_f32_16x16x128_f8f6f4 v[154:157], v[18:25], v[190:197], v[154:157], v187, v188 op_sel_hi:[0,0,0]
	v_mfma_scale_f32_16x16x128_f8f6f4 v[150:153], v[26:33], v[198:205], v[150:153], v187, v188 op_sel_hi:[0,0,0]
	v_mfma_scale_f32_16x16x128_f8f6f4 v[142:145], v[18:25], v[198:205], v[142:145], v187, v188 op_sel_hi:[0,0,0]
	v_mfma_scale_f32_16x16x128_f8f6f4 v[134:137], v[26:33], v[206:213], v[134:137], v187, v188 op_sel_hi:[0,0,0]
	v_mfma_scale_f32_16x16x128_f8f6f4 v[126:129], v[18:25], v[206:213], v[126:129], v187, v188 op_sel_hi:[0,0,0]
	v_mfma_scale_f32_16x16x128_f8f6f4 v[118:121], v[26:33], v[220:227], v[118:121], v187, v188 op_sel_hi:[0,0,0]
	v_mfma_scale_f32_16x16x128_f8f6f4 v[110:113], v[18:25], v[220:227], v[110:113], v187, v188 op_sel_hi:[0,0,0]
	v_mfma_scale_f32_16x16x128_f8f6f4 v[146:149], v[10:17], v[190:197], v[146:149], v187, v188 op_sel_hi:[0,0,0]
	v_mfma_scale_f32_16x16x128_f8f6f4 v[138:141], v[2:9], v[190:197], v[138:141], v187, v188 op_sel_hi:[0,0,0]
	v_mfma_scale_f32_16x16x128_f8f6f4 v[130:133], v[10:17], v[198:205], v[130:133], v187, v188 op_sel_hi:[0,0,0]
	v_mfma_scale_f32_16x16x128_f8f6f4 v[122:125], v[2:9], v[198:205], v[122:125], v187, v188 op_sel_hi:[0,0,0]
	v_mfma_scale_f32_16x16x128_f8f6f4 v[114:117], v[10:17], v[206:213], v[114:117], v187, v188 op_sel_hi:[0,0,0]
	v_mfma_scale_f32_16x16x128_f8f6f4 v[106:109], v[2:9], v[206:213], v[106:109], v187, v188 op_sel_hi:[0,0,0]
	v_mfma_scale_f32_16x16x128_f8f6f4 v[102:105], v[10:17], v[220:227], v[102:105], v187, v188 op_sel_hi:[0,0,0]
	v_mfma_scale_f32_16x16x128_f8f6f4 v[98:101], v[2:9], v[220:227], v[98:101], v187, v188 op_sel_hi:[0,0,0]
	s_barrier
	s_add_i32 s26, s88, s80
	v_lshl_add_u64 v[176:177], s[74:75], 0, v[162:163]
	s_mov_b32 m0, s26
	ds_read_b128 v[190:193], v186 offset:16384
	ds_read_b128 v[194:197], v186 offset:17408
	ds_read_b128 v[198:201], v186 offset:18432
	ds_read_b128 v[202:205], v186 offset:19456
	ds_read_b128 v[206:209], v186 offset:20480
	ds_read_b128 v[210:213], v186 offset:21504
	ds_read_b128 v[220:223], v186 offset:22528
	ds_read_b128 v[224:227], v186 offset:23552
	global_load_lds_dwordx4 v[176:177], off
	v_lshl_add_u64 v[178:179], v[176:177], 0, s[8:9]
	s_add_i32 m0, s26, 0x2000
	s_add_i32 s26, s89, s80
	global_load_lds_dwordx4 v[178:179], off
	v_lshl_add_u64 v[178:179], v[176:177], 0, s[10:11]
	s_mov_b32 m0, s26
	v_lshl_add_u64 v[180:181], s[72:73], 0, v[166:167]
	global_load_lds_dwordx4 v[178:179], off
	v_lshl_add_u64 v[178:179], v[176:177], 0, s[12:13]
	s_add_i32 m0, s26, 0x2000
	s_nop 0
	global_load_lds_dwordx4 v[178:179], off
	v_lshl_add_u64 v[178:179], s[72:73], 0, v[164:165]
	s_mov_b32 m0, s33
	s_nop 0
	global_load_lds_dwordx4 v[178:179], off
	s_mov_b32 m0, s69
	s_nop 0
	global_load_lds_dwordx4 v[180:181], off
	s_waitcnt vmcnt(8) lgkmcnt(0)
	s_barrier
	v_mfma_scale_f32_16x16x128_f8f6f4 v[94:97], v[26:33], v[190:197], v[94:97], v187, v188 op_sel_hi:[0,0,0]
	v_mfma_scale_f32_16x16x128_f8f6f4 v[90:93], v[18:25], v[190:197], v[90:93], v187, v188 op_sel_hi:[0,0,0]
	v_mfma_scale_f32_16x16x128_f8f6f4 v[86:89], v[26:33], v[198:205], v[86:89], v187, v188 op_sel_hi:[0,0,0]
	v_mfma_scale_f32_16x16x128_f8f6f4 v[78:81], v[18:25], v[198:205], v[78:81], v187, v188 op_sel_hi:[0,0,0]
	v_mfma_scale_f32_16x16x128_f8f6f4 v[70:73], v[26:33], v[206:213], v[70:73], v187, v188 op_sel_hi:[0,0,0]
	v_mfma_scale_f32_16x16x128_f8f6f4 v[62:65], v[18:25], v[206:213], v[62:65], v187, v188 op_sel_hi:[0,0,0]
	v_mfma_scale_f32_16x16x128_f8f6f4 v[54:57], v[26:33], v[220:227], v[54:57], v187, v188 op_sel_hi:[0,0,0]
	v_mfma_scale_f32_16x16x128_f8f6f4 v[46:49], v[18:25], v[220:227], v[46:49], v187, v188 op_sel_hi:[0,0,0]
	v_mfma_scale_f32_16x16x128_f8f6f4 v[82:85], v[10:17], v[190:197], v[82:85], v187, v188 op_sel_hi:[0,0,0]
	v_mfma_scale_f32_16x16x128_f8f6f4 v[74:77], v[2:9], v[190:197], v[74:77], v187, v188 op_sel_hi:[0,0,0]
	v_mfma_scale_f32_16x16x128_f8f6f4 v[66:69], v[10:17], v[198:205], v[66:69], v187, v188 op_sel_hi:[0,0,0]
	v_mfma_scale_f32_16x16x128_f8f6f4 v[58:61], v[2:9], v[198:205], v[58:61], v187, v188 op_sel_hi:[0,0,0]
	v_mfma_scale_f32_16x16x128_f8f6f4 v[50:53], v[10:17], v[206:213], v[50:53], v187, v188 op_sel_hi:[0,0,0]
	v_mfma_scale_f32_16x16x128_f8f6f4 v[42:45], v[2:9], v[206:213], v[42:45], v187, v188 op_sel_hi:[0,0,0]
	v_mfma_scale_f32_16x16x128_f8f6f4 v[38:41], v[10:17], v[220:227], v[38:41], v187, v188 op_sel_hi:[0,0,0]
	v_mfma_scale_f32_16x16x128_f8f6f4 v[34:37], v[2:9], v[220:227], v[34:37], v187, v188 op_sel_hi:[0,0,0]
	s_barrier
	s_add_i32 s74, 0, 0x18000
	s_add_i32 s75, 0, 0x1c000
	v_add_u32_e32 v14, s74, v183
	v_add_u32_e32 v30, s75, v183
	ds_read_b128 v[2:5], v14
	ds_read_b128 v[6:9], v14 offset:1024
	ds_read_b128 v[10:13], v14 offset:2048
	ds_read_b128 v[14:17], v14 offset:3072
	ds_read_b128 v[18:21], v30
	ds_read_b128 v[22:25], v30 offset:1024
	ds_read_b128 v[26:29], v30 offset:2048
	ds_read_b128 v[30:33], v30 offset:3072
	s_add_u32 s26, s72, 0x40000
	s_addc_u32 s27, s73, 0
	s_mov_b32 m0, s83
	v_lshl_add_u64 v[214:215], s[26:27], 0, v[164:165]
	ds_read_b128 v[190:193], v186 offset:32768
	ds_read_b128 v[194:197], v186 offset:33792
	ds_read_b128 v[198:201], v186 offset:34816
	ds_read_b128 v[202:205], v186 offset:35840
	ds_read_b128 v[206:209], v186 offset:36864
	ds_read_b128 v[210:213], v186 offset:37888
	ds_read_b128 v[220:223], v186 offset:38912
	ds_read_b128 v[224:227], v186 offset:39936
	global_load_lds_dwordx4 v[214:215], off
	v_lshl_add_u64 v[214:215], s[26:27], 0, v[166:167]
	s_mov_b32 m0, s84
	s_nop 0
	global_load_lds_dwordx4 v[214:215], off
	s_waitcnt vmcnt(8) lgkmcnt(0)
	s_barrier
	v_mfma_scale_f32_16x16x128_f8f6f4 v[158:161], v[2:9], v[190:197], v[158:161], v187, v188 op_sel_hi:[0,0,0]
	v_mfma_scale_f32_16x16x128_f8f6f4 v[154:157], v[10:17], v[190:197], v[154:157], v187, v188 op_sel_hi:[0,0,0]
	v_mfma_scale_f32_16x16x128_f8f6f4 v[150:153], v[2:9], v[198:205], v[150:153], v187, v188 op_sel_hi:[0,0,0]
	v_mfma_scale_f32_16x16x128_f8f6f4 v[142:145], v[10:17], v[198:205], v[142:145], v187, v188 op_sel_hi:[0,0,0]
	v_mfma_scale_f32_16x16x128_f8f6f4 v[134:137], v[2:9], v[206:213], v[134:137], v187, v188 op_sel_hi:[0,0,0]
	v_mfma_scale_f32_16x16x128_f8f6f4 v[126:129], v[10:17], v[206:213], v[126:129], v187, v188 op_sel_hi:[0,0,0]
	v_mfma_scale_f32_16x16x128_f8f6f4 v[118:121], v[2:9], v[220:227], v[118:121], v187, v188 op_sel_hi:[0,0,0]
	v_mfma_scale_f32_16x16x128_f8f6f4 v[110:113], v[10:17], v[220:227], v[110:113], v187, v188 op_sel_hi:[0,0,0]
	v_mfma_scale_f32_16x16x128_f8f6f4 v[146:149], v[18:25], v[190:197], v[146:149], v187, v188 op_sel_hi:[0,0,0]
	v_mfma_scale_f32_16x16x128_f8f6f4 v[138:141], v[26:33], v[190:197], v[138:141], v187, v188 op_sel_hi:[0,0,0]
	v_mfma_scale_f32_16x16x128_f8f6f4 v[130:133], v[18:25], v[198:205], v[130:133], v187, v188 op_sel_hi:[0,0,0]
	v_mfma_scale_f32_16x16x128_f8f6f4 v[122:125], v[26:33], v[198:205], v[122:125], v187, v188 op_sel_hi:[0,0,0]
	v_mfma_scale_f32_16x16x128_f8f6f4 v[114:117], v[18:25], v[206:213], v[114:117], v187, v188 op_sel_hi:[0,0,0]
	v_mfma_scale_f32_16x16x128_f8f6f4 v[106:109], v[26:33], v[206:213], v[106:109], v187, v188 op_sel_hi:[0,0,0]
	v_mfma_scale_f32_16x16x128_f8f6f4 v[102:105], v[18:25], v[220:227], v[102:105], v187, v188 op_sel_hi:[0,0,0]
	v_mfma_scale_f32_16x16x128_f8f6f4 v[98:101], v[26:33], v[220:227], v[98:101], v187, v188 op_sel_hi:[0,0,0]
	s_barrier
	s_add_i32 s26, s74, s80
	v_lshl_add_u64 v[214:215], v[176:177], 0, s[16:17]
	s_mov_b32 m0, s26
	ds_read_b128 v[190:193], v186 offset:49152
	ds_read_b128 v[194:197], v186 offset:50176
	ds_read_b128 v[198:201], v186 offset:51200
	ds_read_b128 v[202:205], v186 offset:52224
	ds_read_b128 v[206:209], v186 offset:53248
	ds_read_b128 v[210:213], v186 offset:54272
	ds_read_b128 v[220:223], v186 offset:55296
	ds_read_b128 v[224:227], v186 offset:56320
	global_load_lds_dwordx4 v[214:215], off
	v_lshl_add_u64 v[214:215], v[176:177], 0, s[18:19]
	s_add_i32 m0, s26, 0x2000
	s_add_i32 s26, s75, s80
	global_load_lds_dwordx4 v[214:215], off
	v_lshl_add_u64 v[214:215], v[176:177], 0, s[22:23]
	s_mov_b32 m0, s26
	v_lshl_add_u64 v[176:177], v[176:177], 0, s[24:25]
	global_load_lds_dwordx4 v[214:215], off
	s_add_i32 m0, s26, 0x2000
	s_nop 0
	global_load_lds_dwordx4 v[176:177], off
	v_lshl_add_u64 v[176:177], v[178:179], 0, s[20:21]
	s_mov_b32 m0, s86
	s_nop 0
	global_load_lds_dwordx4 v[176:177], off
	v_lshl_add_u64 v[176:177], v[180:181], 0, s[20:21]
	s_mov_b32 m0, s87
	s_nop 0
	global_load_lds_dwordx4 v[176:177], off
	s_waitcnt vmcnt(8) lgkmcnt(0)
	s_barrier
	v_mfma_scale_f32_16x16x128_f8f6f4 v[94:97], v[2:9], v[190:197], v[94:97], v187, v188 op_sel_hi:[0,0,0]
	v_mfma_scale_f32_16x16x128_f8f6f4 v[90:93], v[10:17], v[190:197], v[90:93], v187, v188 op_sel_hi:[0,0,0]
	v_mfma_scale_f32_16x16x128_f8f6f4 v[86:89], v[2:9], v[198:205], v[86:89], v187, v188 op_sel_hi:[0,0,0]
	v_mfma_scale_f32_16x16x128_f8f6f4 v[78:81], v[10:17], v[198:205], v[78:81], v187, v188 op_sel_hi:[0,0,0]
	v_mfma_scale_f32_16x16x128_f8f6f4 v[70:73], v[2:9], v[206:213], v[70:73], v187, v188 op_sel_hi:[0,0,0]
	v_mfma_scale_f32_16x16x128_f8f6f4 v[62:65], v[10:17], v[206:213], v[62:65], v187, v188 op_sel_hi:[0,0,0]
	v_mfma_scale_f32_16x16x128_f8f6f4 v[54:57], v[2:9], v[220:227], v[54:57], v187, v188 op_sel_hi:[0,0,0]
	v_mfma_scale_f32_16x16x128_f8f6f4 v[46:49], v[10:17], v[220:227], v[46:49], v187, v188 op_sel_hi:[0,0,0]
	v_mfma_scale_f32_16x16x128_f8f6f4 v[82:85], v[18:25], v[190:197], v[82:85], v187, v188 op_sel_hi:[0,0,0]
	v_mfma_scale_f32_16x16x128_f8f6f4 v[74:77], v[26:33], v[190:197], v[74:77], v187, v188 op_sel_hi:[0,0,0]
	v_mfma_scale_f32_16x16x128_f8f6f4 v[66:69], v[18:25], v[198:205], v[66:69], v187, v188 op_sel_hi:[0,0,0]
	v_mfma_scale_f32_16x16x128_f8f6f4 v[58:61], v[26:33], v[198:205], v[58:61], v187, v188 op_sel_hi:[0,0,0]
	v_mfma_scale_f32_16x16x128_f8f6f4 v[50:53], v[18:25], v[206:213], v[50:53], v187, v188 op_sel_hi:[0,0,0]
	v_mfma_scale_f32_16x16x128_f8f6f4 v[42:45], v[26:33], v[206:213], v[42:45], v187, v188 op_sel_hi:[0,0,0]
	v_mfma_scale_f32_16x16x128_f8f6f4 v[38:41], v[18:25], v[220:227], v[38:41], v187, v188 op_sel_hi:[0,0,0]
	v_mfma_scale_f32_16x16x128_f8f6f4 v[34:37], v[26:33], v[220:227], v[34:37], v187, v188 op_sel_hi:[0,0,0]
	s_barrier
	s_add_i32 s94, s94, 2
	s_add_u32 s92, s92, 0x10000
	s_addc_u32 s93, s93, 0
	s_add_u32 s70, s70, 0x100
	s_addc_u32 s71, s71, 0
	s_cmp_gt_u32 s94, 13
	s_cbranch_scc0 .LBB0_285
	s_and_b64 vcc, exec, s[40:41]
	s_cbranch_vccz .LBB0_288
	s_barrier

.LBB0_659:
	s_ashr_i32 s45, s44, 31
	s_lshl_b64 s[26:27], s[44:45], 20
	v_readlane_b32 s50, v254, 58
	v_readlane_b32 s51, v254, 59
	s_add_u32 s50, s50, s26
	s_addc_u32 s51, s51, s27
	s_and_b64 s[26:27], s[0:1], exec
	s_cselect_b32 s45, s51, s61
	s_cselect_b32 s72, s50, s60
	s_ashr_i32 s41, s40, 31
	s_lshl_b64 s[26:27], s[40:41], 20
	s_add_u32 s54, s3, s26
	s_addc_u32 s55, s33, s27
	s_and_b64 s[26:27], s[0:1], exec
	s_cselect_b32 s41, s55, s59
	s_cselect_b32 s73, s54, s58
	s_add_u32 s74, s58, 0x10000
	s_addc_u32 s75, s59, 0
	s_add_u32 s58, s60, 0x80080
	s_addc_u32 s59, s61, 0
	s_mov_b32 s80, -2
	ds_read_b128 v[130:133], v222
	ds_read_b128 v[134:137], v222 offset:1024
	ds_read_b128 v[138:141], v222 offset:2048
	ds_read_b128 v[142:145], v222 offset:3072
	ds_read_b128 v[146:149], v223
	ds_read_b128 v[150:153], v223 offset:1024
	ds_read_b128 v[154:157], v223 offset:2048
	ds_read_b128 v[158:161], v223 offset:3072
	s_add_u32 s26, s58, 0xfff80080
	s_addc_u32 s27, s59, -1
	s_cmp_eq_u32 s80, 28
	s_cselect_b32 s61, s45, s27
	s_cselect_b32 s60, s72, s26
	s_cselect_b32 s27, s41, s75
	s_cselect_b32 s26, s73, s74
	v_lshl_add_u64 v[208:209], s[58:59], 0, v[200:201]
	s_add_i32 m0, s57, 0xc000
	ds_read_b128 v[162:165], v224
	ds_read_b128 v[166:169], v224 offset:1024
	ds_read_b128 v[170:173], v224 offset:2048
	ds_read_b128 v[174:177], v224 offset:3072
	ds_read_b128 v[178:181], v224 offset:4096
	ds_read_b128 v[182:185], v224 offset:5120
	ds_read_b128 v[186:189], v224 offset:6144
	ds_read_b128 v[190:193], v224 offset:7168
	global_load_lds_dwordx4 v[208:209], off
	v_lshl_add_u64 v[208:209], s[58:59], 0, v[202:203]
	s_add_i32 m0, s57, 0xe000
	s_nop 0
	global_load_lds_dwordx4 v[208:209], off
	s_waitcnt vmcnt(8) lgkmcnt(0)
	s_barrier
	v_mfma_f32_16x16x32_bf16 v[126:129], v[130:133], v[162:165], 0
	v_mfma_f32_16x16x32_bf16 v[122:125], v[138:141], v[162:165], 0
	v_mfma_f32_16x16x32_bf16 v[118:121], v[130:133], v[170:173], 0
	v_mfma_f32_16x16x32_bf16 v[114:117], v[138:141], v[170:173], 0
	v_mfma_f32_16x16x32_bf16 v[110:113], v[130:133], v[178:181], 0
	v_mfma_f32_16x16x32_bf16 v[102:105], v[138:141], v[178:181], 0
	v_mfma_f32_16x16x32_bf16 v[94:97], v[130:133], v[186:189], 0
	v_mfma_f32_16x16x32_bf16 v[74:77], v[138:141], v[186:189], 0
	v_mfma_f32_16x16x32_bf16 v[126:129], v[134:137], v[166:169], v[126:129]
	v_mfma_f32_16x16x32_bf16 v[122:125], v[142:145], v[166:169], v[122:125]
	v_mfma_f32_16x16x32_bf16 v[118:121], v[134:137], v[174:177], v[118:121]
	v_mfma_f32_16x16x32_bf16 v[114:117], v[142:145], v[174:177], v[114:117]
	v_mfma_f32_16x16x32_bf16 v[110:113], v[134:137], v[182:185], v[110:113]
	v_mfma_f32_16x16x32_bf16 v[102:105], v[142:145], v[182:185], v[102:105]
	v_mfma_f32_16x16x32_bf16 v[94:97], v[134:137], v[190:193], v[94:97]
	v_mfma_f32_16x16x32_bf16 v[74:77], v[142:145], v[190:193], v[74:77]
	v_mfma_f32_16x16x32_bf16 v[106:109], v[146:149], v[162:165], 0
	v_mfma_f32_16x16x32_bf16 v[98:101], v[154:157], v[162:165], 0
	v_mfma_f32_16x16x32_bf16 v[90:93], v[146:149], v[170:173], 0
	v_mfma_f32_16x16x32_bf16 v[86:89], v[154:157], v[170:173], 0
	v_mfma_f32_16x16x32_bf16 v[82:85], v[146:149], v[178:181], 0
	v_mfma_f32_16x16x32_bf16 v[78:81], v[154:157], v[178:181], 0
	v_mfma_f32_16x16x32_bf16 v[70:73], v[146:149], v[186:189], 0
	v_mfma_f32_16x16x32_bf16 v[66:69], v[154:157], v[186:189], 0
	v_mfma_f32_16x16x32_bf16 v[106:109], v[150:153], v[166:169], v[106:109]
	v_mfma_f32_16x16x32_bf16 v[98:101], v[158:161], v[166:169], v[98:101]
	v_mfma_f32_16x16x32_bf16 v[90:93], v[150:153], v[174:177], v[90:93]
	v_mfma_f32_16x16x32_bf16 v[86:89], v[158:161], v[174:177], v[86:89]
	v_mfma_f32_16x16x32_bf16 v[82:85], v[150:153], v[182:185], v[82:85]
	v_mfma_f32_16x16x32_bf16 v[78:81], v[158:161], v[182:185], v[78:81]
	v_mfma_f32_16x16x32_bf16 v[70:73], v[150:153], v[190:193], v[70:73]
	v_mfma_f32_16x16x32_bf16 v[66:69], v[158:161], v[190:193], v[66:69]
	s_barrier
	v_lshl_add_u64 v[208:209], s[26:27], 0, v[194:195]
	s_add_i32 s26, s70, s35
	s_mov_b32 m0, s26
	ds_read_b128 v[162:165], v224 offset:16384
	ds_read_b128 v[166:169], v224 offset:17408
	ds_read_b128 v[170:173], v224 offset:18432
	ds_read_b128 v[174:177], v224 offset:19456
	ds_read_b128 v[178:181], v224 offset:20480
	ds_read_b128 v[182:185], v224 offset:21504
	ds_read_b128 v[186:189], v224 offset:22528
	ds_read_b128 v[190:193], v224 offset:23552
	global_load_lds_dwordx4 v[208:209], off
	v_lshl_add_u64 v[210:211], v[208:209], 0, s[6:7]
	s_add_i32 m0, s26, 0x2000
	s_add_i32 s26, s71, s35
	global_load_lds_dwordx4 v[210:211], off
	v_lshl_add_u64 v[210:211], v[208:209], 0, s[8:9]
	s_mov_b32 m0, s26
	v_lshl_add_u64 v[212:213], s[60:61], 0, v[198:199]
	global_load_lds_dwordx4 v[210:211], off
	v_lshl_add_u64 v[210:211], v[208:209], 0, s[10:11]
	s_add_i32 m0, s26, 0x2000
	s_nop 0
	global_load_lds_dwordx4 v[210:211], off
	v_lshl_add_u64 v[210:211], s[60:61], 0, v[196:197]
	s_mov_b32 m0, s57
	s_nop 0
	global_load_lds_dwordx4 v[210:211], off
	s_mov_b32 m0, s63
	s_nop 0
	global_load_lds_dwordx4 v[212:213], off
	s_waitcnt vmcnt(8) lgkmcnt(0)
	s_barrier
	v_mfma_f32_16x16x32_bf16 v[62:65], v[130:133], v[162:165], 0
	v_mfma_f32_16x16x32_bf16 v[58:61], v[138:141], v[162:165], 0
	v_mfma_f32_16x16x32_bf16 v[54:57], v[130:133], v[170:173], 0
	v_mfma_f32_16x16x32_bf16 v[50:53], v[138:141], v[170:173], 0
	v_mfma_f32_16x16x32_bf16 v[46:49], v[130:133], v[178:181], 0
	v_mfma_f32_16x16x32_bf16 v[38:41], v[138:141], v[178:181], 0
	v_mfma_f32_16x16x32_bf16 v[30:33], v[130:133], v[186:189], 0
	v_mfma_f32_16x16x32_bf16 v[10:13], v[138:141], v[186:189], 0
	v_mfma_f32_16x16x32_bf16 v[62:65], v[134:137], v[166:169], v[62:65]
	v_mfma_f32_16x16x32_bf16 v[58:61], v[142:145], v[166:169], v[58:61]
	v_mfma_f32_16x16x32_bf16 v[54:57], v[134:137], v[174:177], v[54:57]
	v_mfma_f32_16x16x32_bf16 v[50:53], v[142:145], v[174:177], v[50:53]
	v_mfma_f32_16x16x32_bf16 v[46:49], v[134:137], v[182:185], v[46:49]
	v_mfma_f32_16x16x32_bf16 v[38:41], v[142:145], v[182:185], v[38:41]
	v_mfma_f32_16x16x32_bf16 v[30:33], v[134:137], v[190:193], v[30:33]
	v_mfma_f32_16x16x32_bf16 v[10:13], v[142:145], v[190:193], v[10:13]
	v_mfma_f32_16x16x32_bf16 v[42:45], v[146:149], v[162:165], 0
	v_mfma_f32_16x16x32_bf16 v[34:37], v[154:157], v[162:165], 0
	v_mfma_f32_16x16x32_bf16 v[26:29], v[146:149], v[170:173], 0
	v_mfma_f32_16x16x32_bf16 v[22:25], v[154:157], v[170:173], 0
	v_mfma_f32_16x16x32_bf16 v[18:21], v[146:149], v[178:181], 0
	v_mfma_f32_16x16x32_bf16 v[14:17], v[154:157], v[178:181], 0
	v_mfma_f32_16x16x32_bf16 v[6:9], v[146:149], v[186:189], 0
	v_mfma_f32_16x16x32_bf16 v[2:5], v[154:157], v[186:189], 0
	v_mfma_f32_16x16x32_bf16 v[42:45], v[150:153], v[166:169], v[42:45]
	v_mfma_f32_16x16x32_bf16 v[34:37], v[158:161], v[166:169], v[34:37]
	v_mfma_f32_16x16x32_bf16 v[26:29], v[150:153], v[174:177], v[26:29]
	v_mfma_f32_16x16x32_bf16 v[22:25], v[158:161], v[174:177], v[22:25]
	v_mfma_f32_16x16x32_bf16 v[18:21], v[150:153], v[182:185], v[18:21]
	v_mfma_f32_16x16x32_bf16 v[14:17], v[158:161], v[182:185], v[14:17]
	v_mfma_f32_16x16x32_bf16 v[6:9], v[150:153], v[190:193], v[6:9]
	v_mfma_f32_16x16x32_bf16 v[2:5], v[158:161], v[190:193], v[2:5]
	s_barrier
	s_add_i32 s81, 0, 0x18000
	s_add_i32 s82, 0, 0x1c000
	v_add_u32_e32 v142, s81, v220
	v_add_u32_e32 v158, s82, v220
	ds_read_b128 v[130:133], v142
	ds_read_b128 v[134:137], v142 offset:1024
	ds_read_b128 v[138:141], v142 offset:2048
	ds_read_b128 v[142:145], v142 offset:3072
	ds_read_b128 v[146:149], v158
	ds_read_b128 v[150:153], v158 offset:1024
	ds_read_b128 v[154:157], v158 offset:2048
	ds_read_b128 v[158:161], v158 offset:3072
	s_add_u32 s26, s60, 0x80000
	s_addc_u32 s27, s61, 0
	s_mov_b32 m0, s64
	v_lshl_add_u64 v[214:215], s[26:27], 0, v[196:197]
	ds_read_b128 v[162:165], v224 offset:32768
	ds_read_b128 v[166:169], v224 offset:33792
	ds_read_b128 v[170:173], v224 offset:34816
	ds_read_b128 v[174:177], v224 offset:35840
	ds_read_b128 v[178:181], v224 offset:36864
	ds_read_b128 v[182:185], v224 offset:37888
	ds_read_b128 v[186:189], v224 offset:38912
	ds_read_b128 v[190:193], v224 offset:39936
	global_load_lds_dwordx4 v[214:215], off
	v_lshl_add_u64 v[214:215], s[26:27], 0, v[198:199]
	s_mov_b32 m0, s65
	s_nop 0
	global_load_lds_dwordx4 v[214:215], off
	s_waitcnt vmcnt(8) lgkmcnt(0)
	s_barrier
	v_mfma_f32_16x16x32_bf16 v[126:129], v[130:133], v[162:165], v[126:129]
	v_mfma_f32_16x16x32_bf16 v[122:125], v[138:141], v[162:165], v[122:125]
	v_mfma_f32_16x16x32_bf16 v[118:121], v[130:133], v[170:173], v[118:121]
	v_mfma_f32_16x16x32_bf16 v[114:117], v[138:141], v[170:173], v[114:117]
	v_mfma_f32_16x16x32_bf16 v[110:113], v[130:133], v[178:181], v[110:113]
	v_mfma_f32_16x16x32_bf16 v[102:105], v[138:141], v[178:181], v[102:105]
	v_mfma_f32_16x16x32_bf16 v[94:97], v[130:133], v[186:189], v[94:97]
	v_mfma_f32_16x16x32_bf16 v[74:77], v[138:141], v[186:189], v[74:77]
	v_mfma_f32_16x16x32_bf16 v[126:129], v[134:137], v[166:169], v[126:129]
	v_mfma_f32_16x16x32_bf16 v[122:125], v[142:145], v[166:169], v[122:125]
	v_mfma_f32_16x16x32_bf16 v[118:121], v[134:137], v[174:177], v[118:121]
	v_mfma_f32_16x16x32_bf16 v[114:117], v[142:145], v[174:177], v[114:117]
	v_mfma_f32_16x16x32_bf16 v[110:113], v[134:137], v[182:185], v[110:113]
	v_mfma_f32_16x16x32_bf16 v[102:105], v[142:145], v[182:185], v[102:105]
	v_mfma_f32_16x16x32_bf16 v[94:97], v[134:137], v[190:193], v[94:97]
	v_mfma_f32_16x16x32_bf16 v[74:77], v[142:145], v[190:193], v[74:77]
	v_mfma_f32_16x16x32_bf16 v[106:109], v[146:149], v[162:165], v[106:109]
	v_mfma_f32_16x16x32_bf16 v[98:101], v[154:157], v[162:165], v[98:101]
	v_mfma_f32_16x16x32_bf16 v[90:93], v[146:149], v[170:173], v[90:93]
	v_mfma_f32_16x16x32_bf16 v[86:89], v[154:157], v[170:173], v[86:89]
	v_mfma_f32_16x16x32_bf16 v[82:85], v[146:149], v[178:181], v[82:85]
	v_mfma_f32_16x16x32_bf16 v[78:81], v[154:157], v[178:181], v[78:81]
	v_mfma_f32_16x16x32_bf16 v[70:73], v[146:149], v[186:189], v[70:73]
	v_mfma_f32_16x16x32_bf16 v[66:69], v[154:157], v[186:189], v[66:69]
	v_mfma_f32_16x16x32_bf16 v[106:109], v[150:153], v[166:169], v[106:109]
	v_mfma_f32_16x16x32_bf16 v[98:101], v[158:161], v[166:169], v[98:101]
	v_mfma_f32_16x16x32_bf16 v[90:93], v[150:153], v[174:177], v[90:93]
	v_mfma_f32_16x16x32_bf16 v[86:89], v[158:161], v[174:177], v[86:89]
	v_mfma_f32_16x16x32_bf16 v[82:85], v[150:153], v[182:185], v[82:85]
	v_mfma_f32_16x16x32_bf16 v[78:81], v[158:161], v[182:185], v[78:81]
	v_mfma_f32_16x16x32_bf16 v[70:73], v[150:153], v[190:193], v[70:73]
	v_mfma_f32_16x16x32_bf16 v[66:69], v[158:161], v[190:193], v[66:69]
	s_barrier
	s_add_i32 s26, s81, s35
	v_lshl_add_u64 v[214:215], v[208:209], 0, s[14:15]
	s_mov_b32 m0, s26
	ds_read_b128 v[162:165], v224 offset:49152
	ds_read_b128 v[166:169], v224 offset:50176
	ds_read_b128 v[170:173], v224 offset:51200
	ds_read_b128 v[174:177], v224 offset:52224
	ds_read_b128 v[178:181], v224 offset:53248
	ds_read_b128 v[182:185], v224 offset:54272
	ds_read_b128 v[186:189], v224 offset:55296
	ds_read_b128 v[190:193], v224 offset:56320
	global_load_lds_dwordx4 v[214:215], off
	v_lshl_add_u64 v[214:215], v[208:209], 0, s[16:17]
	s_add_i32 m0, s26, 0x2000
	s_add_i32 s26, s82, s35
	global_load_lds_dwordx4 v[214:215], off
	v_lshl_add_u64 v[214:215], v[208:209], 0, s[20:21]
	s_mov_b32 m0, s26
	v_lshl_add_u64 v[208:209], v[208:209], 0, s[22:23]
	global_load_lds_dwordx4 v[214:215], off
	s_add_i32 m0, s26, 0x2000
	s_nop 0
	global_load_lds_dwordx4 v[208:209], off
	v_lshl_add_u64 v[208:209], v[210:211], 0, s[18:19]
	s_mov_b32 m0, s67
	s_nop 0
	global_load_lds_dwordx4 v[208:209], off
	v_lshl_add_u64 v[208:209], v[212:213], 0, s[18:19]
	s_mov_b32 m0, s68
	s_nop 0
	global_load_lds_dwordx4 v[208:209], off
	s_waitcnt vmcnt(8) lgkmcnt(0)
	s_barrier
	v_mfma_f32_16x16x32_bf16 v[62:65], v[130:133], v[162:165], v[62:65]
	v_mfma_f32_16x16x32_bf16 v[58:61], v[138:141], v[162:165], v[58:61]
	v_mfma_f32_16x16x32_bf16 v[54:57], v[130:133], v[170:173], v[54:57]
	v_mfma_f32_16x16x32_bf16 v[50:53], v[138:141], v[170:173], v[50:53]
	v_mfma_f32_16x16x32_bf16 v[46:49], v[130:133], v[178:181], v[46:49]
	v_mfma_f32_16x16x32_bf16 v[38:41], v[138:141], v[178:181], v[38:41]
	v_mfma_f32_16x16x32_bf16 v[30:33], v[130:133], v[186:189], v[30:33]
	v_mfma_f32_16x16x32_bf16 v[10:13], v[138:141], v[186:189], v[10:13]
	v_mfma_f32_16x16x32_bf16 v[62:65], v[134:137], v[166:169], v[62:65]
	v_mfma_f32_16x16x32_bf16 v[58:61], v[142:145], v[166:169], v[58:61]
	v_mfma_f32_16x16x32_bf16 v[54:57], v[134:137], v[174:177], v[54:57]
	v_mfma_f32_16x16x32_bf16 v[50:53], v[142:145], v[174:177], v[50:53]
	v_mfma_f32_16x16x32_bf16 v[46:49], v[134:137], v[182:185], v[46:49]
	v_mfma_f32_16x16x32_bf16 v[38:41], v[142:145], v[182:185], v[38:41]
	v_mfma_f32_16x16x32_bf16 v[30:33], v[134:137], v[190:193], v[30:33]
	v_mfma_f32_16x16x32_bf16 v[10:13], v[142:145], v[190:193], v[10:13]
	v_mfma_f32_16x16x32_bf16 v[42:45], v[146:149], v[162:165], v[42:45]
	v_mfma_f32_16x16x32_bf16 v[34:37], v[154:157], v[162:165], v[34:37]
	v_mfma_f32_16x16x32_bf16 v[26:29], v[146:149], v[170:173], v[26:29]
	v_mfma_f32_16x16x32_bf16 v[22:25], v[154:157], v[170:173], v[22:25]
	v_mfma_f32_16x16x32_bf16 v[18:21], v[146:149], v[178:181], v[18:21]
	v_mfma_f32_16x16x32_bf16 v[14:17], v[154:157], v[178:181], v[14:17]
	v_mfma_f32_16x16x32_bf16 v[6:9], v[146:149], v[186:189], v[6:9]
	v_mfma_f32_16x16x32_bf16 v[2:5], v[154:157], v[186:189], v[2:5]
	v_mfma_f32_16x16x32_bf16 v[42:45], v[150:153], v[166:169], v[42:45]
	v_mfma_f32_16x16x32_bf16 v[34:37], v[158:161], v[166:169], v[34:37]
	v_mfma_f32_16x16x32_bf16 v[26:29], v[150:153], v[174:177], v[26:29]
	v_mfma_f32_16x16x32_bf16 v[22:25], v[158:161], v[174:177], v[22:25]
	v_mfma_f32_16x16x32_bf16 v[18:21], v[150:153], v[182:185], v[18:21]
	v_mfma_f32_16x16x32_bf16 v[14:17], v[158:161], v[182:185], v[14:17]
	v_mfma_f32_16x16x32_bf16 v[6:9], v[150:153], v[190:193], v[6:9]
	v_mfma_f32_16x16x32_bf16 v[2:5], v[158:161], v[190:193], v[2:5]
	s_barrier
	s_add_i32 s80, s80, 2
	s_add_u32 s74, s74, 0x10000
	s_addc_u32 s75, s75, 0
	s_add_u32 s58, s58, 0x100
	s_addc_u32 s59, s59, 0
	s_cmp_gt_u32 s80, 29
.LBB0_660:
	ds_read_b128 v[130:133], v222
	ds_read_b128 v[134:137], v222 offset:1024
	ds_read_b128 v[138:141], v222 offset:2048
	ds_read_b128 v[142:145], v222 offset:3072
	ds_read_b128 v[146:149], v223
	ds_read_b128 v[150:153], v223 offset:1024
	ds_read_b128 v[154:157], v223 offset:2048
	ds_read_b128 v[158:161], v223 offset:3072
	s_add_u32 s26, s58, 0xfff80080
	s_addc_u32 s27, s59, -1
	s_cmp_eq_u32 s80, 28
	s_cselect_b32 s61, s45, s27
	s_cselect_b32 s60, s72, s26
	s_cselect_b32 s27, s41, s75
	s_cselect_b32 s26, s73, s74
	v_lshl_add_u64 v[208:209], s[58:59], 0, v[200:201]
	s_add_i32 m0, s57, 0xc000
	ds_read_b128 v[162:165], v224
	ds_read_b128 v[166:169], v224 offset:1024
	ds_read_b128 v[170:173], v224 offset:2048
	ds_read_b128 v[174:177], v224 offset:3072
	ds_read_b128 v[178:181], v224 offset:4096
	ds_read_b128 v[182:185], v224 offset:5120
	ds_read_b128 v[186:189], v224 offset:6144
	ds_read_b128 v[190:193], v224 offset:7168
	global_load_lds_dwordx4 v[208:209], off
	v_lshl_add_u64 v[208:209], s[58:59], 0, v[202:203]
	s_add_i32 m0, s57, 0xe000
	s_nop 0
	global_load_lds_dwordx4 v[208:209], off
	s_waitcnt vmcnt(8) lgkmcnt(0)
	s_barrier
	v_mfma_f32_16x16x32_bf16 v[126:129], v[130:133], v[162:165], v[126:129]
	v_mfma_f32_16x16x32_bf16 v[122:125], v[138:141], v[162:165], v[122:125]
	v_mfma_f32_16x16x32_bf16 v[118:121], v[130:133], v[170:173], v[118:121]
	v_mfma_f32_16x16x32_bf16 v[114:117], v[138:141], v[170:173], v[114:117]
	v_mfma_f32_16x16x32_bf16 v[110:113], v[130:133], v[178:181], v[110:113]
	v_mfma_f32_16x16x32_bf16 v[102:105], v[138:141], v[178:181], v[102:105]
	v_mfma_f32_16x16x32_bf16 v[94:97], v[130:133], v[186:189], v[94:97]
	v_mfma_f32_16x16x32_bf16 v[74:77], v[138:141], v[186:189], v[74:77]
	v_mfma_f32_16x16x32_bf16 v[126:129], v[134:137], v[166:169], v[126:129]
	v_mfma_f32_16x16x32_bf16 v[122:125], v[142:145], v[166:169], v[122:125]
	v_mfma_f32_16x16x32_bf16 v[118:121], v[134:137], v[174:177], v[118:121]
	v_mfma_f32_16x16x32_bf16 v[114:117], v[142:145], v[174:177], v[114:117]
	v_mfma_f32_16x16x32_bf16 v[110:113], v[134:137], v[182:185], v[110:113]
	v_mfma_f32_16x16x32_bf16 v[102:105], v[142:145], v[182:185], v[102:105]
	v_mfma_f32_16x16x32_bf16 v[94:97], v[134:137], v[190:193], v[94:97]
	v_mfma_f32_16x16x32_bf16 v[74:77], v[142:145], v[190:193], v[74:77]
	v_mfma_f32_16x16x32_bf16 v[106:109], v[146:149], v[162:165], v[106:109]
	v_mfma_f32_16x16x32_bf16 v[98:101], v[154:157], v[162:165], v[98:101]
	v_mfma_f32_16x16x32_bf16 v[90:93], v[146:149], v[170:173], v[90:93]
	v_mfma_f32_16x16x32_bf16 v[86:89], v[154:157], v[170:173], v[86:89]
	v_mfma_f32_16x16x32_bf16 v[82:85], v[146:149], v[178:181], v[82:85]
	v_mfma_f32_16x16x32_bf16 v[78:81], v[154:157], v[178:181], v[78:81]
	v_mfma_f32_16x16x32_bf16 v[70:73], v[146:149], v[186:189], v[70:73]
	v_mfma_f32_16x16x32_bf16 v[66:69], v[154:157], v[186:189], v[66:69]
	v_mfma_f32_16x16x32_bf16 v[106:109], v[150:153], v[166:169], v[106:109]
	v_mfma_f32_16x16x32_bf16 v[98:101], v[158:161], v[166:169], v[98:101]
	v_mfma_f32_16x16x32_bf16 v[90:93], v[150:153], v[174:177], v[90:93]
	v_mfma_f32_16x16x32_bf16 v[86:89], v[158:161], v[174:177], v[86:89]
	v_mfma_f32_16x16x32_bf16 v[82:85], v[150:153], v[182:185], v[82:85]
	v_mfma_f32_16x16x32_bf16 v[78:81], v[158:161], v[182:185], v[78:81]
	v_mfma_f32_16x16x32_bf16 v[70:73], v[150:153], v[190:193], v[70:73]
	v_mfma_f32_16x16x32_bf16 v[66:69], v[158:161], v[190:193], v[66:69]
	s_barrier
	v_lshl_add_u64 v[208:209], s[26:27], 0, v[194:195]
	s_add_i32 s26, s70, s35
	s_mov_b32 m0, s26
	ds_read_b128 v[162:165], v224 offset:16384
	ds_read_b128 v[166:169], v224 offset:17408
	ds_read_b128 v[170:173], v224 offset:18432
	ds_read_b128 v[174:177], v224 offset:19456
	ds_read_b128 v[178:181], v224 offset:20480
	ds_read_b128 v[182:185], v224 offset:21504
	ds_read_b128 v[186:189], v224 offset:22528
	ds_read_b128 v[190:193], v224 offset:23552
	global_load_lds_dwordx4 v[208:209], off
	v_lshl_add_u64 v[210:211], v[208:209], 0, s[6:7]
	s_add_i32 m0, s26, 0x2000
	s_add_i32 s26, s71, s35
	global_load_lds_dwordx4 v[210:211], off
	v_lshl_add_u64 v[210:211], v[208:209], 0, s[8:9]
	s_mov_b32 m0, s26
	v_lshl_add_u64 v[212:213], s[60:61], 0, v[198:199]
	global_load_lds_dwordx4 v[210:211], off
	v_lshl_add_u64 v[210:211], v[208:209], 0, s[10:11]
	s_add_i32 m0, s26, 0x2000
	s_nop 0
	global_load_lds_dwordx4 v[210:211], off
	v_lshl_add_u64 v[210:211], s[60:61], 0, v[196:197]
	s_mov_b32 m0, s57
	s_nop 0
	global_load_lds_dwordx4 v[210:211], off
	s_mov_b32 m0, s63
	s_nop 0
	global_load_lds_dwordx4 v[212:213], off
	s_waitcnt vmcnt(8) lgkmcnt(0)
	s_barrier
	v_mfma_f32_16x16x32_bf16 v[62:65], v[130:133], v[162:165], v[62:65]
	v_mfma_f32_16x16x32_bf16 v[58:61], v[138:141], v[162:165], v[58:61]
	v_mfma_f32_16x16x32_bf16 v[54:57], v[130:133], v[170:173], v[54:57]
	v_mfma_f32_16x16x32_bf16 v[50:53], v[138:141], v[170:173], v[50:53]
	v_mfma_f32_16x16x32_bf16 v[46:49], v[130:133], v[178:181], v[46:49]
	v_mfma_f32_16x16x32_bf16 v[38:41], v[138:141], v[178:181], v[38:41]
	v_mfma_f32_16x16x32_bf16 v[30:33], v[130:133], v[186:189], v[30:33]
	v_mfma_f32_16x16x32_bf16 v[10:13], v[138:141], v[186:189], v[10:13]
	v_mfma_f32_16x16x32_bf16 v[62:65], v[134:137], v[166:169], v[62:65]
	v_mfma_f32_16x16x32_bf16 v[58:61], v[142:145], v[166:169], v[58:61]
	v_mfma_f32_16x16x32_bf16 v[54:57], v[134:137], v[174:177], v[54:57]
	v_mfma_f32_16x16x32_bf16 v[50:53], v[142:145], v[174:177], v[50:53]
	v_mfma_f32_16x16x32_bf16 v[46:49], v[134:137], v[182:185], v[46:49]
	v_mfma_f32_16x16x32_bf16 v[38:41], v[142:145], v[182:185], v[38:41]
	v_mfma_f32_16x16x32_bf16 v[30:33], v[134:137], v[190:193], v[30:33]
	v_mfma_f32_16x16x32_bf16 v[10:13], v[142:145], v[190:193], v[10:13]
	v_mfma_f32_16x16x32_bf16 v[42:45], v[146:149], v[162:165], v[42:45]
	v_mfma_f32_16x16x32_bf16 v[34:37], v[154:157], v[162:165], v[34:37]
	v_mfma_f32_16x16x32_bf16 v[26:29], v[146:149], v[170:173], v[26:29]
	v_mfma_f32_16x16x32_bf16 v[22:25], v[154:157], v[170:173], v[22:25]
	v_mfma_f32_16x16x32_bf16 v[18:21], v[146:149], v[178:181], v[18:21]
	v_mfma_f32_16x16x32_bf16 v[14:17], v[154:157], v[178:181], v[14:17]
	v_mfma_f32_16x16x32_bf16 v[6:9], v[146:149], v[186:189], v[6:9]
	v_mfma_f32_16x16x32_bf16 v[2:5], v[154:157], v[186:189], v[2:5]
	v_mfma_f32_16x16x32_bf16 v[42:45], v[150:153], v[166:169], v[42:45]
	v_mfma_f32_16x16x32_bf16 v[34:37], v[158:161], v[166:169], v[34:37]
	v_mfma_f32_16x16x32_bf16 v[26:29], v[150:153], v[174:177], v[26:29]
	v_mfma_f32_16x16x32_bf16 v[22:25], v[158:161], v[174:177], v[22:25]
	v_mfma_f32_16x16x32_bf16 v[18:21], v[150:153], v[182:185], v[18:21]
	v_mfma_f32_16x16x32_bf16 v[14:17], v[158:161], v[182:185], v[14:17]
	v_mfma_f32_16x16x32_bf16 v[6:9], v[150:153], v[190:193], v[6:9]
	v_mfma_f32_16x16x32_bf16 v[2:5], v[158:161], v[190:193], v[2:5]
	s_barrier
	s_add_i32 s81, 0, 0x18000
	s_add_i32 s82, 0, 0x1c000
	v_add_u32_e32 v142, s81, v220
	v_add_u32_e32 v158, s82, v220
	ds_read_b128 v[130:133], v142
	ds_read_b128 v[134:137], v142 offset:1024
	ds_read_b128 v[138:141], v142 offset:2048
	ds_read_b128 v[142:145], v142 offset:3072
	ds_read_b128 v[146:149], v158
	ds_read_b128 v[150:153], v158 offset:1024
	ds_read_b128 v[154:157], v158 offset:2048
	ds_read_b128 v[158:161], v158 offset:3072
	s_add_u32 s26, s60, 0x80000
	s_addc_u32 s27, s61, 0
	s_mov_b32 m0, s64
	v_lshl_add_u64 v[214:215], s[26:27], 0, v[196:197]
	ds_read_b128 v[162:165], v224 offset:32768
	ds_read_b128 v[166:169], v224 offset:33792
	ds_read_b128 v[170:173], v224 offset:34816
	ds_read_b128 v[174:177], v224 offset:35840
	ds_read_b128 v[178:181], v224 offset:36864
	ds_read_b128 v[182:185], v224 offset:37888
	ds_read_b128 v[186:189], v224 offset:38912
	ds_read_b128 v[190:193], v224 offset:39936
	global_load_lds_dwordx4 v[214:215], off
	v_lshl_add_u64 v[214:215], s[26:27], 0, v[198:199]
	s_mov_b32 m0, s65
	s_nop 0
	global_load_lds_dwordx4 v[214:215], off
	s_waitcnt vmcnt(8) lgkmcnt(0)
	s_barrier
	v_mfma_f32_16x16x32_bf16 v[126:129], v[130:133], v[162:165], v[126:129]
	v_mfma_f32_16x16x32_bf16 v[122:125], v[138:141], v[162:165], v[122:125]
	v_mfma_f32_16x16x32_bf16 v[118:121], v[130:133], v[170:173], v[118:121]
	v_mfma_f32_16x16x32_bf16 v[114:117], v[138:141], v[170:173], v[114:117]
	v_mfma_f32_16x16x32_bf16 v[110:113], v[130:133], v[178:181], v[110:113]
	v_mfma_f32_16x16x32_bf16 v[102:105], v[138:141], v[178:181], v[102:105]
	v_mfma_f32_16x16x32_bf16 v[94:97], v[130:133], v[186:189], v[94:97]
	v_mfma_f32_16x16x32_bf16 v[74:77], v[138:141], v[186:189], v[74:77]
	v_mfma_f32_16x16x32_bf16 v[126:129], v[134:137], v[166:169], v[126:129]
	v_mfma_f32_16x16x32_bf16 v[122:125], v[142:145], v[166:169], v[122:125]
	v_mfma_f32_16x16x32_bf16 v[118:121], v[134:137], v[174:177], v[118:121]
	v_mfma_f32_16x16x32_bf16 v[114:117], v[142:145], v[174:177], v[114:117]
	v_mfma_f32_16x16x32_bf16 v[110:113], v[134:137], v[182:185], v[110:113]
	v_mfma_f32_16x16x32_bf16 v[102:105], v[142:145], v[182:185], v[102:105]
	v_mfma_f32_16x16x32_bf16 v[94:97], v[134:137], v[190:193], v[94:97]
	v_mfma_f32_16x16x32_bf16 v[74:77], v[142:145], v[190:193], v[74:77]
	v_mfma_f32_16x16x32_bf16 v[106:109], v[146:149], v[162:165], v[106:109]
	v_mfma_f32_16x16x32_bf16 v[98:101], v[154:157], v[162:165], v[98:101]
	v_mfma_f32_16x16x32_bf16 v[90:93], v[146:149], v[170:173], v[90:93]
	v_mfma_f32_16x16x32_bf16 v[86:89], v[154:157], v[170:173], v[86:89]
	v_mfma_f32_16x16x32_bf16 v[82:85], v[146:149], v[178:181], v[82:85]
	v_mfma_f32_16x16x32_bf16 v[78:81], v[154:157], v[178:181], v[78:81]
	v_mfma_f32_16x16x32_bf16 v[70:73], v[146:149], v[186:189], v[70:73]
	v_mfma_f32_16x16x32_bf16 v[66:69], v[154:157], v[186:189], v[66:69]
	v_mfma_f32_16x16x32_bf16 v[106:109], v[150:153], v[166:169], v[106:109]
	v_mfma_f32_16x16x32_bf16 v[98:101], v[158:161], v[166:169], v[98:101]
	v_mfma_f32_16x16x32_bf16 v[90:93], v[150:153], v[174:177], v[90:93]
	v_mfma_f32_16x16x32_bf16 v[86:89], v[158:161], v[174:177], v[86:89]
	v_mfma_f32_16x16x32_bf16 v[82:85], v[150:153], v[182:185], v[82:85]
	v_mfma_f32_16x16x32_bf16 v[78:81], v[158:161], v[182:185], v[78:81]
	v_mfma_f32_16x16x32_bf16 v[70:73], v[150:153], v[190:193], v[70:73]
	v_mfma_f32_16x16x32_bf16 v[66:69], v[158:161], v[190:193], v[66:69]
	s_barrier
	s_add_i32 s26, s81, s35
	v_lshl_add_u64 v[214:215], v[208:209], 0, s[14:15]
	s_mov_b32 m0, s26
	ds_read_b128 v[162:165], v224 offset:49152
	ds_read_b128 v[166:169], v224 offset:50176
	ds_read_b128 v[170:173], v224 offset:51200
	ds_read_b128 v[174:177], v224 offset:52224
	ds_read_b128 v[178:181], v224 offset:53248
	ds_read_b128 v[182:185], v224 offset:54272
	ds_read_b128 v[186:189], v224 offset:55296
	ds_read_b128 v[190:193], v224 offset:56320
	global_load_lds_dwordx4 v[214:215], off
	v_lshl_add_u64 v[214:215], v[208:209], 0, s[16:17]
	s_add_i32 m0, s26, 0x2000
	s_add_i32 s26, s82, s35
	global_load_lds_dwordx4 v[214:215], off
	v_lshl_add_u64 v[214:215], v[208:209], 0, s[20:21]
	s_mov_b32 m0, s26
	v_lshl_add_u64 v[208:209], v[208:209], 0, s[22:23]
	global_load_lds_dwordx4 v[214:215], off
	s_add_i32 m0, s26, 0x2000
	s_nop 0
	global_load_lds_dwordx4 v[208:209], off
	v_lshl_add_u64 v[208:209], v[210:211], 0, s[18:19]
	s_mov_b32 m0, s67
	s_nop 0
	global_load_lds_dwordx4 v[208:209], off
	v_lshl_add_u64 v[208:209], v[212:213], 0, s[18:19]
	s_mov_b32 m0, s68
	s_nop 0
	global_load_lds_dwordx4 v[208:209], off
	s_waitcnt vmcnt(8) lgkmcnt(0)
	s_barrier
	v_mfma_f32_16x16x32_bf16 v[62:65], v[130:133], v[162:165], v[62:65]
	v_mfma_f32_16x16x32_bf16 v[58:61], v[138:141], v[162:165], v[58:61]
	v_mfma_f32_16x16x32_bf16 v[54:57], v[130:133], v[170:173], v[54:57]
	v_mfma_f32_16x16x32_bf16 v[50:53], v[138:141], v[170:173], v[50:53]
	v_mfma_f32_16x16x32_bf16 v[46:49], v[130:133], v[178:181], v[46:49]
	v_mfma_f32_16x16x32_bf16 v[38:41], v[138:141], v[178:181], v[38:41]
	v_mfma_f32_16x16x32_bf16 v[30:33], v[130:133], v[186:189], v[30:33]
	v_mfma_f32_16x16x32_bf16 v[10:13], v[138:141], v[186:189], v[10:13]
	v_mfma_f32_16x16x32_bf16 v[62:65], v[134:137], v[166:169], v[62:65]
	v_mfma_f32_16x16x32_bf16 v[58:61], v[142:145], v[166:169], v[58:61]
	v_mfma_f32_16x16x32_bf16 v[54:57], v[134:137], v[174:177], v[54:57]
	v_mfma_f32_16x16x32_bf16 v[50:53], v[142:145], v[174:177], v[50:53]
	v_mfma_f32_16x16x32_bf16 v[46:49], v[134:137], v[182:185], v[46:49]
	v_mfma_f32_16x16x32_bf16 v[38:41], v[142:145], v[182:185], v[38:41]
	v_mfma_f32_16x16x32_bf16 v[30:33], v[134:137], v[190:193], v[30:33]
	v_mfma_f32_16x16x32_bf16 v[10:13], v[142:145], v[190:193], v[10:13]
	v_mfma_f32_16x16x32_bf16 v[42:45], v[146:149], v[162:165], v[42:45]
	v_mfma_f32_16x16x32_bf16 v[34:37], v[154:157], v[162:165], v[34:37]
	v_mfma_f32_16x16x32_bf16 v[26:29], v[146:149], v[170:173], v[26:29]
	v_mfma_f32_16x16x32_bf16 v[22:25], v[154:157], v[170:173], v[22:25]
	v_mfma_f32_16x16x32_bf16 v[18:21], v[146:149], v[178:181], v[18:21]
	v_mfma_f32_16x16x32_bf16 v[14:17], v[154:157], v[178:181], v[14:17]
	v_mfma_f32_16x16x32_bf16 v[6:9], v[146:149], v[186:189], v[6:9]
	v_mfma_f32_16x16x32_bf16 v[2:5], v[154:157], v[186:189], v[2:5]
	v_mfma_f32_16x16x32_bf16 v[42:45], v[150:153], v[166:169], v[42:45]
	v_mfma_f32_16x16x32_bf16 v[34:37], v[158:161], v[166:169], v[34:37]
	v_mfma_f32_16x16x32_bf16 v[26:29], v[150:153], v[174:177], v[26:29]
	v_mfma_f32_16x16x32_bf16 v[22:25], v[158:161], v[174:177], v[22:25]
	v_mfma_f32_16x16x32_bf16 v[18:21], v[150:153], v[182:185], v[18:21]
	v_mfma_f32_16x16x32_bf16 v[14:17], v[158:161], v[182:185], v[14:17]
	v_mfma_f32_16x16x32_bf16 v[6:9], v[150:153], v[190:193], v[6:9]
	v_mfma_f32_16x16x32_bf16 v[2:5], v[158:161], v[190:193], v[2:5]
	s_barrier
	s_add_i32 s80, s80, 2
	s_add_u32 s74, s74, 0x10000
	s_addc_u32 s75, s75, 0
	s_add_u32 s58, s58, 0x100
	s_addc_u32 s59, s59, 0
	s_cmp_gt_u32 s80, 29
	s_cbranch_scc0 .LBB0_660
	s_and_b64 vcc, exec, s[24:25]
	s_cbranch_vccz .LBB0_663
	s_barrier

.LBB0_782:
	s_ashr_i32 s55, s54, 31
	s_lshl_b64 s[26:27], s[54:55], 20
	v_readlane_b32 s56, v254, 56
	v_readlane_b32 s57, v254, 57
	s_add_u32 s56, s56, s26
	s_addc_u32 s57, s57, s27
	s_and_b64 s[26:27], s[0:1], exec
	s_cselect_b32 s55, s57, s65
	s_cselect_b32 s81, s56, s64
	s_ashr_i32 s53, s52, 31
	s_lshl_b64 s[26:27], s[52:53], 20
	s_add_u32 s58, s3, s26
	s_addc_u32 s59, s33, s27
	s_and_b64 s[26:27], s[0:1], exec
	s_cselect_b32 s53, s59, s63
	s_cselect_b32 s82, s58, s62
	s_add_u32 s83, s62, 0x10000
	s_addc_u32 s84, s63, 0
	s_add_u32 s62, s64, 0x80080
	s_addc_u32 s63, s65, 0
	s_mov_b32 s85, -2
	ds_read_b128 v[144:147], v151
	ds_read_b128 v[156:159], v151 offset:1024
	ds_read_b128 v[160:163], v151 offset:2048
	ds_read_b128 v[164:167], v151 offset:3072
	ds_read_b128 v[168:171], v152
	ds_read_b128 v[172:175], v152 offset:1024
	ds_read_b128 v[176:179], v152 offset:2048
	ds_read_b128 v[180:183], v152 offset:3072
	s_add_u32 s26, s62, 0xfff80080
	s_addc_u32 s27, s63, -1
	s_cmp_eq_u32 s85, 28
	s_cselect_b32 s65, s55, s27
	s_cselect_b32 s64, s81, s26
	s_cselect_b32 s27, s53, s84
	s_cselect_b32 s26, s82, s83
	v_lshl_add_u64 v[216:217], s[62:63], 0, v[136:137]
	s_add_i32 m0, s61, 0xc000
	ds_read_b128 v[184:187], v153
	ds_read_b128 v[188:191], v153 offset:1024
	ds_read_b128 v[192:195], v153 offset:2048
	ds_read_b128 v[196:199], v153 offset:3072
	ds_read_b128 v[200:203], v153 offset:4096
	ds_read_b128 v[204:207], v153 offset:5120
	ds_read_b128 v[208:211], v153 offset:6144
	ds_read_b128 v[212:215], v153 offset:7168
	global_load_lds_dwordx4 v[216:217], off
	v_lshl_add_u64 v[216:217], s[62:63], 0, v[138:139]
	s_add_i32 m0, s61, 0xe000
	s_nop 0
	global_load_lds_dwordx4 v[216:217], off
	s_waitcnt vmcnt(16) lgkmcnt(0)
	s_barrier
	v_mfma_f32_16x16x32_bf16 v[126:129], v[144:147], v[184:187], 0
	v_mfma_f32_16x16x32_bf16 v[118:121], v[160:163], v[184:187], 0
	v_mfma_f32_16x16x32_bf16 v[110:113], v[144:147], v[192:195], 0
	v_mfma_f32_16x16x32_bf16 v[102:105], v[160:163], v[192:195], 0
	v_mfma_f32_16x16x32_bf16 v[94:97], v[144:147], v[200:203], 0
	v_mfma_f32_16x16x32_bf16 v[86:89], v[160:163], v[200:203], 0
	v_mfma_f32_16x16x32_bf16 v[78:81], v[144:147], v[208:211], 0
	v_mfma_f32_16x16x32_bf16 v[70:73], v[160:163], v[208:211], 0
	v_mfma_f32_16x16x32_bf16 v[126:129], v[156:159], v[188:191], v[126:129]
	v_mfma_f32_16x16x32_bf16 v[118:121], v[164:167], v[188:191], v[118:121]
	v_mfma_f32_16x16x32_bf16 v[110:113], v[156:159], v[196:199], v[110:113]
	v_mfma_f32_16x16x32_bf16 v[102:105], v[164:167], v[196:199], v[102:105]
	v_mfma_f32_16x16x32_bf16 v[94:97], v[156:159], v[204:207], v[94:97]
	v_mfma_f32_16x16x32_bf16 v[86:89], v[164:167], v[204:207], v[86:89]
	v_mfma_f32_16x16x32_bf16 v[78:81], v[156:159], v[212:215], v[78:81]
	v_mfma_f32_16x16x32_bf16 v[70:73], v[164:167], v[212:215], v[70:73]
	v_mfma_f32_16x16x32_bf16 v[122:125], v[168:171], v[184:187], 0
	v_mfma_f32_16x16x32_bf16 v[114:117], v[176:179], v[184:187], 0
	v_mfma_f32_16x16x32_bf16 v[106:109], v[168:171], v[192:195], 0
	v_mfma_f32_16x16x32_bf16 v[98:101], v[176:179], v[192:195], 0
	v_mfma_f32_16x16x32_bf16 v[90:93], v[168:171], v[200:203], 0
	v_mfma_f32_16x16x32_bf16 v[82:85], v[176:179], v[200:203], 0
	v_mfma_f32_16x16x32_bf16 v[74:77], v[168:171], v[208:211], 0
	v_mfma_f32_16x16x32_bf16 v[66:69], v[176:179], v[208:211], 0
	v_mfma_f32_16x16x32_bf16 v[122:125], v[172:175], v[188:191], v[122:125]
	v_mfma_f32_16x16x32_bf16 v[114:117], v[180:183], v[188:191], v[114:117]
	v_mfma_f32_16x16x32_bf16 v[106:109], v[172:175], v[196:199], v[106:109]
	v_mfma_f32_16x16x32_bf16 v[98:101], v[180:183], v[196:199], v[98:101]
	v_mfma_f32_16x16x32_bf16 v[90:93], v[172:175], v[204:207], v[90:93]
	v_mfma_f32_16x16x32_bf16 v[82:85], v[180:183], v[204:207], v[82:85]
	v_mfma_f32_16x16x32_bf16 v[74:77], v[172:175], v[212:215], v[74:77]
	v_mfma_f32_16x16x32_bf16 v[66:69], v[180:183], v[212:215], v[66:69]
	s_barrier
	v_lshl_add_u64 v[216:217], s[26:27], 0, v[130:131]
	s_add_i32 s26, s73, s35
	s_mov_b32 m0, s26
	ds_read_b128 v[184:187], v153 offset:16384
	ds_read_b128 v[188:191], v153 offset:17408
	ds_read_b128 v[192:195], v153 offset:18432
	ds_read_b128 v[196:199], v153 offset:19456
	ds_read_b128 v[200:203], v153 offset:20480
	ds_read_b128 v[204:207], v153 offset:21504
	ds_read_b128 v[208:211], v153 offset:22528
	ds_read_b128 v[212:215], v153 offset:23552
	global_load_lds_dwordx4 v[216:217], off
	v_lshl_add_u64 v[220:221], v[216:217], 0, s[6:7]
	s_add_i32 m0, s26, 0x2000
	s_add_i32 s26, s74, s35
	global_load_lds_dwordx4 v[220:221], off
	v_lshl_add_u64 v[220:221], v[216:217], 0, s[8:9]
	s_mov_b32 m0, s26
	v_lshl_add_u64 v[222:223], s[64:65], 0, v[134:135]
	global_load_lds_dwordx4 v[220:221], off
	v_lshl_add_u64 v[220:221], v[216:217], 0, s[10:11]
	s_add_i32 m0, s26, 0x2000
	s_nop 0
	global_load_lds_dwordx4 v[220:221], off
	v_lshl_add_u64 v[220:221], s[64:65], 0, v[132:133]
	s_mov_b32 m0, s61
	s_nop 0
	global_load_lds_dwordx4 v[220:221], off
	s_mov_b32 m0, s66
	s_nop 0
	global_load_lds_dwordx4 v[222:223], off
	s_waitcnt vmcnt(16) lgkmcnt(0)
	s_barrier
	v_mfma_f32_16x16x32_bf16 v[62:65], v[144:147], v[184:187], 0
	v_mfma_f32_16x16x32_bf16 v[54:57], v[160:163], v[184:187], 0
	v_mfma_f32_16x16x32_bf16 v[46:49], v[144:147], v[192:195], 0
	v_mfma_f32_16x16x32_bf16 v[38:41], v[160:163], v[192:195], 0
	v_mfma_f32_16x16x32_bf16 v[30:33], v[144:147], v[200:203], 0
	v_mfma_f32_16x16x32_bf16 v[22:25], v[160:163], v[200:203], 0
	v_mfma_f32_16x16x32_bf16 v[14:17], v[144:147], v[208:211], 0
	v_mfma_f32_16x16x32_bf16 v[6:9], v[160:163], v[208:211], 0
	v_mfma_f32_16x16x32_bf16 v[62:65], v[156:159], v[188:191], v[62:65]
	v_mfma_f32_16x16x32_bf16 v[54:57], v[164:167], v[188:191], v[54:57]
	v_mfma_f32_16x16x32_bf16 v[46:49], v[156:159], v[196:199], v[46:49]
	v_mfma_f32_16x16x32_bf16 v[38:41], v[164:167], v[196:199], v[38:41]
	v_mfma_f32_16x16x32_bf16 v[30:33], v[156:159], v[204:207], v[30:33]
	v_mfma_f32_16x16x32_bf16 v[22:25], v[164:167], v[204:207], v[22:25]
	v_mfma_f32_16x16x32_bf16 v[14:17], v[156:159], v[212:215], v[14:17]
	v_mfma_f32_16x16x32_bf16 v[6:9], v[164:167], v[212:215], v[6:9]
	v_mfma_f32_16x16x32_bf16 v[58:61], v[168:171], v[184:187], 0
	v_mfma_f32_16x16x32_bf16 v[50:53], v[176:179], v[184:187], 0
	v_mfma_f32_16x16x32_bf16 v[42:45], v[168:171], v[192:195], 0
	v_mfma_f32_16x16x32_bf16 v[34:37], v[176:179], v[192:195], 0
	v_mfma_f32_16x16x32_bf16 v[26:29], v[168:171], v[200:203], 0
	v_mfma_f32_16x16x32_bf16 v[18:21], v[176:179], v[200:203], 0
	v_mfma_f32_16x16x32_bf16 v[10:13], v[168:171], v[208:211], 0
	v_mfma_f32_16x16x32_bf16 v[2:5], v[176:179], v[208:211], 0
	v_mfma_f32_16x16x32_bf16 v[58:61], v[172:175], v[188:191], v[58:61]
	v_mfma_f32_16x16x32_bf16 v[50:53], v[180:183], v[188:191], v[50:53]
	v_mfma_f32_16x16x32_bf16 v[42:45], v[172:175], v[196:199], v[42:45]
	v_mfma_f32_16x16x32_bf16 v[34:37], v[180:183], v[196:199], v[34:37]
	v_mfma_f32_16x16x32_bf16 v[26:29], v[172:175], v[204:207], v[26:29]
	v_mfma_f32_16x16x32_bf16 v[18:21], v[180:183], v[204:207], v[18:21]
	v_mfma_f32_16x16x32_bf16 v[10:13], v[172:175], v[212:215], v[10:13]
	v_mfma_f32_16x16x32_bf16 v[2:5], v[180:183], v[212:215], v[2:5]
	s_barrier
	s_add_i32 s86, 0, 0x18000
	v_add_u32_e32 v155, s86, v149
	s_add_i32 s87, 0, 0x1c000
	ds_read_b128 v[144:147], v155
	ds_read_b128 v[156:159], v155 offset:1024
	ds_read_b128 v[160:163], v155 offset:2048
	ds_read_b128 v[164:167], v155 offset:3072
	v_add_u32_e32 v155, s87, v149
	ds_read_b128 v[168:171], v155
	ds_read_b128 v[172:175], v155 offset:1024
	ds_read_b128 v[176:179], v155 offset:2048
	ds_read_b128 v[180:183], v155 offset:3072
	s_add_u32 s26, s64, 0x80000
	s_addc_u32 s27, s65, 0
	s_mov_b32 m0, s67
	v_lshl_add_u64 v[224:225], s[26:27], 0, v[132:133]
	ds_read_b128 v[184:187], v153 offset:32768
	ds_read_b128 v[188:191], v153 offset:33792
	ds_read_b128 v[192:195], v153 offset:34816
	ds_read_b128 v[196:199], v153 offset:35840
	ds_read_b128 v[200:203], v153 offset:36864
	ds_read_b128 v[204:207], v153 offset:37888
	ds_read_b128 v[208:211], v153 offset:38912
	ds_read_b128 v[212:215], v153 offset:39936
	global_load_lds_dwordx4 v[224:225], off
	v_lshl_add_u64 v[224:225], s[26:27], 0, v[134:135]
	s_mov_b32 m0, s68
	s_nop 0
	global_load_lds_dwordx4 v[224:225], off
	s_waitcnt vmcnt(8) lgkmcnt(0)
	s_barrier
	v_mfma_f32_16x16x32_bf16 v[126:129], v[144:147], v[184:187], v[126:129]
	v_mfma_f32_16x16x32_bf16 v[118:121], v[160:163], v[184:187], v[118:121]
	v_mfma_f32_16x16x32_bf16 v[110:113], v[144:147], v[192:195], v[110:113]
	v_mfma_f32_16x16x32_bf16 v[102:105], v[160:163], v[192:195], v[102:105]
	v_mfma_f32_16x16x32_bf16 v[94:97], v[144:147], v[200:203], v[94:97]
	v_mfma_f32_16x16x32_bf16 v[86:89], v[160:163], v[200:203], v[86:89]
	v_mfma_f32_16x16x32_bf16 v[78:81], v[144:147], v[208:211], v[78:81]
	v_mfma_f32_16x16x32_bf16 v[70:73], v[160:163], v[208:211], v[70:73]
	v_mfma_f32_16x16x32_bf16 v[126:129], v[156:159], v[188:191], v[126:129]
	v_mfma_f32_16x16x32_bf16 v[118:121], v[164:167], v[188:191], v[118:121]
	v_mfma_f32_16x16x32_bf16 v[110:113], v[156:159], v[196:199], v[110:113]
	v_mfma_f32_16x16x32_bf16 v[102:105], v[164:167], v[196:199], v[102:105]
	v_mfma_f32_16x16x32_bf16 v[94:97], v[156:159], v[204:207], v[94:97]
	v_mfma_f32_16x16x32_bf16 v[86:89], v[164:167], v[204:207], v[86:89]
	v_mfma_f32_16x16x32_bf16 v[78:81], v[156:159], v[212:215], v[78:81]
	v_mfma_f32_16x16x32_bf16 v[70:73], v[164:167], v[212:215], v[70:73]
	v_mfma_f32_16x16x32_bf16 v[122:125], v[168:171], v[184:187], v[122:125]
	v_mfma_f32_16x16x32_bf16 v[114:117], v[176:179], v[184:187], v[114:117]
	v_mfma_f32_16x16x32_bf16 v[106:109], v[168:171], v[192:195], v[106:109]
	v_mfma_f32_16x16x32_bf16 v[98:101], v[176:179], v[192:195], v[98:101]
	v_mfma_f32_16x16x32_bf16 v[90:93], v[168:171], v[200:203], v[90:93]
	v_mfma_f32_16x16x32_bf16 v[82:85], v[176:179], v[200:203], v[82:85]
	v_mfma_f32_16x16x32_bf16 v[74:77], v[168:171], v[208:211], v[74:77]
	v_mfma_f32_16x16x32_bf16 v[66:69], v[176:179], v[208:211], v[66:69]
	v_mfma_f32_16x16x32_bf16 v[122:125], v[172:175], v[188:191], v[122:125]
	v_mfma_f32_16x16x32_bf16 v[114:117], v[180:183], v[188:191], v[114:117]
	v_mfma_f32_16x16x32_bf16 v[106:109], v[172:175], v[196:199], v[106:109]
	v_mfma_f32_16x16x32_bf16 v[98:101], v[180:183], v[196:199], v[98:101]
	v_mfma_f32_16x16x32_bf16 v[90:93], v[172:175], v[204:207], v[90:93]
	v_mfma_f32_16x16x32_bf16 v[82:85], v[180:183], v[204:207], v[82:85]
	v_mfma_f32_16x16x32_bf16 v[74:77], v[172:175], v[212:215], v[74:77]
	v_mfma_f32_16x16x32_bf16 v[66:69], v[180:183], v[212:215], v[66:69]
	s_barrier
	s_add_i32 s26, s86, s35
	v_lshl_add_u64 v[224:225], v[216:217], 0, s[16:17]
	s_mov_b32 m0, s26
	ds_read_b128 v[184:187], v153 offset:49152
	ds_read_b128 v[188:191], v153 offset:50176
	ds_read_b128 v[192:195], v153 offset:51200
	ds_read_b128 v[196:199], v153 offset:52224
	ds_read_b128 v[200:203], v153 offset:53248
	ds_read_b128 v[204:207], v153 offset:54272
	ds_read_b128 v[208:211], v153 offset:55296
	ds_read_b128 v[212:215], v153 offset:56320
	global_load_lds_dwordx4 v[224:225], off
	v_lshl_add_u64 v[224:225], v[216:217], 0, s[18:19]
	s_add_i32 m0, s26, 0x2000
	s_add_i32 s26, s87, s35
	global_load_lds_dwordx4 v[224:225], off
	v_lshl_add_u64 v[224:225], v[216:217], 0, s[22:23]
	s_mov_b32 m0, s26
	v_lshl_add_u64 v[216:217], v[216:217], 0, s[24:25]
	global_load_lds_dwordx4 v[224:225], off
	s_add_i32 m0, s26, 0x2000
	s_nop 0
	global_load_lds_dwordx4 v[216:217], off
	v_lshl_add_u64 v[216:217], v[220:221], 0, s[20:21]
	s_mov_b32 m0, s70
	s_nop 0
	global_load_lds_dwordx4 v[216:217], off
	v_lshl_add_u64 v[216:217], v[222:223], 0, s[20:21]
	s_mov_b32 m0, s71
	s_nop 0
	global_load_lds_dwordx4 v[216:217], off
	s_waitcnt vmcnt(8) lgkmcnt(0)
	s_barrier
	v_mfma_f32_16x16x32_bf16 v[62:65], v[144:147], v[184:187], v[62:65]
	v_mfma_f32_16x16x32_bf16 v[54:57], v[160:163], v[184:187], v[54:57]
	v_mfma_f32_16x16x32_bf16 v[46:49], v[144:147], v[192:195], v[46:49]
	v_mfma_f32_16x16x32_bf16 v[38:41], v[160:163], v[192:195], v[38:41]
	v_mfma_f32_16x16x32_bf16 v[30:33], v[144:147], v[200:203], v[30:33]
	v_mfma_f32_16x16x32_bf16 v[22:25], v[160:163], v[200:203], v[22:25]
	v_mfma_f32_16x16x32_bf16 v[14:17], v[144:147], v[208:211], v[14:17]
	v_mfma_f32_16x16x32_bf16 v[6:9], v[160:163], v[208:211], v[6:9]
	v_mfma_f32_16x16x32_bf16 v[62:65], v[156:159], v[188:191], v[62:65]
	v_mfma_f32_16x16x32_bf16 v[54:57], v[164:167], v[188:191], v[54:57]
	v_mfma_f32_16x16x32_bf16 v[46:49], v[156:159], v[196:199], v[46:49]
	v_mfma_f32_16x16x32_bf16 v[38:41], v[164:167], v[196:199], v[38:41]
	v_mfma_f32_16x16x32_bf16 v[30:33], v[156:159], v[204:207], v[30:33]
	v_mfma_f32_16x16x32_bf16 v[22:25], v[164:167], v[204:207], v[22:25]
	v_mfma_f32_16x16x32_bf16 v[14:17], v[156:159], v[212:215], v[14:17]
	v_mfma_f32_16x16x32_bf16 v[6:9], v[164:167], v[212:215], v[6:9]
	v_mfma_f32_16x16x32_bf16 v[58:61], v[168:171], v[184:187], v[58:61]
	v_mfma_f32_16x16x32_bf16 v[50:53], v[176:179], v[184:187], v[50:53]
	v_mfma_f32_16x16x32_bf16 v[42:45], v[168:171], v[192:195], v[42:45]
	v_mfma_f32_16x16x32_bf16 v[34:37], v[176:179], v[192:195], v[34:37]
	v_mfma_f32_16x16x32_bf16 v[26:29], v[168:171], v[200:203], v[26:29]
	v_mfma_f32_16x16x32_bf16 v[18:21], v[176:179], v[200:203], v[18:21]
	v_mfma_f32_16x16x32_bf16 v[10:13], v[168:171], v[208:211], v[10:13]
	v_mfma_f32_16x16x32_bf16 v[2:5], v[176:179], v[208:211], v[2:5]
	v_mfma_f32_16x16x32_bf16 v[58:61], v[172:175], v[188:191], v[58:61]
	v_mfma_f32_16x16x32_bf16 v[50:53], v[180:183], v[188:191], v[50:53]
	v_mfma_f32_16x16x32_bf16 v[42:45], v[172:175], v[196:199], v[42:45]
	v_mfma_f32_16x16x32_bf16 v[34:37], v[180:183], v[196:199], v[34:37]
	v_mfma_f32_16x16x32_bf16 v[26:29], v[172:175], v[204:207], v[26:29]
	v_mfma_f32_16x16x32_bf16 v[18:21], v[180:183], v[204:207], v[18:21]
	v_mfma_f32_16x16x32_bf16 v[10:13], v[172:175], v[212:215], v[10:13]
	v_mfma_f32_16x16x32_bf16 v[2:5], v[180:183], v[212:215], v[2:5]
	s_barrier
	s_add_i32 s85, s85, 2
	s_add_u32 s83, s83, 0x10000
	s_addc_u32 s84, s84, 0
	s_add_u32 s62, s62, 0x100
	s_addc_u32 s63, s63, 0
	s_cmp_gt_u32 s85, 29
.LBB0_783:
	ds_read_b128 v[144:147], v151
	ds_read_b128 v[156:159], v151 offset:1024
	ds_read_b128 v[160:163], v151 offset:2048
	ds_read_b128 v[164:167], v151 offset:3072
	ds_read_b128 v[168:171], v152
	ds_read_b128 v[172:175], v152 offset:1024
	ds_read_b128 v[176:179], v152 offset:2048
	ds_read_b128 v[180:183], v152 offset:3072
	s_add_u32 s26, s62, 0xfff80080
	s_addc_u32 s27, s63, -1
	s_cmp_eq_u32 s85, 28
	s_cselect_b32 s65, s55, s27
	s_cselect_b32 s64, s81, s26
	s_cselect_b32 s27, s53, s84
	s_cselect_b32 s26, s82, s83
	v_lshl_add_u64 v[216:217], s[62:63], 0, v[136:137]
	s_add_i32 m0, s61, 0xc000
	ds_read_b128 v[184:187], v153
	ds_read_b128 v[188:191], v153 offset:1024
	ds_read_b128 v[192:195], v153 offset:2048
	ds_read_b128 v[196:199], v153 offset:3072
	ds_read_b128 v[200:203], v153 offset:4096
	ds_read_b128 v[204:207], v153 offset:5120
	ds_read_b128 v[208:211], v153 offset:6144
	ds_read_b128 v[212:215], v153 offset:7168
	global_load_lds_dwordx4 v[216:217], off
	v_lshl_add_u64 v[216:217], s[62:63], 0, v[138:139]
	s_add_i32 m0, s61, 0xe000
	s_nop 0
	global_load_lds_dwordx4 v[216:217], off
	s_waitcnt vmcnt(8) lgkmcnt(0)
	s_barrier
	v_mfma_f32_16x16x32_bf16 v[126:129], v[144:147], v[184:187], v[126:129]
	v_mfma_f32_16x16x32_bf16 v[118:121], v[160:163], v[184:187], v[118:121]
	v_mfma_f32_16x16x32_bf16 v[110:113], v[144:147], v[192:195], v[110:113]
	v_mfma_f32_16x16x32_bf16 v[102:105], v[160:163], v[192:195], v[102:105]
	v_mfma_f32_16x16x32_bf16 v[94:97], v[144:147], v[200:203], v[94:97]
	v_mfma_f32_16x16x32_bf16 v[86:89], v[160:163], v[200:203], v[86:89]
	v_mfma_f32_16x16x32_bf16 v[78:81], v[144:147], v[208:211], v[78:81]
	v_mfma_f32_16x16x32_bf16 v[70:73], v[160:163], v[208:211], v[70:73]
	v_mfma_f32_16x16x32_bf16 v[126:129], v[156:159], v[188:191], v[126:129]
	v_mfma_f32_16x16x32_bf16 v[118:121], v[164:167], v[188:191], v[118:121]
	v_mfma_f32_16x16x32_bf16 v[110:113], v[156:159], v[196:199], v[110:113]
	v_mfma_f32_16x16x32_bf16 v[102:105], v[164:167], v[196:199], v[102:105]
	v_mfma_f32_16x16x32_bf16 v[94:97], v[156:159], v[204:207], v[94:97]
	v_mfma_f32_16x16x32_bf16 v[86:89], v[164:167], v[204:207], v[86:89]
	v_mfma_f32_16x16x32_bf16 v[78:81], v[156:159], v[212:215], v[78:81]
	v_mfma_f32_16x16x32_bf16 v[70:73], v[164:167], v[212:215], v[70:73]
	v_mfma_f32_16x16x32_bf16 v[122:125], v[168:171], v[184:187], v[122:125]
	v_mfma_f32_16x16x32_bf16 v[114:117], v[176:179], v[184:187], v[114:117]
	v_mfma_f32_16x16x32_bf16 v[106:109], v[168:171], v[192:195], v[106:109]
	v_mfma_f32_16x16x32_bf16 v[98:101], v[176:179], v[192:195], v[98:101]
	v_mfma_f32_16x16x32_bf16 v[90:93], v[168:171], v[200:203], v[90:93]
	v_mfma_f32_16x16x32_bf16 v[82:85], v[176:179], v[200:203], v[82:85]
	v_mfma_f32_16x16x32_bf16 v[74:77], v[168:171], v[208:211], v[74:77]
	v_mfma_f32_16x16x32_bf16 v[66:69], v[176:179], v[208:211], v[66:69]
	v_mfma_f32_16x16x32_bf16 v[122:125], v[172:175], v[188:191], v[122:125]
	v_mfma_f32_16x16x32_bf16 v[114:117], v[180:183], v[188:191], v[114:117]
	v_mfma_f32_16x16x32_bf16 v[106:109], v[172:175], v[196:199], v[106:109]
	v_mfma_f32_16x16x32_bf16 v[98:101], v[180:183], v[196:199], v[98:101]
	v_mfma_f32_16x16x32_bf16 v[90:93], v[172:175], v[204:207], v[90:93]
	v_mfma_f32_16x16x32_bf16 v[82:85], v[180:183], v[204:207], v[82:85]
	v_mfma_f32_16x16x32_bf16 v[74:77], v[172:175], v[212:215], v[74:77]
	v_mfma_f32_16x16x32_bf16 v[66:69], v[180:183], v[212:215], v[66:69]
	s_barrier
	v_lshl_add_u64 v[216:217], s[26:27], 0, v[130:131]
	s_add_i32 s26, s73, s35
	s_mov_b32 m0, s26
	ds_read_b128 v[184:187], v153 offset:16384
	ds_read_b128 v[188:191], v153 offset:17408
	ds_read_b128 v[192:195], v153 offset:18432
	ds_read_b128 v[196:199], v153 offset:19456
	ds_read_b128 v[200:203], v153 offset:20480
	ds_read_b128 v[204:207], v153 offset:21504
	ds_read_b128 v[208:211], v153 offset:22528
	ds_read_b128 v[212:215], v153 offset:23552
	global_load_lds_dwordx4 v[216:217], off
	v_lshl_add_u64 v[220:221], v[216:217], 0, s[6:7]
	s_add_i32 m0, s26, 0x2000
	s_add_i32 s26, s74, s35
	global_load_lds_dwordx4 v[220:221], off
	v_lshl_add_u64 v[220:221], v[216:217], 0, s[8:9]
	s_mov_b32 m0, s26
	v_lshl_add_u64 v[222:223], s[64:65], 0, v[134:135]
	global_load_lds_dwordx4 v[220:221], off
	v_lshl_add_u64 v[220:221], v[216:217], 0, s[10:11]
	s_add_i32 m0, s26, 0x2000
	s_nop 0
	global_load_lds_dwordx4 v[220:221], off
	v_lshl_add_u64 v[220:221], s[64:65], 0, v[132:133]
	s_mov_b32 m0, s61
	s_nop 0
	global_load_lds_dwordx4 v[220:221], off
	s_mov_b32 m0, s66
	s_nop 0
	global_load_lds_dwordx4 v[222:223], off
	s_waitcnt vmcnt(8) lgkmcnt(0)
	s_barrier
	v_mfma_f32_16x16x32_bf16 v[62:65], v[144:147], v[184:187], v[62:65]
	v_mfma_f32_16x16x32_bf16 v[54:57], v[160:163], v[184:187], v[54:57]
	v_mfma_f32_16x16x32_bf16 v[46:49], v[144:147], v[192:195], v[46:49]
	v_mfma_f32_16x16x32_bf16 v[38:41], v[160:163], v[192:195], v[38:41]
	v_mfma_f32_16x16x32_bf16 v[30:33], v[144:147], v[200:203], v[30:33]
	v_mfma_f32_16x16x32_bf16 v[22:25], v[160:163], v[200:203], v[22:25]
	v_mfma_f32_16x16x32_bf16 v[14:17], v[144:147], v[208:211], v[14:17]
	v_mfma_f32_16x16x32_bf16 v[6:9], v[160:163], v[208:211], v[6:9]
	v_mfma_f32_16x16x32_bf16 v[62:65], v[156:159], v[188:191], v[62:65]
	v_mfma_f32_16x16x32_bf16 v[54:57], v[164:167], v[188:191], v[54:57]
	v_mfma_f32_16x16x32_bf16 v[46:49], v[156:159], v[196:199], v[46:49]
	v_mfma_f32_16x16x32_bf16 v[38:41], v[164:167], v[196:199], v[38:41]
	v_mfma_f32_16x16x32_bf16 v[30:33], v[156:159], v[204:207], v[30:33]
	v_mfma_f32_16x16x32_bf16 v[22:25], v[164:167], v[204:207], v[22:25]
	v_mfma_f32_16x16x32_bf16 v[14:17], v[156:159], v[212:215], v[14:17]
	v_mfma_f32_16x16x32_bf16 v[6:9], v[164:167], v[212:215], v[6:9]
	v_mfma_f32_16x16x32_bf16 v[58:61], v[168:171], v[184:187], v[58:61]
	v_mfma_f32_16x16x32_bf16 v[50:53], v[176:179], v[184:187], v[50:53]
	v_mfma_f32_16x16x32_bf16 v[42:45], v[168:171], v[192:195], v[42:45]
	v_mfma_f32_16x16x32_bf16 v[34:37], v[176:179], v[192:195], v[34:37]
	v_mfma_f32_16x16x32_bf16 v[26:29], v[168:171], v[200:203], v[26:29]
	v_mfma_f32_16x16x32_bf16 v[18:21], v[176:179], v[200:203], v[18:21]
	v_mfma_f32_16x16x32_bf16 v[10:13], v[168:171], v[208:211], v[10:13]
	v_mfma_f32_16x16x32_bf16 v[2:5], v[176:179], v[208:211], v[2:5]
	v_mfma_f32_16x16x32_bf16 v[58:61], v[172:175], v[188:191], v[58:61]
	v_mfma_f32_16x16x32_bf16 v[50:53], v[180:183], v[188:191], v[50:53]
	v_mfma_f32_16x16x32_bf16 v[42:45], v[172:175], v[196:199], v[42:45]
	v_mfma_f32_16x16x32_bf16 v[34:37], v[180:183], v[196:199], v[34:37]
	v_mfma_f32_16x16x32_bf16 v[26:29], v[172:175], v[204:207], v[26:29]
	v_mfma_f32_16x16x32_bf16 v[18:21], v[180:183], v[204:207], v[18:21]
	v_mfma_f32_16x16x32_bf16 v[10:13], v[172:175], v[212:215], v[10:13]
	v_mfma_f32_16x16x32_bf16 v[2:5], v[180:183], v[212:215], v[2:5]
	s_barrier
	s_add_i32 s86, 0, 0x18000
	v_add_u32_e32 v155, s86, v149
	s_add_i32 s87, 0, 0x1c000
	ds_read_b128 v[144:147], v155
	ds_read_b128 v[156:159], v155 offset:1024
	ds_read_b128 v[160:163], v155 offset:2048
	ds_read_b128 v[164:167], v155 offset:3072
	v_add_u32_e32 v155, s87, v149
	ds_read_b128 v[168:171], v155
	ds_read_b128 v[172:175], v155 offset:1024
	ds_read_b128 v[176:179], v155 offset:2048
	ds_read_b128 v[180:183], v155 offset:3072
	s_add_u32 s26, s64, 0x80000
	s_addc_u32 s27, s65, 0
	s_mov_b32 m0, s67
	v_lshl_add_u64 v[224:225], s[26:27], 0, v[132:133]
	ds_read_b128 v[184:187], v153 offset:32768
	ds_read_b128 v[188:191], v153 offset:33792
	ds_read_b128 v[192:195], v153 offset:34816
	ds_read_b128 v[196:199], v153 offset:35840
	ds_read_b128 v[200:203], v153 offset:36864
	ds_read_b128 v[204:207], v153 offset:37888
	ds_read_b128 v[208:211], v153 offset:38912
	ds_read_b128 v[212:215], v153 offset:39936
	global_load_lds_dwordx4 v[224:225], off
	v_lshl_add_u64 v[224:225], s[26:27], 0, v[134:135]
	s_mov_b32 m0, s68
	s_nop 0
	global_load_lds_dwordx4 v[224:225], off
	s_waitcnt vmcnt(8) lgkmcnt(0)
	s_barrier
	v_mfma_f32_16x16x32_bf16 v[126:129], v[144:147], v[184:187], v[126:129]
	v_mfma_f32_16x16x32_bf16 v[118:121], v[160:163], v[184:187], v[118:121]
	v_mfma_f32_16x16x32_bf16 v[110:113], v[144:147], v[192:195], v[110:113]
	v_mfma_f32_16x16x32_bf16 v[102:105], v[160:163], v[192:195], v[102:105]
	v_mfma_f32_16x16x32_bf16 v[94:97], v[144:147], v[200:203], v[94:97]
	v_mfma_f32_16x16x32_bf16 v[86:89], v[160:163], v[200:203], v[86:89]
	v_mfma_f32_16x16x32_bf16 v[78:81], v[144:147], v[208:211], v[78:81]
	v_mfma_f32_16x16x32_bf16 v[70:73], v[160:163], v[208:211], v[70:73]
	v_mfma_f32_16x16x32_bf16 v[126:129], v[156:159], v[188:191], v[126:129]
	v_mfma_f32_16x16x32_bf16 v[118:121], v[164:167], v[188:191], v[118:121]
	v_mfma_f32_16x16x32_bf16 v[110:113], v[156:159], v[196:199], v[110:113]
	v_mfma_f32_16x16x32_bf16 v[102:105], v[164:167], v[196:199], v[102:105]
	v_mfma_f32_16x16x32_bf16 v[94:97], v[156:159], v[204:207], v[94:97]
	v_mfma_f32_16x16x32_bf16 v[86:89], v[164:167], v[204:207], v[86:89]
	v_mfma_f32_16x16x32_bf16 v[78:81], v[156:159], v[212:215], v[78:81]
	v_mfma_f32_16x16x32_bf16 v[70:73], v[164:167], v[212:215], v[70:73]
	v_mfma_f32_16x16x32_bf16 v[122:125], v[168:171], v[184:187], v[122:125]
	v_mfma_f32_16x16x32_bf16 v[114:117], v[176:179], v[184:187], v[114:117]
	v_mfma_f32_16x16x32_bf16 v[106:109], v[168:171], v[192:195], v[106:109]
	v_mfma_f32_16x16x32_bf16 v[98:101], v[176:179], v[192:195], v[98:101]
	v_mfma_f32_16x16x32_bf16 v[90:93], v[168:171], v[200:203], v[90:93]
	v_mfma_f32_16x16x32_bf16 v[82:85], v[176:179], v[200:203], v[82:85]
	v_mfma_f32_16x16x32_bf16 v[74:77], v[168:171], v[208:211], v[74:77]
	v_mfma_f32_16x16x32_bf16 v[66:69], v[176:179], v[208:211], v[66:69]
	v_mfma_f32_16x16x32_bf16 v[122:125], v[172:175], v[188:191], v[122:125]
	v_mfma_f32_16x16x32_bf16 v[114:117], v[180:183], v[188:191], v[114:117]
	v_mfma_f32_16x16x32_bf16 v[106:109], v[172:175], v[196:199], v[106:109]
	v_mfma_f32_16x16x32_bf16 v[98:101], v[180:183], v[196:199], v[98:101]
	v_mfma_f32_16x16x32_bf16 v[90:93], v[172:175], v[204:207], v[90:93]
	v_mfma_f32_16x16x32_bf16 v[82:85], v[180:183], v[204:207], v[82:85]
	v_mfma_f32_16x16x32_bf16 v[74:77], v[172:175], v[212:215], v[74:77]
	v_mfma_f32_16x16x32_bf16 v[66:69], v[180:183], v[212:215], v[66:69]
	s_barrier
	s_add_i32 s26, s86, s35
	v_lshl_add_u64 v[224:225], v[216:217], 0, s[16:17]
	s_mov_b32 m0, s26
	ds_read_b128 v[184:187], v153 offset:49152
	ds_read_b128 v[188:191], v153 offset:50176
	ds_read_b128 v[192:195], v153 offset:51200
	ds_read_b128 v[196:199], v153 offset:52224
	ds_read_b128 v[200:203], v153 offset:53248
	ds_read_b128 v[204:207], v153 offset:54272
	ds_read_b128 v[208:211], v153 offset:55296
	ds_read_b128 v[212:215], v153 offset:56320
	global_load_lds_dwordx4 v[224:225], off
	v_lshl_add_u64 v[224:225], v[216:217], 0, s[18:19]
	s_add_i32 m0, s26, 0x2000
	s_add_i32 s26, s87, s35
	global_load_lds_dwordx4 v[224:225], off
	v_lshl_add_u64 v[224:225], v[216:217], 0, s[22:23]
	s_mov_b32 m0, s26
	v_lshl_add_u64 v[216:217], v[216:217], 0, s[24:25]
	global_load_lds_dwordx4 v[224:225], off
	s_add_i32 m0, s26, 0x2000
	s_nop 0
	global_load_lds_dwordx4 v[216:217], off
	v_lshl_add_u64 v[216:217], v[220:221], 0, s[20:21]
	s_mov_b32 m0, s70
	s_nop 0
	global_load_lds_dwordx4 v[216:217], off
	v_lshl_add_u64 v[216:217], v[222:223], 0, s[20:21]
	s_mov_b32 m0, s71
	s_nop 0
	global_load_lds_dwordx4 v[216:217], off
	s_waitcnt vmcnt(8) lgkmcnt(0)
	s_barrier
	v_mfma_f32_16x16x32_bf16 v[62:65], v[144:147], v[184:187], v[62:65]
	v_mfma_f32_16x16x32_bf16 v[54:57], v[160:163], v[184:187], v[54:57]
	v_mfma_f32_16x16x32_bf16 v[46:49], v[144:147], v[192:195], v[46:49]
	v_mfma_f32_16x16x32_bf16 v[38:41], v[160:163], v[192:195], v[38:41]
	v_mfma_f32_16x16x32_bf16 v[30:33], v[144:147], v[200:203], v[30:33]
	v_mfma_f32_16x16x32_bf16 v[22:25], v[160:163], v[200:203], v[22:25]
	v_mfma_f32_16x16x32_bf16 v[14:17], v[144:147], v[208:211], v[14:17]
	v_mfma_f32_16x16x32_bf16 v[6:9], v[160:163], v[208:211], v[6:9]
	v_mfma_f32_16x16x32_bf16 v[62:65], v[156:159], v[188:191], v[62:65]
	v_mfma_f32_16x16x32_bf16 v[54:57], v[164:167], v[188:191], v[54:57]
	v_mfma_f32_16x16x32_bf16 v[46:49], v[156:159], v[196:199], v[46:49]
	v_mfma_f32_16x16x32_bf16 v[38:41], v[164:167], v[196:199], v[38:41]
	v_mfma_f32_16x16x32_bf16 v[30:33], v[156:159], v[204:207], v[30:33]
	v_mfma_f32_16x16x32_bf16 v[22:25], v[164:167], v[204:207], v[22:25]
	v_mfma_f32_16x16x32_bf16 v[14:17], v[156:159], v[212:215], v[14:17]
	v_mfma_f32_16x16x32_bf16 v[6:9], v[164:167], v[212:215], v[6:9]
	v_mfma_f32_16x16x32_bf16 v[58:61], v[168:171], v[184:187], v[58:61]
	v_mfma_f32_16x16x32_bf16 v[50:53], v[176:179], v[184:187], v[50:53]
	v_mfma_f32_16x16x32_bf16 v[42:45], v[168:171], v[192:195], v[42:45]
	v_mfma_f32_16x16x32_bf16 v[34:37], v[176:179], v[192:195], v[34:37]
	v_mfma_f32_16x16x32_bf16 v[26:29], v[168:171], v[200:203], v[26:29]
	v_mfma_f32_16x16x32_bf16 v[18:21], v[176:179], v[200:203], v[18:21]
	v_mfma_f32_16x16x32_bf16 v[10:13], v[168:171], v[208:211], v[10:13]
	v_mfma_f32_16x16x32_bf16 v[2:5], v[176:179], v[208:211], v[2:5]
	v_mfma_f32_16x16x32_bf16 v[58:61], v[172:175], v[188:191], v[58:61]
	v_mfma_f32_16x16x32_bf16 v[50:53], v[180:183], v[188:191], v[50:53]
	v_mfma_f32_16x16x32_bf16 v[42:45], v[172:175], v[196:199], v[42:45]
	v_mfma_f32_16x16x32_bf16 v[34:37], v[180:183], v[196:199], v[34:37]
	v_mfma_f32_16x16x32_bf16 v[26:29], v[172:175], v[204:207], v[26:29]
	v_mfma_f32_16x16x32_bf16 v[18:21], v[180:183], v[204:207], v[18:21]
	v_mfma_f32_16x16x32_bf16 v[10:13], v[172:175], v[212:215], v[10:13]
	v_mfma_f32_16x16x32_bf16 v[2:5], v[180:183], v[212:215], v[2:5]
	s_barrier
	s_add_i32 s85, s85, 2
	s_add_u32 s83, s83, 0x10000
	s_addc_u32 s84, s84, 0
	s_add_u32 s62, s62, 0x100
	s_addc_u32 s63, s63, 0
	s_cmp_gt_u32 s85, 29
	s_cbranch_scc0 .LBB0_783
	s_and_b64 vcc, exec, s[40:41]
	s_cbranch_vccz .LBB0_786
	s_barrier

.LBB0_857:
	s_add_u32 s72, s50, 0x10000
	s_addc_u32 s73, s51, 0
	s_add_u32 s50, s52, 0xb0080
	s_addc_u32 s51, s53, 0
	s_mov_b32 s74, -2
	ds_read_b128 v[26:29], v185
	ds_read_b128 v[30:33], v185 offset:1024
	ds_read_b128 v[18:21], v185 offset:2048
	ds_read_b128 v[22:25], v185 offset:3072
	ds_read_b128 v[10:13], v186
	ds_read_b128 v[14:17], v186 offset:1024
	ds_read_b128 v[2:5], v186 offset:2048
	ds_read_b128 v[6:9], v186 offset:3072
	s_add_u32 s26, s50, 0xfff50080
	s_addc_u32 s27, s51, -1
	s_cmp_eq_u32 s74, 40
	s_cselect_b32 s53, s5, s27
	s_cselect_b32 s52, s4, s26
	s_cselect_b32 s55, s45, s73
	s_cselect_b32 s54, s44, s72
	v_lshl_add_u64 v[176:177], s[50:51], 0, v[168:169]
	s_add_i32 m0, s59, 0xc000
	ds_read_b128 v[190:193], v187
	ds_read_b128 v[194:197], v187 offset:1024
	ds_read_b128 v[198:201], v187 offset:2048
	ds_read_b128 v[202:205], v187 offset:3072
	ds_read_b128 v[206:209], v187 offset:4096
	ds_read_b128 v[210:213], v187 offset:5120
	ds_read_b128 v[220:223], v187 offset:6144
	ds_read_b128 v[224:227], v187 offset:7168
	global_load_lds_dwordx4 v[176:177], off
	v_lshl_add_u64 v[176:177], s[50:51], 0, v[170:171]
	s_add_i32 m0, s59, 0xe000
	s_nop 0
	global_load_lds_dwordx4 v[176:177], off
	s_waitcnt vmcnt(8) lgkmcnt(0)
	s_barrier
	v_mfma_scale_f32_16x16x128_f8f6f4 v[158:161], v[26:33], v[190:197], 0, v188, v189 op_sel_hi:[0,0,0]
	v_mfma_scale_f32_16x16x128_f8f6f4 v[154:157], v[18:25], v[190:197], 0, v188, v189 op_sel_hi:[0,0,0]
	v_mfma_scale_f32_16x16x128_f8f6f4 v[150:153], v[26:33], v[198:205], 0, v188, v189 op_sel_hi:[0,0,0]
	v_mfma_scale_f32_16x16x128_f8f6f4 v[146:149], v[18:25], v[198:205], 0, v188, v189 op_sel_hi:[0,0,0]
	v_mfma_scale_f32_16x16x128_f8f6f4 v[138:141], v[26:33], v[206:213], 0, v188, v189 op_sel_hi:[0,0,0]
	v_mfma_scale_f32_16x16x128_f8f6f4 v[130:133], v[18:25], v[206:213], 0, v188, v189 op_sel_hi:[0,0,0]
	v_mfma_scale_f32_16x16x128_f8f6f4 v[122:125], v[26:33], v[220:227], 0, v188, v189 op_sel_hi:[0,0,0]
	v_mfma_scale_f32_16x16x128_f8f6f4 v[114:117], v[18:25], v[220:227], 0, v188, v189 op_sel_hi:[0,0,0]
	v_mfma_scale_f32_16x16x128_f8f6f4 v[142:145], v[10:17], v[190:197], 0, v188, v189 op_sel_hi:[0,0,0]
	v_mfma_scale_f32_16x16x128_f8f6f4 v[134:137], v[2:9], v[190:197], 0, v188, v189 op_sel_hi:[0,0,0]
	v_mfma_scale_f32_16x16x128_f8f6f4 v[126:129], v[10:17], v[198:205], 0, v188, v189 op_sel_hi:[0,0,0]
	v_mfma_scale_f32_16x16x128_f8f6f4 v[118:121], v[2:9], v[198:205], 0, v188, v189 op_sel_hi:[0,0,0]
	v_mfma_scale_f32_16x16x128_f8f6f4 v[110:113], v[10:17], v[206:213], 0, v188, v189 op_sel_hi:[0,0,0]
	v_mfma_scale_f32_16x16x128_f8f6f4 v[106:109], v[2:9], v[206:213], 0, v188, v189 op_sel_hi:[0,0,0]
	v_mfma_scale_f32_16x16x128_f8f6f4 v[102:105], v[10:17], v[220:227], 0, v188, v189 op_sel_hi:[0,0,0]
	v_mfma_scale_f32_16x16x128_f8f6f4 v[98:101], v[2:9], v[220:227], 0, v188, v189 op_sel_hi:[0,0,0]
	s_barrier
	s_add_i32 s26, s67, s57
	v_lshl_add_u64 v[176:177], s[54:55], 0, v[162:163]
	s_mov_b32 m0, s26
	ds_read_b128 v[190:193], v187 offset:16384
	ds_read_b128 v[194:197], v187 offset:17408
	ds_read_b128 v[198:201], v187 offset:18432
	ds_read_b128 v[202:205], v187 offset:19456
	ds_read_b128 v[206:209], v187 offset:20480
	ds_read_b128 v[210:213], v187 offset:21504
	ds_read_b128 v[220:223], v187 offset:22528
	ds_read_b128 v[224:227], v187 offset:23552
	global_load_lds_dwordx4 v[176:177], off
	v_lshl_add_u64 v[178:179], v[176:177], 0, s[8:9]
	s_add_i32 m0, s26, 0x2000
	s_add_i32 s26, s68, s57
	global_load_lds_dwordx4 v[178:179], off
	v_lshl_add_u64 v[178:179], v[176:177], 0, s[10:11]
	s_mov_b32 m0, s26
	v_lshl_add_u64 v[180:181], s[52:53], 0, v[166:167]
	global_load_lds_dwordx4 v[178:179], off
	v_lshl_add_u64 v[178:179], v[176:177], 0, s[12:13]
	s_add_i32 m0, s26, 0x2000
	s_nop 0
	global_load_lds_dwordx4 v[178:179], off
	v_lshl_add_u64 v[178:179], s[52:53], 0, v[164:165]
	s_mov_b32 m0, s59
	s_nop 0
	global_load_lds_dwordx4 v[178:179], off
	s_mov_b32 m0, s60
	s_nop 0
	global_load_lds_dwordx4 v[180:181], off
	s_waitcnt vmcnt(8) lgkmcnt(0)
	s_barrier
	v_mfma_scale_f32_16x16x128_f8f6f4 v[94:97], v[26:33], v[190:197], 0, v188, v189 op_sel_hi:[0,0,0]
	v_mfma_scale_f32_16x16x128_f8f6f4 v[90:93], v[18:25], v[190:197], 0, v188, v189 op_sel_hi:[0,0,0]
	v_mfma_scale_f32_16x16x128_f8f6f4 v[86:89], v[26:33], v[198:205], 0, v188, v189 op_sel_hi:[0,0,0]
	v_mfma_scale_f32_16x16x128_f8f6f4 v[78:81], v[18:25], v[198:205], 0, v188, v189 op_sel_hi:[0,0,0]
	v_mfma_scale_f32_16x16x128_f8f6f4 v[70:73], v[26:33], v[206:213], 0, v188, v189 op_sel_hi:[0,0,0]
	v_mfma_scale_f32_16x16x128_f8f6f4 v[62:65], v[18:25], v[206:213], 0, v188, v189 op_sel_hi:[0,0,0]
	v_mfma_scale_f32_16x16x128_f8f6f4 v[54:57], v[26:33], v[220:227], 0, v188, v189 op_sel_hi:[0,0,0]
	v_mfma_scale_f32_16x16x128_f8f6f4 v[46:49], v[18:25], v[220:227], 0, v188, v189 op_sel_hi:[0,0,0]
	v_mfma_scale_f32_16x16x128_f8f6f4 v[82:85], v[10:17], v[190:197], 0, v188, v189 op_sel_hi:[0,0,0]
	v_mfma_scale_f32_16x16x128_f8f6f4 v[74:77], v[2:9], v[190:197], 0, v188, v189 op_sel_hi:[0,0,0]
	v_mfma_scale_f32_16x16x128_f8f6f4 v[66:69], v[10:17], v[198:205], 0, v188, v189 op_sel_hi:[0,0,0]
	v_mfma_scale_f32_16x16x128_f8f6f4 v[58:61], v[2:9], v[198:205], 0, v188, v189 op_sel_hi:[0,0,0]
	v_mfma_scale_f32_16x16x128_f8f6f4 v[50:53], v[10:17], v[206:213], 0, v188, v189 op_sel_hi:[0,0,0]
	v_mfma_scale_f32_16x16x128_f8f6f4 v[42:45], v[2:9], v[206:213], 0, v188, v189 op_sel_hi:[0,0,0]
	v_mfma_scale_f32_16x16x128_f8f6f4 v[38:41], v[10:17], v[220:227], 0, v188, v189 op_sel_hi:[0,0,0]
	v_mfma_scale_f32_16x16x128_f8f6f4 v[34:37], v[2:9], v[220:227], 0, v188, v189 op_sel_hi:[0,0,0]
	s_barrier
	s_add_i32 s54, 0, 0x18000
	s_add_i32 s55, 0, 0x1c000
	v_add_u32_e32 v14, s54, v183
	v_add_u32_e32 v30, s55, v183
	ds_read_b128 v[2:5], v14
	ds_read_b128 v[6:9], v14 offset:1024
	ds_read_b128 v[10:13], v14 offset:2048
	ds_read_b128 v[14:17], v14 offset:3072
	ds_read_b128 v[18:21], v30
	ds_read_b128 v[22:25], v30 offset:1024
	ds_read_b128 v[26:29], v30 offset:2048
	ds_read_b128 v[30:33], v30 offset:3072
	s_add_u32 s26, s52, 0xb0000
	s_addc_u32 s27, s53, 0
	s_mov_b32 m0, s61
	v_lshl_add_u64 v[214:215], s[26:27], 0, v[164:165]
	ds_read_b128 v[190:193], v187 offset:32768
	ds_read_b128 v[194:197], v187 offset:33792
	ds_read_b128 v[198:201], v187 offset:34816
	ds_read_b128 v[202:205], v187 offset:35840
	ds_read_b128 v[206:209], v187 offset:36864
	ds_read_b128 v[210:213], v187 offset:37888
	ds_read_b128 v[220:223], v187 offset:38912
	ds_read_b128 v[224:227], v187 offset:39936
	global_load_lds_dwordx4 v[214:215], off
	v_lshl_add_u64 v[214:215], s[26:27], 0, v[166:167]
	s_mov_b32 m0, s62
	s_nop 0
	global_load_lds_dwordx4 v[214:215], off
	s_waitcnt vmcnt(8) lgkmcnt(0)
	s_barrier
	v_mfma_scale_f32_16x16x128_f8f6f4 v[158:161], v[2:9], v[190:197], v[158:161], v188, v189 op_sel_hi:[0,0,0]
	v_mfma_scale_f32_16x16x128_f8f6f4 v[154:157], v[10:17], v[190:197], v[154:157], v188, v189 op_sel_hi:[0,0,0]
	v_mfma_scale_f32_16x16x128_f8f6f4 v[150:153], v[2:9], v[198:205], v[150:153], v188, v189 op_sel_hi:[0,0,0]
	v_mfma_scale_f32_16x16x128_f8f6f4 v[146:149], v[10:17], v[198:205], v[146:149], v188, v189 op_sel_hi:[0,0,0]
	v_mfma_scale_f32_16x16x128_f8f6f4 v[138:141], v[2:9], v[206:213], v[138:141], v188, v189 op_sel_hi:[0,0,0]
	v_mfma_scale_f32_16x16x128_f8f6f4 v[130:133], v[10:17], v[206:213], v[130:133], v188, v189 op_sel_hi:[0,0,0]
	v_mfma_scale_f32_16x16x128_f8f6f4 v[122:125], v[2:9], v[220:227], v[122:125], v188, v189 op_sel_hi:[0,0,0]
	v_mfma_scale_f32_16x16x128_f8f6f4 v[114:117], v[10:17], v[220:227], v[114:117], v188, v189 op_sel_hi:[0,0,0]
	v_mfma_scale_f32_16x16x128_f8f6f4 v[142:145], v[18:25], v[190:197], v[142:145], v188, v189 op_sel_hi:[0,0,0]
	v_mfma_scale_f32_16x16x128_f8f6f4 v[134:137], v[26:33], v[190:197], v[134:137], v188, v189 op_sel_hi:[0,0,0]
	v_mfma_scale_f32_16x16x128_f8f6f4 v[126:129], v[18:25], v[198:205], v[126:129], v188, v189 op_sel_hi:[0,0,0]
	v_mfma_scale_f32_16x16x128_f8f6f4 v[118:121], v[26:33], v[198:205], v[118:121], v188, v189 op_sel_hi:[0,0,0]
	v_mfma_scale_f32_16x16x128_f8f6f4 v[110:113], v[18:25], v[206:213], v[110:113], v188, v189 op_sel_hi:[0,0,0]
	v_mfma_scale_f32_16x16x128_f8f6f4 v[106:109], v[26:33], v[206:213], v[106:109], v188, v189 op_sel_hi:[0,0,0]
	v_mfma_scale_f32_16x16x128_f8f6f4 v[102:105], v[18:25], v[220:227], v[102:105], v188, v189 op_sel_hi:[0,0,0]
	v_mfma_scale_f32_16x16x128_f8f6f4 v[98:101], v[26:33], v[220:227], v[98:101], v188, v189 op_sel_hi:[0,0,0]
	s_barrier
	s_add_i32 s26, s54, s57
	v_lshl_add_u64 v[214:215], v[176:177], 0, s[16:17]
	s_mov_b32 m0, s26
	ds_read_b128 v[190:193], v187 offset:49152
	ds_read_b128 v[194:197], v187 offset:50176
	ds_read_b128 v[198:201], v187 offset:51200
	ds_read_b128 v[202:205], v187 offset:52224
	ds_read_b128 v[206:209], v187 offset:53248
	ds_read_b128 v[210:213], v187 offset:54272
	ds_read_b128 v[220:223], v187 offset:55296
	ds_read_b128 v[224:227], v187 offset:56320
	global_load_lds_dwordx4 v[214:215], off
	v_lshl_add_u64 v[214:215], v[176:177], 0, s[18:19]
	s_add_i32 m0, s26, 0x2000
	s_add_i32 s26, s55, s57
	global_load_lds_dwordx4 v[214:215], off
	v_lshl_add_u64 v[214:215], v[176:177], 0, s[22:23]
	s_mov_b32 m0, s26
	v_lshl_add_u64 v[176:177], v[176:177], 0, s[24:25]
	global_load_lds_dwordx4 v[214:215], off
	s_add_i32 m0, s26, 0x2000
	s_nop 0
	global_load_lds_dwordx4 v[176:177], off
	v_lshl_add_u64 v[176:177], v[178:179], 0, s[20:21]
	s_mov_b32 m0, s64
	s_nop 0
	global_load_lds_dwordx4 v[176:177], off
	v_lshl_add_u64 v[176:177], v[180:181], 0, s[20:21]
	s_mov_b32 m0, s65
	s_nop 0
	global_load_lds_dwordx4 v[176:177], off
	s_waitcnt vmcnt(8) lgkmcnt(0)
	s_barrier
	v_mfma_scale_f32_16x16x128_f8f6f4 v[94:97], v[2:9], v[190:197], v[94:97], v188, v189 op_sel_hi:[0,0,0]
	v_mfma_scale_f32_16x16x128_f8f6f4 v[90:93], v[10:17], v[190:197], v[90:93], v188, v189 op_sel_hi:[0,0,0]
	v_mfma_scale_f32_16x16x128_f8f6f4 v[86:89], v[2:9], v[198:205], v[86:89], v188, v189 op_sel_hi:[0,0,0]
	v_mfma_scale_f32_16x16x128_f8f6f4 v[78:81], v[10:17], v[198:205], v[78:81], v188, v189 op_sel_hi:[0,0,0]
	v_mfma_scale_f32_16x16x128_f8f6f4 v[70:73], v[2:9], v[206:213], v[70:73], v188, v189 op_sel_hi:[0,0,0]
	v_mfma_scale_f32_16x16x128_f8f6f4 v[62:65], v[10:17], v[206:213], v[62:65], v188, v189 op_sel_hi:[0,0,0]
	v_mfma_scale_f32_16x16x128_f8f6f4 v[54:57], v[2:9], v[220:227], v[54:57], v188, v189 op_sel_hi:[0,0,0]
	v_mfma_scale_f32_16x16x128_f8f6f4 v[46:49], v[10:17], v[220:227], v[46:49], v188, v189 op_sel_hi:[0,0,0]
	v_mfma_scale_f32_16x16x128_f8f6f4 v[82:85], v[18:25], v[190:197], v[82:85], v188, v189 op_sel_hi:[0,0,0]
	v_mfma_scale_f32_16x16x128_f8f6f4 v[74:77], v[26:33], v[190:197], v[74:77], v188, v189 op_sel_hi:[0,0,0]
	v_mfma_scale_f32_16x16x128_f8f6f4 v[66:69], v[18:25], v[198:205], v[66:69], v188, v189 op_sel_hi:[0,0,0]
	v_mfma_scale_f32_16x16x128_f8f6f4 v[58:61], v[26:33], v[198:205], v[58:61], v188, v189 op_sel_hi:[0,0,0]
	v_mfma_scale_f32_16x16x128_f8f6f4 v[50:53], v[18:25], v[206:213], v[50:53], v188, v189 op_sel_hi:[0,0,0]
	v_mfma_scale_f32_16x16x128_f8f6f4 v[42:45], v[26:33], v[206:213], v[42:45], v188, v189 op_sel_hi:[0,0,0]
	v_mfma_scale_f32_16x16x128_f8f6f4 v[38:41], v[18:25], v[220:227], v[38:41], v188, v189 op_sel_hi:[0,0,0]
	v_mfma_scale_f32_16x16x128_f8f6f4 v[34:37], v[26:33], v[220:227], v[34:37], v188, v189 op_sel_hi:[0,0,0]
	s_barrier
	s_add_i32 s74, s74, 2
	s_add_u32 s72, s72, 0x10000
	s_addc_u32 s73, s73, 0
	s_add_u32 s50, s50, 0x100
	s_addc_u32 s51, s51, 0
	s_cmp_gt_u32 s74, 41
.LBB0_858:
	ds_read_b128 v[26:29], v185
	ds_read_b128 v[30:33], v185 offset:1024
	ds_read_b128 v[18:21], v185 offset:2048
	ds_read_b128 v[22:25], v185 offset:3072
	ds_read_b128 v[10:13], v186
	ds_read_b128 v[14:17], v186 offset:1024
	ds_read_b128 v[2:5], v186 offset:2048
	ds_read_b128 v[6:9], v186 offset:3072
	s_add_u32 s26, s50, 0xfff50080
	s_addc_u32 s27, s51, -1
	s_cmp_eq_u32 s74, 40
	s_cselect_b32 s53, s5, s27
	s_cselect_b32 s52, s4, s26
	s_cselect_b32 s55, s45, s73
	s_cselect_b32 s54, s44, s72
	v_lshl_add_u64 v[176:177], s[50:51], 0, v[168:169]
	s_add_i32 m0, s59, 0xc000
	ds_read_b128 v[190:193], v187
	ds_read_b128 v[194:197], v187 offset:1024
	ds_read_b128 v[198:201], v187 offset:2048
	ds_read_b128 v[202:205], v187 offset:3072
	ds_read_b128 v[206:209], v187 offset:4096
	ds_read_b128 v[210:213], v187 offset:5120
	ds_read_b128 v[220:223], v187 offset:6144
	ds_read_b128 v[224:227], v187 offset:7168
	global_load_lds_dwordx4 v[176:177], off
	v_lshl_add_u64 v[176:177], s[50:51], 0, v[170:171]
	s_add_i32 m0, s59, 0xe000
	s_nop 0
	global_load_lds_dwordx4 v[176:177], off
	s_waitcnt vmcnt(8) lgkmcnt(0)
	s_barrier
	v_mfma_scale_f32_16x16x128_f8f6f4 v[158:161], v[26:33], v[190:197], v[158:161], v188, v189 op_sel_hi:[0,0,0]
	v_mfma_scale_f32_16x16x128_f8f6f4 v[154:157], v[18:25], v[190:197], v[154:157], v188, v189 op_sel_hi:[0,0,0]
	v_mfma_scale_f32_16x16x128_f8f6f4 v[150:153], v[26:33], v[198:205], v[150:153], v188, v189 op_sel_hi:[0,0,0]
	v_mfma_scale_f32_16x16x128_f8f6f4 v[146:149], v[18:25], v[198:205], v[146:149], v188, v189 op_sel_hi:[0,0,0]
	v_mfma_scale_f32_16x16x128_f8f6f4 v[138:141], v[26:33], v[206:213], v[138:141], v188, v189 op_sel_hi:[0,0,0]
	v_mfma_scale_f32_16x16x128_f8f6f4 v[130:133], v[18:25], v[206:213], v[130:133], v188, v189 op_sel_hi:[0,0,0]
	v_mfma_scale_f32_16x16x128_f8f6f4 v[122:125], v[26:33], v[220:227], v[122:125], v188, v189 op_sel_hi:[0,0,0]
	v_mfma_scale_f32_16x16x128_f8f6f4 v[114:117], v[18:25], v[220:227], v[114:117], v188, v189 op_sel_hi:[0,0,0]
	v_mfma_scale_f32_16x16x128_f8f6f4 v[142:145], v[10:17], v[190:197], v[142:145], v188, v189 op_sel_hi:[0,0,0]
	v_mfma_scale_f32_16x16x128_f8f6f4 v[134:137], v[2:9], v[190:197], v[134:137], v188, v189 op_sel_hi:[0,0,0]
	v_mfma_scale_f32_16x16x128_f8f6f4 v[126:129], v[10:17], v[198:205], v[126:129], v188, v189 op_sel_hi:[0,0,0]
	v_mfma_scale_f32_16x16x128_f8f6f4 v[118:121], v[2:9], v[198:205], v[118:121], v188, v189 op_sel_hi:[0,0,0]
	v_mfma_scale_f32_16x16x128_f8f6f4 v[110:113], v[10:17], v[206:213], v[110:113], v188, v189 op_sel_hi:[0,0,0]
	v_mfma_scale_f32_16x16x128_f8f6f4 v[106:109], v[2:9], v[206:213], v[106:109], v188, v189 op_sel_hi:[0,0,0]
	v_mfma_scale_f32_16x16x128_f8f6f4 v[102:105], v[10:17], v[220:227], v[102:105], v188, v189 op_sel_hi:[0,0,0]
	v_mfma_scale_f32_16x16x128_f8f6f4 v[98:101], v[2:9], v[220:227], v[98:101], v188, v189 op_sel_hi:[0,0,0]
	s_barrier
	s_add_i32 s26, s67, s57
	v_lshl_add_u64 v[176:177], s[54:55], 0, v[162:163]
	s_mov_b32 m0, s26
	ds_read_b128 v[190:193], v187 offset:16384
	ds_read_b128 v[194:197], v187 offset:17408
	ds_read_b128 v[198:201], v187 offset:18432
	ds_read_b128 v[202:205], v187 offset:19456
	ds_read_b128 v[206:209], v187 offset:20480
	ds_read_b128 v[210:213], v187 offset:21504
	ds_read_b128 v[220:223], v187 offset:22528
	ds_read_b128 v[224:227], v187 offset:23552
	global_load_lds_dwordx4 v[176:177], off
	v_lshl_add_u64 v[178:179], v[176:177], 0, s[8:9]
	s_add_i32 m0, s26, 0x2000
	s_add_i32 s26, s68, s57
	global_load_lds_dwordx4 v[178:179], off
	v_lshl_add_u64 v[178:179], v[176:177], 0, s[10:11]
	s_mov_b32 m0, s26
	v_lshl_add_u64 v[180:181], s[52:53], 0, v[166:167]
	global_load_lds_dwordx4 v[178:179], off
	v_lshl_add_u64 v[178:179], v[176:177], 0, s[12:13]
	s_add_i32 m0, s26, 0x2000
	s_nop 0
	global_load_lds_dwordx4 v[178:179], off
	v_lshl_add_u64 v[178:179], s[52:53], 0, v[164:165]
	s_mov_b32 m0, s59
	s_nop 0
	global_load_lds_dwordx4 v[178:179], off
	s_mov_b32 m0, s60
	s_nop 0
	global_load_lds_dwordx4 v[180:181], off
	s_waitcnt vmcnt(8) lgkmcnt(0)
	s_barrier
	v_mfma_scale_f32_16x16x128_f8f6f4 v[94:97], v[26:33], v[190:197], v[94:97], v188, v189 op_sel_hi:[0,0,0]
	v_mfma_scale_f32_16x16x128_f8f6f4 v[90:93], v[18:25], v[190:197], v[90:93], v188, v189 op_sel_hi:[0,0,0]
	v_mfma_scale_f32_16x16x128_f8f6f4 v[86:89], v[26:33], v[198:205], v[86:89], v188, v189 op_sel_hi:[0,0,0]
	v_mfma_scale_f32_16x16x128_f8f6f4 v[78:81], v[18:25], v[198:205], v[78:81], v188, v189 op_sel_hi:[0,0,0]
	v_mfma_scale_f32_16x16x128_f8f6f4 v[70:73], v[26:33], v[206:213], v[70:73], v188, v189 op_sel_hi:[0,0,0]
	v_mfma_scale_f32_16x16x128_f8f6f4 v[62:65], v[18:25], v[206:213], v[62:65], v188, v189 op_sel_hi:[0,0,0]
	v_mfma_scale_f32_16x16x128_f8f6f4 v[54:57], v[26:33], v[220:227], v[54:57], v188, v189 op_sel_hi:[0,0,0]
	v_mfma_scale_f32_16x16x128_f8f6f4 v[46:49], v[18:25], v[220:227], v[46:49], v188, v189 op_sel_hi:[0,0,0]
	v_mfma_scale_f32_16x16x128_f8f6f4 v[82:85], v[10:17], v[190:197], v[82:85], v188, v189 op_sel_hi:[0,0,0]
	v_mfma_scale_f32_16x16x128_f8f6f4 v[74:77], v[2:9], v[190:197], v[74:77], v188, v189 op_sel_hi:[0,0,0]
	v_mfma_scale_f32_16x16x128_f8f6f4 v[66:69], v[10:17], v[198:205], v[66:69], v188, v189 op_sel_hi:[0,0,0]
	v_mfma_scale_f32_16x16x128_f8f6f4 v[58:61], v[2:9], v[198:205], v[58:61], v188, v189 op_sel_hi:[0,0,0]
	v_mfma_scale_f32_16x16x128_f8f6f4 v[50:53], v[10:17], v[206:213], v[50:53], v188, v189 op_sel_hi:[0,0,0]
	v_mfma_scale_f32_16x16x128_f8f6f4 v[42:45], v[2:9], v[206:213], v[42:45], v188, v189 op_sel_hi:[0,0,0]
	v_mfma_scale_f32_16x16x128_f8f6f4 v[38:41], v[10:17], v[220:227], v[38:41], v188, v189 op_sel_hi:[0,0,0]
	v_mfma_scale_f32_16x16x128_f8f6f4 v[34:37], v[2:9], v[220:227], v[34:37], v188, v189 op_sel_hi:[0,0,0]
	s_barrier
	s_add_i32 s54, 0, 0x18000
	s_add_i32 s55, 0, 0x1c000
	v_add_u32_e32 v14, s54, v183
	v_add_u32_e32 v30, s55, v183
	ds_read_b128 v[2:5], v14
	ds_read_b128 v[6:9], v14 offset:1024
	ds_read_b128 v[10:13], v14 offset:2048
	ds_read_b128 v[14:17], v14 offset:3072
	ds_read_b128 v[18:21], v30
	ds_read_b128 v[22:25], v30 offset:1024
	ds_read_b128 v[26:29], v30 offset:2048
	ds_read_b128 v[30:33], v30 offset:3072
	s_add_u32 s26, s52, 0xb0000
	s_addc_u32 s27, s53, 0
	s_mov_b32 m0, s61
	v_lshl_add_u64 v[214:215], s[26:27], 0, v[164:165]
	ds_read_b128 v[190:193], v187 offset:32768
	ds_read_b128 v[194:197], v187 offset:33792
	ds_read_b128 v[198:201], v187 offset:34816
	ds_read_b128 v[202:205], v187 offset:35840
	ds_read_b128 v[206:209], v187 offset:36864
	ds_read_b128 v[210:213], v187 offset:37888
	ds_read_b128 v[220:223], v187 offset:38912
	ds_read_b128 v[224:227], v187 offset:39936
	global_load_lds_dwordx4 v[214:215], off
	v_lshl_add_u64 v[214:215], s[26:27], 0, v[166:167]
	s_mov_b32 m0, s62
	s_nop 0
	global_load_lds_dwordx4 v[214:215], off
	s_waitcnt vmcnt(8) lgkmcnt(0)
	s_barrier
	v_mfma_scale_f32_16x16x128_f8f6f4 v[158:161], v[2:9], v[190:197], v[158:161], v188, v189 op_sel_hi:[0,0,0]
	v_mfma_scale_f32_16x16x128_f8f6f4 v[154:157], v[10:17], v[190:197], v[154:157], v188, v189 op_sel_hi:[0,0,0]
	v_mfma_scale_f32_16x16x128_f8f6f4 v[150:153], v[2:9], v[198:205], v[150:153], v188, v189 op_sel_hi:[0,0,0]
	v_mfma_scale_f32_16x16x128_f8f6f4 v[146:149], v[10:17], v[198:205], v[146:149], v188, v189 op_sel_hi:[0,0,0]
	v_mfma_scale_f32_16x16x128_f8f6f4 v[138:141], v[2:9], v[206:213], v[138:141], v188, v189 op_sel_hi:[0,0,0]
	v_mfma_scale_f32_16x16x128_f8f6f4 v[130:133], v[10:17], v[206:213], v[130:133], v188, v189 op_sel_hi:[0,0,0]
	v_mfma_scale_f32_16x16x128_f8f6f4 v[122:125], v[2:9], v[220:227], v[122:125], v188, v189 op_sel_hi:[0,0,0]
	v_mfma_scale_f32_16x16x128_f8f6f4 v[114:117], v[10:17], v[220:227], v[114:117], v188, v189 op_sel_hi:[0,0,0]
	v_mfma_scale_f32_16x16x128_f8f6f4 v[142:145], v[18:25], v[190:197], v[142:145], v188, v189 op_sel_hi:[0,0,0]
	v_mfma_scale_f32_16x16x128_f8f6f4 v[134:137], v[26:33], v[190:197], v[134:137], v188, v189 op_sel_hi:[0,0,0]
	v_mfma_scale_f32_16x16x128_f8f6f4 v[126:129], v[18:25], v[198:205], v[126:129], v188, v189 op_sel_hi:[0,0,0]
	v_mfma_scale_f32_16x16x128_f8f6f4 v[118:121], v[26:33], v[198:205], v[118:121], v188, v189 op_sel_hi:[0,0,0]
	v_mfma_scale_f32_16x16x128_f8f6f4 v[110:113], v[18:25], v[206:213], v[110:113], v188, v189 op_sel_hi:[0,0,0]
	v_mfma_scale_f32_16x16x128_f8f6f4 v[106:109], v[26:33], v[206:213], v[106:109], v188, v189 op_sel_hi:[0,0,0]
	v_mfma_scale_f32_16x16x128_f8f6f4 v[102:105], v[18:25], v[220:227], v[102:105], v188, v189 op_sel_hi:[0,0,0]
	v_mfma_scale_f32_16x16x128_f8f6f4 v[98:101], v[26:33], v[220:227], v[98:101], v188, v189 op_sel_hi:[0,0,0]
	s_barrier
	s_add_i32 s26, s54, s57
	v_lshl_add_u64 v[214:215], v[176:177], 0, s[16:17]
	s_mov_b32 m0, s26
	ds_read_b128 v[190:193], v187 offset:49152
	ds_read_b128 v[194:197], v187 offset:50176
	ds_read_b128 v[198:201], v187 offset:51200
	ds_read_b128 v[202:205], v187 offset:52224
	ds_read_b128 v[206:209], v187 offset:53248
	ds_read_b128 v[210:213], v187 offset:54272
	ds_read_b128 v[220:223], v187 offset:55296
	ds_read_b128 v[224:227], v187 offset:56320
	global_load_lds_dwordx4 v[214:215], off
	v_lshl_add_u64 v[214:215], v[176:177], 0, s[18:19]
	s_add_i32 m0, s26, 0x2000
	s_add_i32 s26, s55, s57
	global_load_lds_dwordx4 v[214:215], off
	v_lshl_add_u64 v[214:215], v[176:177], 0, s[22:23]
	s_mov_b32 m0, s26
	v_lshl_add_u64 v[176:177], v[176:177], 0, s[24:25]
	global_load_lds_dwordx4 v[214:215], off
	s_add_i32 m0, s26, 0x2000
	s_nop 0
	global_load_lds_dwordx4 v[176:177], off
	v_lshl_add_u64 v[176:177], v[178:179], 0, s[20:21]
	s_mov_b32 m0, s64
	s_nop 0
	global_load_lds_dwordx4 v[176:177], off
	v_lshl_add_u64 v[176:177], v[180:181], 0, s[20:21]
	s_mov_b32 m0, s65
	s_nop 0
	global_load_lds_dwordx4 v[176:177], off
	s_waitcnt vmcnt(8) lgkmcnt(0)
	s_barrier
	v_mfma_scale_f32_16x16x128_f8f6f4 v[94:97], v[2:9], v[190:197], v[94:97], v188, v189 op_sel_hi:[0,0,0]
	v_mfma_scale_f32_16x16x128_f8f6f4 v[90:93], v[10:17], v[190:197], v[90:93], v188, v189 op_sel_hi:[0,0,0]
	v_mfma_scale_f32_16x16x128_f8f6f4 v[86:89], v[2:9], v[198:205], v[86:89], v188, v189 op_sel_hi:[0,0,0]
	v_mfma_scale_f32_16x16x128_f8f6f4 v[78:81], v[10:17], v[198:205], v[78:81], v188, v189 op_sel_hi:[0,0,0]
	v_mfma_scale_f32_16x16x128_f8f6f4 v[70:73], v[2:9], v[206:213], v[70:73], v188, v189 op_sel_hi:[0,0,0]
	v_mfma_scale_f32_16x16x128_f8f6f4 v[62:65], v[10:17], v[206:213], v[62:65], v188, v189 op_sel_hi:[0,0,0]
	v_mfma_scale_f32_16x16x128_f8f6f4 v[54:57], v[2:9], v[220:227], v[54:57], v188, v189 op_sel_hi:[0,0,0]
	v_mfma_scale_f32_16x16x128_f8f6f4 v[46:49], v[10:17], v[220:227], v[46:49], v188, v189 op_sel_hi:[0,0,0]
	v_mfma_scale_f32_16x16x128_f8f6f4 v[82:85], v[18:25], v[190:197], v[82:85], v188, v189 op_sel_hi:[0,0,0]
	v_mfma_scale_f32_16x16x128_f8f6f4 v[74:77], v[26:33], v[190:197], v[74:77], v188, v189 op_sel_hi:[0,0,0]
	v_mfma_scale_f32_16x16x128_f8f6f4 v[66:69], v[18:25], v[198:205], v[66:69], v188, v189 op_sel_hi:[0,0,0]
	v_mfma_scale_f32_16x16x128_f8f6f4 v[58:61], v[26:33], v[198:205], v[58:61], v188, v189 op_sel_hi:[0,0,0]
	v_mfma_scale_f32_16x16x128_f8f6f4 v[50:53], v[18:25], v[206:213], v[50:53], v188, v189 op_sel_hi:[0,0,0]
	v_mfma_scale_f32_16x16x128_f8f6f4 v[42:45], v[26:33], v[206:213], v[42:45], v188, v189 op_sel_hi:[0,0,0]
	v_mfma_scale_f32_16x16x128_f8f6f4 v[38:41], v[18:25], v[220:227], v[38:41], v188, v189 op_sel_hi:[0,0,0]
	v_mfma_scale_f32_16x16x128_f8f6f4 v[34:37], v[26:33], v[220:227], v[34:37], v188, v189 op_sel_hi:[0,0,0]
	s_barrier
	s_add_i32 s74, s74, 2
	s_add_u32 s72, s72, 0x10000
	s_addc_u32 s73, s73, 0
	s_add_u32 s50, s50, 0x100
	s_addc_u32 s51, s51, 0
	s_cmp_gt_u32 s74, 41
	s_cbranch_scc0 .LBB0_858
	s_and_b64 vcc, exec, s[40:41]
	s_cbranch_vccz .LBB0_861
	s_barrier

.LBB0_984:
	s_ashr_i32 s45, s44, 31
	s_lshl_b64 s[26:27], s[44:45], 19
	v_readlane_b32 s50, v254, 56
	v_readlane_b32 s51, v254, 57
	s_add_u32 s50, s50, s26
	s_addc_u32 s51, s51, s27
	s_and_b64 s[26:27], s[0:1], exec
	s_cselect_b32 s45, s51, s59
	s_cselect_b32 s72, s50, s58
	s_ashr_i32 s41, s40, 31
	s_lshl_b64 s[26:27], s[40:41], 19
	s_add_u32 s52, s3, s26
	s_addc_u32 s53, s33, s27
	s_and_b64 s[26:27], s[0:1], exec
	s_cselect_b32 s41, s53, s57
	s_cselect_b32 s73, s52, s56
	s_add_u32 s74, s56, 0x10000
	s_addc_u32 s75, s57, 0
	s_add_u32 s56, s58, 0x40080
	s_addc_u32 s57, s59, 0
	s_mov_b32 s80, -2
	ds_read_b128 v[26:29], v185
	ds_read_b128 v[30:33], v185 offset:1024
	ds_read_b128 v[18:21], v185 offset:2048
	ds_read_b128 v[22:25], v185 offset:3072
	ds_read_b128 v[10:13], v186
	ds_read_b128 v[14:17], v186 offset:1024
	ds_read_b128 v[2:5], v186 offset:2048
	ds_read_b128 v[6:9], v186 offset:3072
	s_add_u32 s26, s56, 0xfffc0080
	s_addc_u32 s27, s57, -1
	s_cmp_eq_u32 s80, 12
	s_cselect_b32 s59, s45, s27
	s_cselect_b32 s58, s72, s26
	s_cselect_b32 s61, s41, s75
	s_cselect_b32 s60, s73, s74
	v_lshl_add_u64 v[176:177], s[56:57], 0, v[168:169]
	s_add_i32 m0, s55, 0xc000
	ds_read_b128 v[192:195], v187
	ds_read_b128 v[196:199], v187 offset:1024
	ds_read_b128 v[200:203], v187 offset:2048
	ds_read_b128 v[204:207], v187 offset:3072
	ds_read_b128 v[208:211], v187 offset:4096
	ds_read_b128 v[212:215], v187 offset:5120
	ds_read_b128 v[220:223], v187 offset:6144
	ds_read_b128 v[224:227], v187 offset:7168
	global_load_lds_dwordx4 v[176:177], off
	v_lshl_add_u64 v[176:177], s[56:57], 0, v[170:171]
	s_add_i32 m0, s55, 0xe000
	s_nop 0
	global_load_lds_dwordx4 v[176:177], off
	s_waitcnt vmcnt(24) lgkmcnt(0)
	s_barrier
	v_mfma_scale_f32_16x16x128_f8f6f4 v[158:161], v[26:33], v[192:199], 0, v188, v189 op_sel_hi:[0,0,0]
	v_mfma_scale_f32_16x16x128_f8f6f4 v[154:157], v[18:25], v[192:199], 0, v188, v189 op_sel_hi:[0,0,0]
	v_mfma_scale_f32_16x16x128_f8f6f4 v[146:149], v[26:33], v[200:207], 0, v188, v189 op_sel_hi:[0,0,0]
	v_mfma_scale_f32_16x16x128_f8f6f4 v[138:141], v[18:25], v[200:207], 0, v188, v189 op_sel_hi:[0,0,0]
	v_mfma_scale_f32_16x16x128_f8f6f4 v[130:133], v[26:33], v[208:215], 0, v188, v189 op_sel_hi:[0,0,0]
	v_mfma_scale_f32_16x16x128_f8f6f4 v[122:125], v[18:25], v[208:215], 0, v188, v189 op_sel_hi:[0,0,0]
	v_mfma_scale_f32_16x16x128_f8f6f4 v[114:117], v[26:33], v[220:227], 0, v188, v189 op_sel_hi:[0,0,0]
	v_mfma_scale_f32_16x16x128_f8f6f4 v[106:109], v[18:25], v[220:227], 0, v188, v189 op_sel_hi:[0,0,0]
	v_mfma_scale_f32_16x16x128_f8f6f4 v[150:153], v[10:17], v[192:199], 0, v188, v189 op_sel_hi:[0,0,0]
	v_mfma_scale_f32_16x16x128_f8f6f4 v[142:145], v[2:9], v[192:199], 0, v188, v189 op_sel_hi:[0,0,0]
	v_mfma_scale_f32_16x16x128_f8f6f4 v[134:137], v[10:17], v[200:207], 0, v188, v189 op_sel_hi:[0,0,0]
	v_mfma_scale_f32_16x16x128_f8f6f4 v[126:129], v[2:9], v[200:207], 0, v188, v189 op_sel_hi:[0,0,0]
	v_mfma_scale_f32_16x16x128_f8f6f4 v[118:121], v[10:17], v[208:215], 0, v188, v189 op_sel_hi:[0,0,0]
	v_mfma_scale_f32_16x16x128_f8f6f4 v[110:113], v[2:9], v[208:215], 0, v188, v189 op_sel_hi:[0,0,0]
	v_mfma_scale_f32_16x16x128_f8f6f4 v[102:105], v[10:17], v[220:227], 0, v188, v189 op_sel_hi:[0,0,0]
	v_mfma_scale_f32_16x16x128_f8f6f4 v[98:101], v[2:9], v[220:227], 0, v188, v189 op_sel_hi:[0,0,0]
	s_barrier
	s_add_i32 s26, s70, s35
	v_lshl_add_u64 v[176:177], s[60:61], 0, v[162:163]
	s_mov_b32 m0, s26
	ds_read_b128 v[192:195], v187 offset:16384
	ds_read_b128 v[196:199], v187 offset:17408
	ds_read_b128 v[200:203], v187 offset:18432
	ds_read_b128 v[204:207], v187 offset:19456
	ds_read_b128 v[208:211], v187 offset:20480
	ds_read_b128 v[212:215], v187 offset:21504
	ds_read_b128 v[220:223], v187 offset:22528
	ds_read_b128 v[224:227], v187 offset:23552
	global_load_lds_dwordx4 v[176:177], off
	v_lshl_add_u64 v[178:179], v[176:177], 0, s[6:7]
	s_add_i32 m0, s26, 0x2000
	s_add_i32 s26, s71, s35
	global_load_lds_dwordx4 v[178:179], off
	v_lshl_add_u64 v[178:179], v[176:177], 0, s[8:9]
	s_mov_b32 m0, s26
	v_lshl_add_u64 v[180:181], s[58:59], 0, v[166:167]
	global_load_lds_dwordx4 v[178:179], off
	v_lshl_add_u64 v[178:179], v[176:177], 0, s[10:11]
	s_add_i32 m0, s26, 0x2000
	s_nop 0
	global_load_lds_dwordx4 v[178:179], off
	v_lshl_add_u64 v[178:179], s[58:59], 0, v[164:165]
	s_mov_b32 m0, s55
	s_nop 0
	global_load_lds_dwordx4 v[178:179], off
	s_mov_b32 m0, s63
	s_nop 0
	global_load_lds_dwordx4 v[180:181], off
	s_waitcnt vmcnt(24) lgkmcnt(0)
	s_barrier
	v_mfma_scale_f32_16x16x128_f8f6f4 v[94:97], v[26:33], v[192:199], 0, v188, v189 op_sel_hi:[0,0,0]
	v_mfma_scale_f32_16x16x128_f8f6f4 v[90:93], v[18:25], v[192:199], 0, v188, v189 op_sel_hi:[0,0,0]
	v_mfma_scale_f32_16x16x128_f8f6f4 v[82:85], v[26:33], v[200:207], 0, v188, v189 op_sel_hi:[0,0,0]
	v_mfma_scale_f32_16x16x128_f8f6f4 v[74:77], v[18:25], v[200:207], 0, v188, v189 op_sel_hi:[0,0,0]
	v_mfma_scale_f32_16x16x128_f8f6f4 v[66:69], v[26:33], v[208:215], 0, v188, v189 op_sel_hi:[0,0,0]
	v_mfma_scale_f32_16x16x128_f8f6f4 v[58:61], v[18:25], v[208:215], 0, v188, v189 op_sel_hi:[0,0,0]
	v_mfma_scale_f32_16x16x128_f8f6f4 v[50:53], v[26:33], v[220:227], 0, v188, v189 op_sel_hi:[0,0,0]
	v_mfma_scale_f32_16x16x128_f8f6f4 v[42:45], v[18:25], v[220:227], 0, v188, v189 op_sel_hi:[0,0,0]
	v_mfma_scale_f32_16x16x128_f8f6f4 v[86:89], v[10:17], v[192:199], 0, v188, v189 op_sel_hi:[0,0,0]
	v_mfma_scale_f32_16x16x128_f8f6f4 v[78:81], v[2:9], v[192:199], 0, v188, v189 op_sel_hi:[0,0,0]
	v_mfma_scale_f32_16x16x128_f8f6f4 v[70:73], v[10:17], v[200:207], 0, v188, v189 op_sel_hi:[0,0,0]
	v_mfma_scale_f32_16x16x128_f8f6f4 v[62:65], v[2:9], v[200:207], 0, v188, v189 op_sel_hi:[0,0,0]
	v_mfma_scale_f32_16x16x128_f8f6f4 v[54:57], v[10:17], v[208:215], 0, v188, v189 op_sel_hi:[0,0,0]
	v_mfma_scale_f32_16x16x128_f8f6f4 v[46:49], v[2:9], v[208:215], 0, v188, v189 op_sel_hi:[0,0,0]
	v_mfma_scale_f32_16x16x128_f8f6f4 v[38:41], v[10:17], v[220:227], 0, v188, v189 op_sel_hi:[0,0,0]
	v_mfma_scale_f32_16x16x128_f8f6f4 v[34:37], v[2:9], v[220:227], 0, v188, v189 op_sel_hi:[0,0,0]
	s_barrier
	s_add_i32 s60, 0, 0x18000
	s_add_i32 s61, 0, 0x1c000
	v_add_u32_e32 v14, s60, v183
	v_add_u32_e32 v30, s61, v183
	ds_read_b128 v[2:5], v14
	ds_read_b128 v[6:9], v14 offset:1024
	ds_read_b128 v[10:13], v14 offset:2048
	ds_read_b128 v[14:17], v14 offset:3072
	ds_read_b128 v[18:21], v30
	ds_read_b128 v[22:25], v30 offset:1024
	ds_read_b128 v[26:29], v30 offset:2048
	ds_read_b128 v[30:33], v30 offset:3072
	s_add_u32 s26, s58, 0x40000
	s_addc_u32 s27, s59, 0
	s_mov_b32 m0, s64
	v_lshl_add_u64 v[216:217], s[26:27], 0, v[164:165]
	ds_read_b128 v[192:195], v187 offset:32768
	ds_read_b128 v[196:199], v187 offset:33792
	ds_read_b128 v[200:203], v187 offset:34816
	ds_read_b128 v[204:207], v187 offset:35840
	ds_read_b128 v[208:211], v187 offset:36864
	ds_read_b128 v[212:215], v187 offset:37888
	ds_read_b128 v[220:223], v187 offset:38912
	ds_read_b128 v[224:227], v187 offset:39936
	global_load_lds_dwordx4 v[216:217], off
	v_lshl_add_u64 v[216:217], s[26:27], 0, v[166:167]
	s_mov_b32 m0, s65
	s_nop 0
	global_load_lds_dwordx4 v[216:217], off
	s_waitcnt vmcnt(8) lgkmcnt(0)
	s_barrier
	v_mfma_scale_f32_16x16x128_f8f6f4 v[158:161], v[2:9], v[192:199], v[158:161], v188, v189 op_sel_hi:[0,0,0]
	v_mfma_scale_f32_16x16x128_f8f6f4 v[154:157], v[10:17], v[192:199], v[154:157], v188, v189 op_sel_hi:[0,0,0]
	v_mfma_scale_f32_16x16x128_f8f6f4 v[146:149], v[2:9], v[200:207], v[146:149], v188, v189 op_sel_hi:[0,0,0]
	v_mfma_scale_f32_16x16x128_f8f6f4 v[138:141], v[10:17], v[200:207], v[138:141], v188, v189 op_sel_hi:[0,0,0]
	v_mfma_scale_f32_16x16x128_f8f6f4 v[130:133], v[2:9], v[208:215], v[130:133], v188, v189 op_sel_hi:[0,0,0]
	v_mfma_scale_f32_16x16x128_f8f6f4 v[122:125], v[10:17], v[208:215], v[122:125], v188, v189 op_sel_hi:[0,0,0]
	v_mfma_scale_f32_16x16x128_f8f6f4 v[114:117], v[2:9], v[220:227], v[114:117], v188, v189 op_sel_hi:[0,0,0]
	v_mfma_scale_f32_16x16x128_f8f6f4 v[106:109], v[10:17], v[220:227], v[106:109], v188, v189 op_sel_hi:[0,0,0]
	v_mfma_scale_f32_16x16x128_f8f6f4 v[150:153], v[18:25], v[192:199], v[150:153], v188, v189 op_sel_hi:[0,0,0]
	v_mfma_scale_f32_16x16x128_f8f6f4 v[142:145], v[26:33], v[192:199], v[142:145], v188, v189 op_sel_hi:[0,0,0]
	v_mfma_scale_f32_16x16x128_f8f6f4 v[134:137], v[18:25], v[200:207], v[134:137], v188, v189 op_sel_hi:[0,0,0]
	v_mfma_scale_f32_16x16x128_f8f6f4 v[126:129], v[26:33], v[200:207], v[126:129], v188, v189 op_sel_hi:[0,0,0]
	v_mfma_scale_f32_16x16x128_f8f6f4 v[118:121], v[18:25], v[208:215], v[118:121], v188, v189 op_sel_hi:[0,0,0]
	v_mfma_scale_f32_16x16x128_f8f6f4 v[110:113], v[26:33], v[208:215], v[110:113], v188, v189 op_sel_hi:[0,0,0]
	v_mfma_scale_f32_16x16x128_f8f6f4 v[102:105], v[18:25], v[220:227], v[102:105], v188, v189 op_sel_hi:[0,0,0]
	v_mfma_scale_f32_16x16x128_f8f6f4 v[98:101], v[26:33], v[220:227], v[98:101], v188, v189 op_sel_hi:[0,0,0]
	s_barrier
	s_add_i32 s26, s60, s35
	v_lshl_add_u64 v[216:217], v[176:177], 0, s[14:15]
	s_mov_b32 m0, s26
	ds_read_b128 v[192:195], v187 offset:49152
	ds_read_b128 v[196:199], v187 offset:50176
	ds_read_b128 v[200:203], v187 offset:51200
	ds_read_b128 v[204:207], v187 offset:52224
	ds_read_b128 v[208:211], v187 offset:53248
	ds_read_b128 v[212:215], v187 offset:54272
	ds_read_b128 v[220:223], v187 offset:55296
	ds_read_b128 v[224:227], v187 offset:56320
	global_load_lds_dwordx4 v[216:217], off
	v_lshl_add_u64 v[216:217], v[176:177], 0, s[16:17]
	s_add_i32 m0, s26, 0x2000
	s_add_i32 s26, s61, s35
	global_load_lds_dwordx4 v[216:217], off
	v_lshl_add_u64 v[216:217], v[176:177], 0, s[20:21]
	s_mov_b32 m0, s26
	v_lshl_add_u64 v[176:177], v[176:177], 0, s[22:23]
	global_load_lds_dwordx4 v[216:217], off
	s_add_i32 m0, s26, 0x2000
	s_nop 0
	global_load_lds_dwordx4 v[176:177], off
	v_lshl_add_u64 v[176:177], v[178:179], 0, s[18:19]
	s_mov_b32 m0, s67
	s_nop 0
	global_load_lds_dwordx4 v[176:177], off
	v_lshl_add_u64 v[176:177], v[180:181], 0, s[18:19]
	s_mov_b32 m0, s68
	s_nop 0
	global_load_lds_dwordx4 v[176:177], off
	s_waitcnt vmcnt(8) lgkmcnt(0)
	s_barrier
	v_mfma_scale_f32_16x16x128_f8f6f4 v[94:97], v[2:9], v[192:199], v[94:97], v188, v189 op_sel_hi:[0,0,0]
	v_mfma_scale_f32_16x16x128_f8f6f4 v[90:93], v[10:17], v[192:199], v[90:93], v188, v189 op_sel_hi:[0,0,0]
	v_mfma_scale_f32_16x16x128_f8f6f4 v[82:85], v[2:9], v[200:207], v[82:85], v188, v189 op_sel_hi:[0,0,0]
	v_mfma_scale_f32_16x16x128_f8f6f4 v[74:77], v[10:17], v[200:207], v[74:77], v188, v189 op_sel_hi:[0,0,0]
	v_mfma_scale_f32_16x16x128_f8f6f4 v[66:69], v[2:9], v[208:215], v[66:69], v188, v189 op_sel_hi:[0,0,0]
	v_mfma_scale_f32_16x16x128_f8f6f4 v[58:61], v[10:17], v[208:215], v[58:61], v188, v189 op_sel_hi:[0,0,0]
	v_mfma_scale_f32_16x16x128_f8f6f4 v[50:53], v[2:9], v[220:227], v[50:53], v188, v189 op_sel_hi:[0,0,0]
	v_mfma_scale_f32_16x16x128_f8f6f4 v[42:45], v[10:17], v[220:227], v[42:45], v188, v189 op_sel_hi:[0,0,0]
	v_mfma_scale_f32_16x16x128_f8f6f4 v[86:89], v[18:25], v[192:199], v[86:89], v188, v189 op_sel_hi:[0,0,0]
	v_mfma_scale_f32_16x16x128_f8f6f4 v[78:81], v[26:33], v[192:199], v[78:81], v188, v189 op_sel_hi:[0,0,0]
	v_mfma_scale_f32_16x16x128_f8f6f4 v[70:73], v[18:25], v[200:207], v[70:73], v188, v189 op_sel_hi:[0,0,0]
	v_mfma_scale_f32_16x16x128_f8f6f4 v[62:65], v[26:33], v[200:207], v[62:65], v188, v189 op_sel_hi:[0,0,0]
	v_mfma_scale_f32_16x16x128_f8f6f4 v[54:57], v[18:25], v[208:215], v[54:57], v188, v189 op_sel_hi:[0,0,0]
	v_mfma_scale_f32_16x16x128_f8f6f4 v[46:49], v[26:33], v[208:215], v[46:49], v188, v189 op_sel_hi:[0,0,0]
	v_mfma_scale_f32_16x16x128_f8f6f4 v[38:41], v[18:25], v[220:227], v[38:41], v188, v189 op_sel_hi:[0,0,0]
	v_mfma_scale_f32_16x16x128_f8f6f4 v[34:37], v[26:33], v[220:227], v[34:37], v188, v189 op_sel_hi:[0,0,0]
	s_barrier
	s_add_i32 s80, s80, 2
	s_add_u32 s74, s74, 0x10000
	s_addc_u32 s75, s75, 0
	s_add_u32 s56, s56, 0x100
	s_addc_u32 s57, s57, 0
	s_cmp_gt_u32 s80, 13
.LBB0_985:
	ds_read_b128 v[26:29], v185
	ds_read_b128 v[30:33], v185 offset:1024
	ds_read_b128 v[18:21], v185 offset:2048
	ds_read_b128 v[22:25], v185 offset:3072
	ds_read_b128 v[10:13], v186
	ds_read_b128 v[14:17], v186 offset:1024
	ds_read_b128 v[2:5], v186 offset:2048
	ds_read_b128 v[6:9], v186 offset:3072
	s_add_u32 s26, s56, 0xfffc0080
	s_addc_u32 s27, s57, -1
	s_cmp_eq_u32 s80, 12
	s_cselect_b32 s59, s45, s27
	s_cselect_b32 s58, s72, s26
	s_cselect_b32 s61, s41, s75
	s_cselect_b32 s60, s73, s74
	v_lshl_add_u64 v[176:177], s[56:57], 0, v[168:169]
	s_add_i32 m0, s55, 0xc000
	ds_read_b128 v[192:195], v187
	ds_read_b128 v[196:199], v187 offset:1024
	ds_read_b128 v[200:203], v187 offset:2048
	ds_read_b128 v[204:207], v187 offset:3072
	ds_read_b128 v[208:211], v187 offset:4096
	ds_read_b128 v[212:215], v187 offset:5120
	ds_read_b128 v[220:223], v187 offset:6144
	ds_read_b128 v[224:227], v187 offset:7168
	global_load_lds_dwordx4 v[176:177], off
	v_lshl_add_u64 v[176:177], s[56:57], 0, v[170:171]
	s_add_i32 m0, s55, 0xe000
	s_nop 0
	global_load_lds_dwordx4 v[176:177], off
	s_waitcnt vmcnt(8) lgkmcnt(0)
	s_barrier
	v_mfma_scale_f32_16x16x128_f8f6f4 v[158:161], v[26:33], v[192:199], v[158:161], v188, v189 op_sel_hi:[0,0,0]
	v_mfma_scale_f32_16x16x128_f8f6f4 v[154:157], v[18:25], v[192:199], v[154:157], v188, v189 op_sel_hi:[0,0,0]
	v_mfma_scale_f32_16x16x128_f8f6f4 v[146:149], v[26:33], v[200:207], v[146:149], v188, v189 op_sel_hi:[0,0,0]
	v_mfma_scale_f32_16x16x128_f8f6f4 v[138:141], v[18:25], v[200:207], v[138:141], v188, v189 op_sel_hi:[0,0,0]
	v_mfma_scale_f32_16x16x128_f8f6f4 v[130:133], v[26:33], v[208:215], v[130:133], v188, v189 op_sel_hi:[0,0,0]
	v_mfma_scale_f32_16x16x128_f8f6f4 v[122:125], v[18:25], v[208:215], v[122:125], v188, v189 op_sel_hi:[0,0,0]
	v_mfma_scale_f32_16x16x128_f8f6f4 v[114:117], v[26:33], v[220:227], v[114:117], v188, v189 op_sel_hi:[0,0,0]
	v_mfma_scale_f32_16x16x128_f8f6f4 v[106:109], v[18:25], v[220:227], v[106:109], v188, v189 op_sel_hi:[0,0,0]
	v_mfma_scale_f32_16x16x128_f8f6f4 v[150:153], v[10:17], v[192:199], v[150:153], v188, v189 op_sel_hi:[0,0,0]
	v_mfma_scale_f32_16x16x128_f8f6f4 v[142:145], v[2:9], v[192:199], v[142:145], v188, v189 op_sel_hi:[0,0,0]
	v_mfma_scale_f32_16x16x128_f8f6f4 v[134:137], v[10:17], v[200:207], v[134:137], v188, v189 op_sel_hi:[0,0,0]
	v_mfma_scale_f32_16x16x128_f8f6f4 v[126:129], v[2:9], v[200:207], v[126:129], v188, v189 op_sel_hi:[0,0,0]
	v_mfma_scale_f32_16x16x128_f8f6f4 v[118:121], v[10:17], v[208:215], v[118:121], v188, v189 op_sel_hi:[0,0,0]
	v_mfma_scale_f32_16x16x128_f8f6f4 v[110:113], v[2:9], v[208:215], v[110:113], v188, v189 op_sel_hi:[0,0,0]
	v_mfma_scale_f32_16x16x128_f8f6f4 v[102:105], v[10:17], v[220:227], v[102:105], v188, v189 op_sel_hi:[0,0,0]
	v_mfma_scale_f32_16x16x128_f8f6f4 v[98:101], v[2:9], v[220:227], v[98:101], v188, v189 op_sel_hi:[0,0,0]
	s_barrier
	s_add_i32 s26, s70, s35
	v_lshl_add_u64 v[176:177], s[60:61], 0, v[162:163]
	s_mov_b32 m0, s26
	ds_read_b128 v[192:195], v187 offset:16384
	ds_read_b128 v[196:199], v187 offset:17408
	ds_read_b128 v[200:203], v187 offset:18432
	ds_read_b128 v[204:207], v187 offset:19456
	ds_read_b128 v[208:211], v187 offset:20480
	ds_read_b128 v[212:215], v187 offset:21504
	ds_read_b128 v[220:223], v187 offset:22528
	ds_read_b128 v[224:227], v187 offset:23552
	global_load_lds_dwordx4 v[176:177], off
	v_lshl_add_u64 v[178:179], v[176:177], 0, s[6:7]
	s_add_i32 m0, s26, 0x2000
	s_add_i32 s26, s71, s35
	global_load_lds_dwordx4 v[178:179], off
	v_lshl_add_u64 v[178:179], v[176:177], 0, s[8:9]
	s_mov_b32 m0, s26
	v_lshl_add_u64 v[180:181], s[58:59], 0, v[166:167]
	global_load_lds_dwordx4 v[178:179], off
	v_lshl_add_u64 v[178:179], v[176:177], 0, s[10:11]
	s_add_i32 m0, s26, 0x2000
	s_nop 0
	global_load_lds_dwordx4 v[178:179], off
	v_lshl_add_u64 v[178:179], s[58:59], 0, v[164:165]
	s_mov_b32 m0, s55
	s_nop 0
	global_load_lds_dwordx4 v[178:179], off
	s_mov_b32 m0, s63
	s_nop 0
	global_load_lds_dwordx4 v[180:181], off
	s_waitcnt vmcnt(8) lgkmcnt(0)
	s_barrier
	v_mfma_scale_f32_16x16x128_f8f6f4 v[94:97], v[26:33], v[192:199], v[94:97], v188, v189 op_sel_hi:[0,0,0]
	v_mfma_scale_f32_16x16x128_f8f6f4 v[90:93], v[18:25], v[192:199], v[90:93], v188, v189 op_sel_hi:[0,0,0]
	v_mfma_scale_f32_16x16x128_f8f6f4 v[82:85], v[26:33], v[200:207], v[82:85], v188, v189 op_sel_hi:[0,0,0]
	v_mfma_scale_f32_16x16x128_f8f6f4 v[74:77], v[18:25], v[200:207], v[74:77], v188, v189 op_sel_hi:[0,0,0]
	v_mfma_scale_f32_16x16x128_f8f6f4 v[66:69], v[26:33], v[208:215], v[66:69], v188, v189 op_sel_hi:[0,0,0]
	v_mfma_scale_f32_16x16x128_f8f6f4 v[58:61], v[18:25], v[208:215], v[58:61], v188, v189 op_sel_hi:[0,0,0]
	v_mfma_scale_f32_16x16x128_f8f6f4 v[50:53], v[26:33], v[220:227], v[50:53], v188, v189 op_sel_hi:[0,0,0]
	v_mfma_scale_f32_16x16x128_f8f6f4 v[42:45], v[18:25], v[220:227], v[42:45], v188, v189 op_sel_hi:[0,0,0]
	v_mfma_scale_f32_16x16x128_f8f6f4 v[86:89], v[10:17], v[192:199], v[86:89], v188, v189 op_sel_hi:[0,0,0]
	v_mfma_scale_f32_16x16x128_f8f6f4 v[78:81], v[2:9], v[192:199], v[78:81], v188, v189 op_sel_hi:[0,0,0]
	v_mfma_scale_f32_16x16x128_f8f6f4 v[70:73], v[10:17], v[200:207], v[70:73], v188, v189 op_sel_hi:[0,0,0]
	v_mfma_scale_f32_16x16x128_f8f6f4 v[62:65], v[2:9], v[200:207], v[62:65], v188, v189 op_sel_hi:[0,0,0]
	v_mfma_scale_f32_16x16x128_f8f6f4 v[54:57], v[10:17], v[208:215], v[54:57], v188, v189 op_sel_hi:[0,0,0]
	v_mfma_scale_f32_16x16x128_f8f6f4 v[46:49], v[2:9], v[208:215], v[46:49], v188, v189 op_sel_hi:[0,0,0]
	v_mfma_scale_f32_16x16x128_f8f6f4 v[38:41], v[10:17], v[220:227], v[38:41], v188, v189 op_sel_hi:[0,0,0]
	v_mfma_scale_f32_16x16x128_f8f6f4 v[34:37], v[2:9], v[220:227], v[34:37], v188, v189 op_sel_hi:[0,0,0]
	s_barrier
	s_add_i32 s60, 0, 0x18000
	s_add_i32 s61, 0, 0x1c000
	v_add_u32_e32 v14, s60, v183
	v_add_u32_e32 v30, s61, v183
	ds_read_b128 v[2:5], v14
	ds_read_b128 v[6:9], v14 offset:1024
	ds_read_b128 v[10:13], v14 offset:2048
	ds_read_b128 v[14:17], v14 offset:3072
	ds_read_b128 v[18:21], v30
	ds_read_b128 v[22:25], v30 offset:1024
	ds_read_b128 v[26:29], v30 offset:2048
	ds_read_b128 v[30:33], v30 offset:3072
	s_add_u32 s26, s58, 0x40000
	s_addc_u32 s27, s59, 0
	s_mov_b32 m0, s64
	v_lshl_add_u64 v[216:217], s[26:27], 0, v[164:165]
	ds_read_b128 v[192:195], v187 offset:32768
	ds_read_b128 v[196:199], v187 offset:33792
	ds_read_b128 v[200:203], v187 offset:34816
	ds_read_b128 v[204:207], v187 offset:35840
	ds_read_b128 v[208:211], v187 offset:36864
	ds_read_b128 v[212:215], v187 offset:37888
	ds_read_b128 v[220:223], v187 offset:38912
	ds_read_b128 v[224:227], v187 offset:39936
	global_load_lds_dwordx4 v[216:217], off
	v_lshl_add_u64 v[216:217], s[26:27], 0, v[166:167]
	s_mov_b32 m0, s65
	s_nop 0
	global_load_lds_dwordx4 v[216:217], off
	s_waitcnt vmcnt(8) lgkmcnt(0)
	s_barrier
	v_mfma_scale_f32_16x16x128_f8f6f4 v[158:161], v[2:9], v[192:199], v[158:161], v188, v189 op_sel_hi:[0,0,0]
	v_mfma_scale_f32_16x16x128_f8f6f4 v[154:157], v[10:17], v[192:199], v[154:157], v188, v189 op_sel_hi:[0,0,0]
	v_mfma_scale_f32_16x16x128_f8f6f4 v[146:149], v[2:9], v[200:207], v[146:149], v188, v189 op_sel_hi:[0,0,0]
	v_mfma_scale_f32_16x16x128_f8f6f4 v[138:141], v[10:17], v[200:207], v[138:141], v188, v189 op_sel_hi:[0,0,0]
	v_mfma_scale_f32_16x16x128_f8f6f4 v[130:133], v[2:9], v[208:215], v[130:133], v188, v189 op_sel_hi:[0,0,0]
	v_mfma_scale_f32_16x16x128_f8f6f4 v[122:125], v[10:17], v[208:215], v[122:125], v188, v189 op_sel_hi:[0,0,0]
	v_mfma_scale_f32_16x16x128_f8f6f4 v[114:117], v[2:9], v[220:227], v[114:117], v188, v189 op_sel_hi:[0,0,0]
	v_mfma_scale_f32_16x16x128_f8f6f4 v[106:109], v[10:17], v[220:227], v[106:109], v188, v189 op_sel_hi:[0,0,0]
	v_mfma_scale_f32_16x16x128_f8f6f4 v[150:153], v[18:25], v[192:199], v[150:153], v188, v189 op_sel_hi:[0,0,0]
	v_mfma_scale_f32_16x16x128_f8f6f4 v[142:145], v[26:33], v[192:199], v[142:145], v188, v189 op_sel_hi:[0,0,0]
	v_mfma_scale_f32_16x16x128_f8f6f4 v[134:137], v[18:25], v[200:207], v[134:137], v188, v189 op_sel_hi:[0,0,0]
	v_mfma_scale_f32_16x16x128_f8f6f4 v[126:129], v[26:33], v[200:207], v[126:129], v188, v189 op_sel_hi:[0,0,0]
	v_mfma_scale_f32_16x16x128_f8f6f4 v[118:121], v[18:25], v[208:215], v[118:121], v188, v189 op_sel_hi:[0,0,0]
	v_mfma_scale_f32_16x16x128_f8f6f4 v[110:113], v[26:33], v[208:215], v[110:113], v188, v189 op_sel_hi:[0,0,0]
	v_mfma_scale_f32_16x16x128_f8f6f4 v[102:105], v[18:25], v[220:227], v[102:105], v188, v189 op_sel_hi:[0,0,0]
	v_mfma_scale_f32_16x16x128_f8f6f4 v[98:101], v[26:33], v[220:227], v[98:101], v188, v189 op_sel_hi:[0,0,0]
	s_barrier
	s_add_i32 s26, s60, s35
	v_lshl_add_u64 v[216:217], v[176:177], 0, s[14:15]
	s_mov_b32 m0, s26
	ds_read_b128 v[192:195], v187 offset:49152
	ds_read_b128 v[196:199], v187 offset:50176
	ds_read_b128 v[200:203], v187 offset:51200
	ds_read_b128 v[204:207], v187 offset:52224
	ds_read_b128 v[208:211], v187 offset:53248
	ds_read_b128 v[212:215], v187 offset:54272
	ds_read_b128 v[220:223], v187 offset:55296
	ds_read_b128 v[224:227], v187 offset:56320
	global_load_lds_dwordx4 v[216:217], off
	v_lshl_add_u64 v[216:217], v[176:177], 0, s[16:17]
	s_add_i32 m0, s26, 0x2000
	s_add_i32 s26, s61, s35
	global_load_lds_dwordx4 v[216:217], off
	v_lshl_add_u64 v[216:217], v[176:177], 0, s[20:21]
	s_mov_b32 m0, s26
	v_lshl_add_u64 v[176:177], v[176:177], 0, s[22:23]
	global_load_lds_dwordx4 v[216:217], off
	s_add_i32 m0, s26, 0x2000
	s_nop 0
	global_load_lds_dwordx4 v[176:177], off
	v_lshl_add_u64 v[176:177], v[178:179], 0, s[18:19]
	s_mov_b32 m0, s67
	s_nop 0
	global_load_lds_dwordx4 v[176:177], off
	v_lshl_add_u64 v[176:177], v[180:181], 0, s[18:19]
	s_mov_b32 m0, s68
	s_nop 0
	global_load_lds_dwordx4 v[176:177], off
	s_waitcnt vmcnt(8) lgkmcnt(0)
	s_barrier
	v_mfma_scale_f32_16x16x128_f8f6f4 v[94:97], v[2:9], v[192:199], v[94:97], v188, v189 op_sel_hi:[0,0,0]
	v_mfma_scale_f32_16x16x128_f8f6f4 v[90:93], v[10:17], v[192:199], v[90:93], v188, v189 op_sel_hi:[0,0,0]
	v_mfma_scale_f32_16x16x128_f8f6f4 v[82:85], v[2:9], v[200:207], v[82:85], v188, v189 op_sel_hi:[0,0,0]
	v_mfma_scale_f32_16x16x128_f8f6f4 v[74:77], v[10:17], v[200:207], v[74:77], v188, v189 op_sel_hi:[0,0,0]
	v_mfma_scale_f32_16x16x128_f8f6f4 v[66:69], v[2:9], v[208:215], v[66:69], v188, v189 op_sel_hi:[0,0,0]
	v_mfma_scale_f32_16x16x128_f8f6f4 v[58:61], v[10:17], v[208:215], v[58:61], v188, v189 op_sel_hi:[0,0,0]
	v_mfma_scale_f32_16x16x128_f8f6f4 v[50:53], v[2:9], v[220:227], v[50:53], v188, v189 op_sel_hi:[0,0,0]
	v_mfma_scale_f32_16x16x128_f8f6f4 v[42:45], v[10:17], v[220:227], v[42:45], v188, v189 op_sel_hi:[0,0,0]
	v_mfma_scale_f32_16x16x128_f8f6f4 v[86:89], v[18:25], v[192:199], v[86:89], v188, v189 op_sel_hi:[0,0,0]
	v_mfma_scale_f32_16x16x128_f8f6f4 v[78:81], v[26:33], v[192:199], v[78:81], v188, v189 op_sel_hi:[0,0,0]
	v_mfma_scale_f32_16x16x128_f8f6f4 v[70:73], v[18:25], v[200:207], v[70:73], v188, v189 op_sel_hi:[0,0,0]
	v_mfma_scale_f32_16x16x128_f8f6f4 v[62:65], v[26:33], v[200:207], v[62:65], v188, v189 op_sel_hi:[0,0,0]
	v_mfma_scale_f32_16x16x128_f8f6f4 v[54:57], v[18:25], v[208:215], v[54:57], v188, v189 op_sel_hi:[0,0,0]
	v_mfma_scale_f32_16x16x128_f8f6f4 v[46:49], v[26:33], v[208:215], v[46:49], v188, v189 op_sel_hi:[0,0,0]
	v_mfma_scale_f32_16x16x128_f8f6f4 v[38:41], v[18:25], v[220:227], v[38:41], v188, v189 op_sel_hi:[0,0,0]
	v_mfma_scale_f32_16x16x128_f8f6f4 v[34:37], v[26:33], v[220:227], v[34:37], v188, v189 op_sel_hi:[0,0,0]
	s_barrier
	s_add_i32 s80, s80, 2
	s_add_u32 s74, s74, 0x10000
	s_addc_u32 s75, s75, 0
	s_add_u32 s56, s56, 0x100
	s_addc_u32 s57, s57, 0
	s_cmp_gt_u32 s80, 13
	s_cbranch_scc0 .LBB0_985
	s_and_b64 vcc, exec, s[24:25]
	s_cbranch_vccz .LBB0_988
	s_barrier

.LBB0_1191:
	s_ashr_i32 s45, s44, 31
	s_lshl_b64 s[26:27], s[44:45], 19
	s_add_u32 s50, s4, s26
	s_addc_u32 s51, s5, s27
	s_and_b64 s[26:27], s[0:1], exec
	s_cselect_b32 s45, s51, s59
	s_cselect_b32 s69, s50, s58
	s_ashr_i32 s41, s40, 31
	s_lshl_b64 s[26:27], s[40:41], 19
	s_add_u32 s52, s3, s26
	s_addc_u32 s53, s33, s27
	s_and_b64 s[26:27], s[0:1], exec
	s_cselect_b32 s41, s53, s57
	s_cselect_b32 s70, s52, s56
	s_add_u32 s71, s56, 0x10000
	s_addc_u32 s72, s57, 0
	s_add_u32 s56, s58, 0x40080
	s_addc_u32 s57, s59, 0
	s_mov_b32 s73, -2
	ds_read_b128 v[66:69], v199
	ds_read_b128 v[70:73], v199 offset:1024
	ds_read_b128 v[82:85], v199 offset:2048
	ds_read_b128 v[86:89], v199 offset:3072
	ds_read_b128 v[146:149], v200
	ds_read_b128 v[150:153], v200 offset:1024
	ds_read_b128 v[154:157], v200 offset:2048
	ds_read_b128 v[158:161], v200 offset:3072
	s_add_u32 s26, s56, 0xfffc0080
	s_addc_u32 s27, s57, -1
	s_cmp_eq_u32 s73, 12
	s_cselect_b32 s59, s45, s27
	s_cselect_b32 s58, s69, s26
	s_cselect_b32 s27, s41, s72
	s_cselect_b32 s26, s70, s71
	v_lshl_add_u64 v[214:215], s[56:57], 0, v[176:177]
	s_add_i32 m0, s55, 0xc000
	ds_read_b128 v[162:165], v201
	ds_read_b128 v[166:169], v201 offset:1024
	ds_read_b128 v[184:187], v201 offset:2048
	ds_read_b128 v[188:191], v201 offset:3072
	ds_read_b128 v[192:195], v201 offset:4096
	ds_read_b128 v[202:205], v201 offset:5120
	ds_read_b128 v[206:209], v201 offset:6144
	ds_read_b128 v[210:213], v201 offset:7168
	global_load_lds_dwordx4 v[214:215], off
	v_lshl_add_u64 v[214:215], s[56:57], 0, v[178:179]
	s_add_i32 m0, s55, 0xe000
	s_nop 0
	global_load_lds_dwordx4 v[214:215], off
	s_waitcnt vmcnt(8) lgkmcnt(0)
	s_barrier
	v_mfma_f32_16x16x32_bf16 v[142:145], v[66:69], v[162:165], 0
	v_mfma_f32_16x16x32_bf16 v[138:141], v[82:85], v[162:165], 0
	v_mfma_f32_16x16x32_bf16 v[126:129], v[66:69], v[184:187], 0
	v_mfma_f32_16x16x32_bf16 v[122:125], v[82:85], v[184:187], 0
	v_mfma_f32_16x16x32_bf16 v[110:113], v[66:69], v[192:195], 0
	v_mfma_f32_16x16x32_bf16 v[106:109], v[82:85], v[192:195], 0
	v_mfma_f32_16x16x32_bf16 v[94:97], v[66:69], v[206:209], 0
	v_mfma_f32_16x16x32_bf16 v[90:93], v[82:85], v[206:209], 0
	v_mfma_f32_16x16x32_bf16 v[142:145], v[70:73], v[166:169], v[142:145]
	v_mfma_f32_16x16x32_bf16 v[138:141], v[86:89], v[166:169], v[138:141]
	v_mfma_f32_16x16x32_bf16 v[126:129], v[70:73], v[188:191], v[126:129]
	v_mfma_f32_16x16x32_bf16 v[122:125], v[86:89], v[188:191], v[122:125]
	v_mfma_f32_16x16x32_bf16 v[110:113], v[70:73], v[202:205], v[110:113]
	v_mfma_f32_16x16x32_bf16 v[106:109], v[86:89], v[202:205], v[106:109]
	v_mfma_f32_16x16x32_bf16 v[94:97], v[70:73], v[210:213], v[94:97]
	v_mfma_f32_16x16x32_bf16 v[90:93], v[86:89], v[210:213], v[90:93]
	v_mfma_f32_16x16x32_bf16 v[134:137], v[146:149], v[162:165], 0
	v_mfma_f32_16x16x32_bf16 v[130:133], v[154:157], v[162:165], 0
	v_mfma_f32_16x16x32_bf16 v[118:121], v[146:149], v[184:187], 0
	v_mfma_f32_16x16x32_bf16 v[114:117], v[154:157], v[184:187], 0
	v_mfma_f32_16x16x32_bf16 v[102:105], v[146:149], v[192:195], 0
	v_mfma_f32_16x16x32_bf16 v[98:101], v[154:157], v[192:195], 0
	v_mfma_f32_16x16x32_bf16 v[78:81], v[146:149], v[206:209], 0
	v_mfma_f32_16x16x32_bf16 v[74:77], v[154:157], v[206:209], 0
	v_mfma_f32_16x16x32_bf16 v[134:137], v[150:153], v[166:169], v[134:137]
	v_mfma_f32_16x16x32_bf16 v[130:133], v[158:161], v[166:169], v[130:133]
	v_mfma_f32_16x16x32_bf16 v[118:121], v[150:153], v[188:191], v[118:121]
	v_mfma_f32_16x16x32_bf16 v[114:117], v[158:161], v[188:191], v[114:117]
	v_mfma_f32_16x16x32_bf16 v[102:105], v[150:153], v[202:205], v[102:105]
	v_mfma_f32_16x16x32_bf16 v[98:101], v[158:161], v[202:205], v[98:101]
	v_mfma_f32_16x16x32_bf16 v[78:81], v[150:153], v[210:213], v[78:81]
	v_mfma_f32_16x16x32_bf16 v[74:77], v[158:161], v[210:213], v[74:77]
	s_barrier
	v_lshl_add_u64 v[214:215], s[26:27], 0, v[170:171]
	s_add_i32 s26, s67, s35
	s_mov_b32 m0, s26
	ds_read_b128 v[162:165], v201 offset:16384
	ds_read_b128 v[166:169], v201 offset:17408
	ds_read_b128 v[184:187], v201 offset:18432
	ds_read_b128 v[188:191], v201 offset:19456
	ds_read_b128 v[192:195], v201 offset:20480
	ds_read_b128 v[202:205], v201 offset:21504
	ds_read_b128 v[206:209], v201 offset:22528
	ds_read_b128 v[210:213], v201 offset:23552
	global_load_lds_dwordx4 v[214:215], off
	v_lshl_add_u64 v[216:217], v[214:215], 0, s[6:7]
	s_add_i32 m0, s26, 0x2000
	s_add_i32 s26, s68, s35
	global_load_lds_dwordx4 v[216:217], off
	v_lshl_add_u64 v[216:217], v[214:215], 0, s[10:11]
	s_mov_b32 m0, s26
	v_lshl_add_u64 v[220:221], s[58:59], 0, v[174:175]
	global_load_lds_dwordx4 v[216:217], off
	v_lshl_add_u64 v[216:217], v[214:215], 0, s[12:13]
	s_add_i32 m0, s26, 0x2000
	s_nop 0
	global_load_lds_dwordx4 v[216:217], off
	v_lshl_add_u64 v[216:217], s[58:59], 0, v[172:173]
	s_mov_b32 m0, s55
	s_nop 0
	global_load_lds_dwordx4 v[216:217], off
	s_mov_b32 m0, s60
	s_nop 0
	global_load_lds_dwordx4 v[220:221], off
	s_waitcnt vmcnt(8) lgkmcnt(0)
	s_barrier
	v_mfma_f32_16x16x32_bf16 v[62:65], v[66:69], v[162:165], 0
	v_mfma_f32_16x16x32_bf16 v[58:61], v[82:85], v[162:165], 0
	v_mfma_f32_16x16x32_bf16 v[46:49], v[66:69], v[184:187], 0
	v_mfma_f32_16x16x32_bf16 v[42:45], v[82:85], v[184:187], 0
	v_mfma_f32_16x16x32_bf16 v[30:33], v[66:69], v[192:195], 0
	v_mfma_f32_16x16x32_bf16 v[26:29], v[82:85], v[192:195], 0
	v_mfma_f32_16x16x32_bf16 v[14:17], v[66:69], v[206:209], 0
	v_mfma_f32_16x16x32_bf16 v[10:13], v[82:85], v[206:209], 0
	v_mfma_f32_16x16x32_bf16 v[62:65], v[70:73], v[166:169], v[62:65]
	v_mfma_f32_16x16x32_bf16 v[58:61], v[86:89], v[166:169], v[58:61]
	v_mfma_f32_16x16x32_bf16 v[46:49], v[70:73], v[188:191], v[46:49]
	v_mfma_f32_16x16x32_bf16 v[42:45], v[86:89], v[188:191], v[42:45]
	v_mfma_f32_16x16x32_bf16 v[30:33], v[70:73], v[202:205], v[30:33]
	v_mfma_f32_16x16x32_bf16 v[26:29], v[86:89], v[202:205], v[26:29]
	v_mfma_f32_16x16x32_bf16 v[14:17], v[70:73], v[210:213], v[14:17]
	v_mfma_f32_16x16x32_bf16 v[10:13], v[86:89], v[210:213], v[10:13]
	v_mfma_f32_16x16x32_bf16 v[54:57], v[146:149], v[162:165], 0
	v_mfma_f32_16x16x32_bf16 v[50:53], v[154:157], v[162:165], 0
	v_mfma_f32_16x16x32_bf16 v[38:41], v[146:149], v[184:187], 0
	v_mfma_f32_16x16x32_bf16 v[34:37], v[154:157], v[184:187], 0
	v_mfma_f32_16x16x32_bf16 v[22:25], v[146:149], v[192:195], 0
	v_mfma_f32_16x16x32_bf16 v[18:21], v[154:157], v[192:195], 0
	v_mfma_f32_16x16x32_bf16 v[6:9], v[146:149], v[206:209], 0
	v_mfma_f32_16x16x32_bf16 v[2:5], v[154:157], v[206:209], 0
	v_mfma_f32_16x16x32_bf16 v[54:57], v[150:153], v[166:169], v[54:57]
	v_mfma_f32_16x16x32_bf16 v[50:53], v[158:161], v[166:169], v[50:53]
	v_mfma_f32_16x16x32_bf16 v[38:41], v[150:153], v[188:191], v[38:41]
	v_mfma_f32_16x16x32_bf16 v[34:37], v[158:161], v[188:191], v[34:37]
	v_mfma_f32_16x16x32_bf16 v[22:25], v[150:153], v[202:205], v[22:25]
	v_mfma_f32_16x16x32_bf16 v[18:21], v[158:161], v[202:205], v[18:21]
	v_mfma_f32_16x16x32_bf16 v[6:9], v[150:153], v[210:213], v[6:9]
	v_mfma_f32_16x16x32_bf16 v[2:5], v[158:161], v[210:213], v[2:5]
	s_barrier
	s_add_i32 s74, 0, 0x18000
	s_add_i32 s75, 0, 0x1c000
	v_add_u32_e32 v86, s74, v197
	v_add_u32_e32 v158, s75, v197
	ds_read_b128 v[66:69], v86
	ds_read_b128 v[70:73], v86 offset:1024
	ds_read_b128 v[82:85], v86 offset:2048
	ds_read_b128 v[86:89], v86 offset:3072
	ds_read_b128 v[146:149], v158
	ds_read_b128 v[150:153], v158 offset:1024
	ds_read_b128 v[154:157], v158 offset:2048
	ds_read_b128 v[158:161], v158 offset:3072
	s_add_u32 s26, s58, 0x40000
	s_addc_u32 s27, s59, 0
	s_mov_b32 m0, s61
	v_lshl_add_u64 v[222:223], s[26:27], 0, v[172:173]
	ds_read_b128 v[162:165], v201 offset:32768
	ds_read_b128 v[166:169], v201 offset:33792
	ds_read_b128 v[184:187], v201 offset:34816
	ds_read_b128 v[188:191], v201 offset:35840
	ds_read_b128 v[192:195], v201 offset:36864
	ds_read_b128 v[202:205], v201 offset:37888
	ds_read_b128 v[206:209], v201 offset:38912
	ds_read_b128 v[210:213], v201 offset:39936
	global_load_lds_dwordx4 v[222:223], off
	v_lshl_add_u64 v[222:223], s[26:27], 0, v[174:175]
	s_mov_b32 m0, s62
	s_nop 0
	global_load_lds_dwordx4 v[222:223], off
	s_waitcnt vmcnt(8) lgkmcnt(0)
	s_barrier
	v_mfma_f32_16x16x32_bf16 v[142:145], v[66:69], v[162:165], v[142:145]
	v_mfma_f32_16x16x32_bf16 v[138:141], v[82:85], v[162:165], v[138:141]
	v_mfma_f32_16x16x32_bf16 v[126:129], v[66:69], v[184:187], v[126:129]
	v_mfma_f32_16x16x32_bf16 v[122:125], v[82:85], v[184:187], v[122:125]
	v_mfma_f32_16x16x32_bf16 v[110:113], v[66:69], v[192:195], v[110:113]
	v_mfma_f32_16x16x32_bf16 v[106:109], v[82:85], v[192:195], v[106:109]
	v_mfma_f32_16x16x32_bf16 v[94:97], v[66:69], v[206:209], v[94:97]
	v_mfma_f32_16x16x32_bf16 v[90:93], v[82:85], v[206:209], v[90:93]
	v_mfma_f32_16x16x32_bf16 v[142:145], v[70:73], v[166:169], v[142:145]
	v_mfma_f32_16x16x32_bf16 v[138:141], v[86:89], v[166:169], v[138:141]
	v_mfma_f32_16x16x32_bf16 v[126:129], v[70:73], v[188:191], v[126:129]
	v_mfma_f32_16x16x32_bf16 v[122:125], v[86:89], v[188:191], v[122:125]
	v_mfma_f32_16x16x32_bf16 v[110:113], v[70:73], v[202:205], v[110:113]
	v_mfma_f32_16x16x32_bf16 v[106:109], v[86:89], v[202:205], v[106:109]
	v_mfma_f32_16x16x32_bf16 v[94:97], v[70:73], v[210:213], v[94:97]
	v_mfma_f32_16x16x32_bf16 v[90:93], v[86:89], v[210:213], v[90:93]
	v_mfma_f32_16x16x32_bf16 v[134:137], v[146:149], v[162:165], v[134:137]
	v_mfma_f32_16x16x32_bf16 v[130:133], v[154:157], v[162:165], v[130:133]
	v_mfma_f32_16x16x32_bf16 v[118:121], v[146:149], v[184:187], v[118:121]
	v_mfma_f32_16x16x32_bf16 v[114:117], v[154:157], v[184:187], v[114:117]
	v_mfma_f32_16x16x32_bf16 v[102:105], v[146:149], v[192:195], v[102:105]
	v_mfma_f32_16x16x32_bf16 v[98:101], v[154:157], v[192:195], v[98:101]
	v_mfma_f32_16x16x32_bf16 v[78:81], v[146:149], v[206:209], v[78:81]
	v_mfma_f32_16x16x32_bf16 v[74:77], v[154:157], v[206:209], v[74:77]
	v_mfma_f32_16x16x32_bf16 v[134:137], v[150:153], v[166:169], v[134:137]
	v_mfma_f32_16x16x32_bf16 v[130:133], v[158:161], v[166:169], v[130:133]
	v_mfma_f32_16x16x32_bf16 v[118:121], v[150:153], v[188:191], v[118:121]
	v_mfma_f32_16x16x32_bf16 v[114:117], v[158:161], v[188:191], v[114:117]
	v_mfma_f32_16x16x32_bf16 v[102:105], v[150:153], v[202:205], v[102:105]
	v_mfma_f32_16x16x32_bf16 v[98:101], v[158:161], v[202:205], v[98:101]
	v_mfma_f32_16x16x32_bf16 v[78:81], v[150:153], v[210:213], v[78:81]
	v_mfma_f32_16x16x32_bf16 v[74:77], v[158:161], v[210:213], v[74:77]
	s_barrier
	s_add_i32 s26, s74, s35
	v_lshl_add_u64 v[222:223], v[214:215], 0, s[16:17]
	s_mov_b32 m0, s26
	ds_read_b128 v[162:165], v201 offset:49152
	ds_read_b128 v[166:169], v201 offset:50176
	ds_read_b128 v[184:187], v201 offset:51200
	ds_read_b128 v[188:191], v201 offset:52224
	ds_read_b128 v[192:195], v201 offset:53248
	ds_read_b128 v[202:205], v201 offset:54272
	ds_read_b128 v[206:209], v201 offset:55296
	ds_read_b128 v[210:213], v201 offset:56320
	global_load_lds_dwordx4 v[222:223], off
	v_lshl_add_u64 v[222:223], v[214:215], 0, s[18:19]
	s_add_i32 m0, s26, 0x2000
	s_add_i32 s26, s75, s35
	global_load_lds_dwordx4 v[222:223], off
	v_lshl_add_u64 v[222:223], v[214:215], 0, s[22:23]
	s_mov_b32 m0, s26
	v_lshl_add_u64 v[214:215], v[214:215], 0, s[24:25]
	global_load_lds_dwordx4 v[222:223], off
	s_add_i32 m0, s26, 0x2000
	s_nop 0
	global_load_lds_dwordx4 v[214:215], off
	v_lshl_add_u64 v[214:215], v[216:217], 0, s[20:21]
	s_mov_b32 m0, s64
	s_nop 0
	global_load_lds_dwordx4 v[214:215], off
	v_lshl_add_u64 v[214:215], v[220:221], 0, s[20:21]
	s_mov_b32 m0, s65
	s_nop 0
	global_load_lds_dwordx4 v[214:215], off
	s_waitcnt vmcnt(8) lgkmcnt(0)
	s_barrier
	v_mfma_f32_16x16x32_bf16 v[62:65], v[66:69], v[162:165], v[62:65]
	v_mfma_f32_16x16x32_bf16 v[58:61], v[82:85], v[162:165], v[58:61]
	v_mfma_f32_16x16x32_bf16 v[46:49], v[66:69], v[184:187], v[46:49]
	v_mfma_f32_16x16x32_bf16 v[42:45], v[82:85], v[184:187], v[42:45]
	v_mfma_f32_16x16x32_bf16 v[30:33], v[66:69], v[192:195], v[30:33]
	v_mfma_f32_16x16x32_bf16 v[26:29], v[82:85], v[192:195], v[26:29]
	v_mfma_f32_16x16x32_bf16 v[14:17], v[66:69], v[206:209], v[14:17]
	v_mfma_f32_16x16x32_bf16 v[10:13], v[82:85], v[206:209], v[10:13]
	v_mfma_f32_16x16x32_bf16 v[62:65], v[70:73], v[166:169], v[62:65]
	v_mfma_f32_16x16x32_bf16 v[58:61], v[86:89], v[166:169], v[58:61]
	v_mfma_f32_16x16x32_bf16 v[46:49], v[70:73], v[188:191], v[46:49]
	v_mfma_f32_16x16x32_bf16 v[42:45], v[86:89], v[188:191], v[42:45]
	v_mfma_f32_16x16x32_bf16 v[30:33], v[70:73], v[202:205], v[30:33]
	v_mfma_f32_16x16x32_bf16 v[26:29], v[86:89], v[202:205], v[26:29]
	v_mfma_f32_16x16x32_bf16 v[14:17], v[70:73], v[210:213], v[14:17]
	v_mfma_f32_16x16x32_bf16 v[10:13], v[86:89], v[210:213], v[10:13]
	v_mfma_f32_16x16x32_bf16 v[54:57], v[146:149], v[162:165], v[54:57]
	v_mfma_f32_16x16x32_bf16 v[50:53], v[154:157], v[162:165], v[50:53]
	v_mfma_f32_16x16x32_bf16 v[38:41], v[146:149], v[184:187], v[38:41]
	v_mfma_f32_16x16x32_bf16 v[34:37], v[154:157], v[184:187], v[34:37]
	v_mfma_f32_16x16x32_bf16 v[22:25], v[146:149], v[192:195], v[22:25]
	v_mfma_f32_16x16x32_bf16 v[18:21], v[154:157], v[192:195], v[18:21]
	v_mfma_f32_16x16x32_bf16 v[6:9], v[146:149], v[206:209], v[6:9]
	v_mfma_f32_16x16x32_bf16 v[2:5], v[154:157], v[206:209], v[2:5]
	v_mfma_f32_16x16x32_bf16 v[54:57], v[150:153], v[166:169], v[54:57]
	v_mfma_f32_16x16x32_bf16 v[50:53], v[158:161], v[166:169], v[50:53]
	v_mfma_f32_16x16x32_bf16 v[38:41], v[150:153], v[188:191], v[38:41]
	v_mfma_f32_16x16x32_bf16 v[34:37], v[158:161], v[188:191], v[34:37]
	v_mfma_f32_16x16x32_bf16 v[22:25], v[150:153], v[202:205], v[22:25]
	v_mfma_f32_16x16x32_bf16 v[18:21], v[158:161], v[202:205], v[18:21]
	v_mfma_f32_16x16x32_bf16 v[6:9], v[150:153], v[210:213], v[6:9]
	v_mfma_f32_16x16x32_bf16 v[2:5], v[158:161], v[210:213], v[2:5]
	s_barrier
	s_add_i32 s73, s73, 2
	s_add_u32 s71, s71, 0x10000
	s_addc_u32 s72, s72, 0
	s_add_u32 s56, s56, 0x100
	s_addc_u32 s57, s57, 0
	s_cmp_gt_u32 s73, 13
.LBB0_1192:
	ds_read_b128 v[66:69], v199
	ds_read_b128 v[70:73], v199 offset:1024
	ds_read_b128 v[82:85], v199 offset:2048
	ds_read_b128 v[86:89], v199 offset:3072
	ds_read_b128 v[146:149], v200
	ds_read_b128 v[150:153], v200 offset:1024
	ds_read_b128 v[154:157], v200 offset:2048
	ds_read_b128 v[158:161], v200 offset:3072
	s_add_u32 s26, s56, 0xfffc0080
	s_addc_u32 s27, s57, -1
	s_cmp_eq_u32 s73, 12
	s_cselect_b32 s59, s45, s27
	s_cselect_b32 s58, s69, s26
	s_cselect_b32 s27, s41, s72
	s_cselect_b32 s26, s70, s71
	v_lshl_add_u64 v[214:215], s[56:57], 0, v[176:177]
	s_add_i32 m0, s55, 0xc000
	ds_read_b128 v[162:165], v201
	ds_read_b128 v[166:169], v201 offset:1024
	ds_read_b128 v[184:187], v201 offset:2048
	ds_read_b128 v[188:191], v201 offset:3072
	ds_read_b128 v[192:195], v201 offset:4096
	ds_read_b128 v[202:205], v201 offset:5120
	ds_read_b128 v[206:209], v201 offset:6144
	ds_read_b128 v[210:213], v201 offset:7168
	global_load_lds_dwordx4 v[214:215], off
	v_lshl_add_u64 v[214:215], s[56:57], 0, v[178:179]
	s_add_i32 m0, s55, 0xe000
	s_nop 0
	global_load_lds_dwordx4 v[214:215], off
	s_waitcnt vmcnt(8) lgkmcnt(0)
	s_barrier
	v_mfma_f32_16x16x32_bf16 v[142:145], v[66:69], v[162:165], v[142:145]
	v_mfma_f32_16x16x32_bf16 v[138:141], v[82:85], v[162:165], v[138:141]
	v_mfma_f32_16x16x32_bf16 v[126:129], v[66:69], v[184:187], v[126:129]
	v_mfma_f32_16x16x32_bf16 v[122:125], v[82:85], v[184:187], v[122:125]
	v_mfma_f32_16x16x32_bf16 v[110:113], v[66:69], v[192:195], v[110:113]
	v_mfma_f32_16x16x32_bf16 v[106:109], v[82:85], v[192:195], v[106:109]
	v_mfma_f32_16x16x32_bf16 v[94:97], v[66:69], v[206:209], v[94:97]
	v_mfma_f32_16x16x32_bf16 v[90:93], v[82:85], v[206:209], v[90:93]
	v_mfma_f32_16x16x32_bf16 v[142:145], v[70:73], v[166:169], v[142:145]
	v_mfma_f32_16x16x32_bf16 v[138:141], v[86:89], v[166:169], v[138:141]
	v_mfma_f32_16x16x32_bf16 v[126:129], v[70:73], v[188:191], v[126:129]
	v_mfma_f32_16x16x32_bf16 v[122:125], v[86:89], v[188:191], v[122:125]
	v_mfma_f32_16x16x32_bf16 v[110:113], v[70:73], v[202:205], v[110:113]
	v_mfma_f32_16x16x32_bf16 v[106:109], v[86:89], v[202:205], v[106:109]
	v_mfma_f32_16x16x32_bf16 v[94:97], v[70:73], v[210:213], v[94:97]
	v_mfma_f32_16x16x32_bf16 v[90:93], v[86:89], v[210:213], v[90:93]
	v_mfma_f32_16x16x32_bf16 v[134:137], v[146:149], v[162:165], v[134:137]
	v_mfma_f32_16x16x32_bf16 v[130:133], v[154:157], v[162:165], v[130:133]
	v_mfma_f32_16x16x32_bf16 v[118:121], v[146:149], v[184:187], v[118:121]
	v_mfma_f32_16x16x32_bf16 v[114:117], v[154:157], v[184:187], v[114:117]
	v_mfma_f32_16x16x32_bf16 v[102:105], v[146:149], v[192:195], v[102:105]
	v_mfma_f32_16x16x32_bf16 v[98:101], v[154:157], v[192:195], v[98:101]
	v_mfma_f32_16x16x32_bf16 v[78:81], v[146:149], v[206:209], v[78:81]
	v_mfma_f32_16x16x32_bf16 v[74:77], v[154:157], v[206:209], v[74:77]
	v_mfma_f32_16x16x32_bf16 v[134:137], v[150:153], v[166:169], v[134:137]
	v_mfma_f32_16x16x32_bf16 v[130:133], v[158:161], v[166:169], v[130:133]
	v_mfma_f32_16x16x32_bf16 v[118:121], v[150:153], v[188:191], v[118:121]
	v_mfma_f32_16x16x32_bf16 v[114:117], v[158:161], v[188:191], v[114:117]
	v_mfma_f32_16x16x32_bf16 v[102:105], v[150:153], v[202:205], v[102:105]
	v_mfma_f32_16x16x32_bf16 v[98:101], v[158:161], v[202:205], v[98:101]
	v_mfma_f32_16x16x32_bf16 v[78:81], v[150:153], v[210:213], v[78:81]
	v_mfma_f32_16x16x32_bf16 v[74:77], v[158:161], v[210:213], v[74:77]
	s_barrier
	v_lshl_add_u64 v[214:215], s[26:27], 0, v[170:171]
	s_add_i32 s26, s67, s35
	s_mov_b32 m0, s26
	ds_read_b128 v[162:165], v201 offset:16384
	ds_read_b128 v[166:169], v201 offset:17408
	ds_read_b128 v[184:187], v201 offset:18432
	ds_read_b128 v[188:191], v201 offset:19456
	ds_read_b128 v[192:195], v201 offset:20480
	ds_read_b128 v[202:205], v201 offset:21504
	ds_read_b128 v[206:209], v201 offset:22528
	ds_read_b128 v[210:213], v201 offset:23552
	global_load_lds_dwordx4 v[214:215], off
	v_lshl_add_u64 v[216:217], v[214:215], 0, s[6:7]
	s_add_i32 m0, s26, 0x2000
	s_add_i32 s26, s68, s35
	global_load_lds_dwordx4 v[216:217], off
	v_lshl_add_u64 v[216:217], v[214:215], 0, s[10:11]
	s_mov_b32 m0, s26
	v_lshl_add_u64 v[220:221], s[58:59], 0, v[174:175]
	global_load_lds_dwordx4 v[216:217], off
	v_lshl_add_u64 v[216:217], v[214:215], 0, s[12:13]
	s_add_i32 m0, s26, 0x2000
	s_nop 0
	global_load_lds_dwordx4 v[216:217], off
	v_lshl_add_u64 v[216:217], s[58:59], 0, v[172:173]
	s_mov_b32 m0, s55
	s_nop 0
	global_load_lds_dwordx4 v[216:217], off
	s_mov_b32 m0, s60
	s_nop 0
	global_load_lds_dwordx4 v[220:221], off
	s_waitcnt vmcnt(8) lgkmcnt(0)
	s_barrier
	v_mfma_f32_16x16x32_bf16 v[62:65], v[66:69], v[162:165], v[62:65]
	v_mfma_f32_16x16x32_bf16 v[58:61], v[82:85], v[162:165], v[58:61]
	v_mfma_f32_16x16x32_bf16 v[46:49], v[66:69], v[184:187], v[46:49]
	v_mfma_f32_16x16x32_bf16 v[42:45], v[82:85], v[184:187], v[42:45]
	v_mfma_f32_16x16x32_bf16 v[30:33], v[66:69], v[192:195], v[30:33]
	v_mfma_f32_16x16x32_bf16 v[26:29], v[82:85], v[192:195], v[26:29]
	v_mfma_f32_16x16x32_bf16 v[14:17], v[66:69], v[206:209], v[14:17]
	v_mfma_f32_16x16x32_bf16 v[10:13], v[82:85], v[206:209], v[10:13]
	v_mfma_f32_16x16x32_bf16 v[62:65], v[70:73], v[166:169], v[62:65]
	v_mfma_f32_16x16x32_bf16 v[58:61], v[86:89], v[166:169], v[58:61]
	v_mfma_f32_16x16x32_bf16 v[46:49], v[70:73], v[188:191], v[46:49]
	v_mfma_f32_16x16x32_bf16 v[42:45], v[86:89], v[188:191], v[42:45]
	v_mfma_f32_16x16x32_bf16 v[30:33], v[70:73], v[202:205], v[30:33]
	v_mfma_f32_16x16x32_bf16 v[26:29], v[86:89], v[202:205], v[26:29]
	v_mfma_f32_16x16x32_bf16 v[14:17], v[70:73], v[210:213], v[14:17]
	v_mfma_f32_16x16x32_bf16 v[10:13], v[86:89], v[210:213], v[10:13]
	v_mfma_f32_16x16x32_bf16 v[54:57], v[146:149], v[162:165], v[54:57]
	v_mfma_f32_16x16x32_bf16 v[50:53], v[154:157], v[162:165], v[50:53]
	v_mfma_f32_16x16x32_bf16 v[38:41], v[146:149], v[184:187], v[38:41]
	v_mfma_f32_16x16x32_bf16 v[34:37], v[154:157], v[184:187], v[34:37]
	v_mfma_f32_16x16x32_bf16 v[22:25], v[146:149], v[192:195], v[22:25]
	v_mfma_f32_16x16x32_bf16 v[18:21], v[154:157], v[192:195], v[18:21]
	v_mfma_f32_16x16x32_bf16 v[6:9], v[146:149], v[206:209], v[6:9]
	v_mfma_f32_16x16x32_bf16 v[2:5], v[154:157], v[206:209], v[2:5]
	v_mfma_f32_16x16x32_bf16 v[54:57], v[150:153], v[166:169], v[54:57]
	v_mfma_f32_16x16x32_bf16 v[50:53], v[158:161], v[166:169], v[50:53]
	v_mfma_f32_16x16x32_bf16 v[38:41], v[150:153], v[188:191], v[38:41]
	v_mfma_f32_16x16x32_bf16 v[34:37], v[158:161], v[188:191], v[34:37]
	v_mfma_f32_16x16x32_bf16 v[22:25], v[150:153], v[202:205], v[22:25]
	v_mfma_f32_16x16x32_bf16 v[18:21], v[158:161], v[202:205], v[18:21]
	v_mfma_f32_16x16x32_bf16 v[6:9], v[150:153], v[210:213], v[6:9]
	v_mfma_f32_16x16x32_bf16 v[2:5], v[158:161], v[210:213], v[2:5]
	s_barrier
	s_add_i32 s74, 0, 0x18000
	s_add_i32 s75, 0, 0x1c000
	v_add_u32_e32 v86, s74, v197
	v_add_u32_e32 v158, s75, v197
	ds_read_b128 v[66:69], v86
	ds_read_b128 v[70:73], v86 offset:1024
	ds_read_b128 v[82:85], v86 offset:2048
	ds_read_b128 v[86:89], v86 offset:3072
	ds_read_b128 v[146:149], v158
	ds_read_b128 v[150:153], v158 offset:1024
	ds_read_b128 v[154:157], v158 offset:2048
	ds_read_b128 v[158:161], v158 offset:3072
	s_add_u32 s26, s58, 0x40000
	s_addc_u32 s27, s59, 0
	s_mov_b32 m0, s61
	v_lshl_add_u64 v[222:223], s[26:27], 0, v[172:173]
	ds_read_b128 v[162:165], v201 offset:32768
	ds_read_b128 v[166:169], v201 offset:33792
	ds_read_b128 v[184:187], v201 offset:34816
	ds_read_b128 v[188:191], v201 offset:35840
	ds_read_b128 v[192:195], v201 offset:36864
	ds_read_b128 v[202:205], v201 offset:37888
	ds_read_b128 v[206:209], v201 offset:38912
	ds_read_b128 v[210:213], v201 offset:39936
	global_load_lds_dwordx4 v[222:223], off
	v_lshl_add_u64 v[222:223], s[26:27], 0, v[174:175]
	s_mov_b32 m0, s62
	s_nop 0
	global_load_lds_dwordx4 v[222:223], off
	s_waitcnt vmcnt(8) lgkmcnt(0)
	s_barrier
	v_mfma_f32_16x16x32_bf16 v[142:145], v[66:69], v[162:165], v[142:145]
	v_mfma_f32_16x16x32_bf16 v[138:141], v[82:85], v[162:165], v[138:141]
	v_mfma_f32_16x16x32_bf16 v[126:129], v[66:69], v[184:187], v[126:129]
	v_mfma_f32_16x16x32_bf16 v[122:125], v[82:85], v[184:187], v[122:125]
	v_mfma_f32_16x16x32_bf16 v[110:113], v[66:69], v[192:195], v[110:113]
	v_mfma_f32_16x16x32_bf16 v[106:109], v[82:85], v[192:195], v[106:109]
	v_mfma_f32_16x16x32_bf16 v[94:97], v[66:69], v[206:209], v[94:97]
	v_mfma_f32_16x16x32_bf16 v[90:93], v[82:85], v[206:209], v[90:93]
	v_mfma_f32_16x16x32_bf16 v[142:145], v[70:73], v[166:169], v[142:145]
	v_mfma_f32_16x16x32_bf16 v[138:141], v[86:89], v[166:169], v[138:141]
	v_mfma_f32_16x16x32_bf16 v[126:129], v[70:73], v[188:191], v[126:129]
	v_mfma_f32_16x16x32_bf16 v[122:125], v[86:89], v[188:191], v[122:125]
	v_mfma_f32_16x16x32_bf16 v[110:113], v[70:73], v[202:205], v[110:113]
	v_mfma_f32_16x16x32_bf16 v[106:109], v[86:89], v[202:205], v[106:109]
	v_mfma_f32_16x16x32_bf16 v[94:97], v[70:73], v[210:213], v[94:97]
	v_mfma_f32_16x16x32_bf16 v[90:93], v[86:89], v[210:213], v[90:93]
	v_mfma_f32_16x16x32_bf16 v[134:137], v[146:149], v[162:165], v[134:137]
	v_mfma_f32_16x16x32_bf16 v[130:133], v[154:157], v[162:165], v[130:133]
	v_mfma_f32_16x16x32_bf16 v[118:121], v[146:149], v[184:187], v[118:121]
	v_mfma_f32_16x16x32_bf16 v[114:117], v[154:157], v[184:187], v[114:117]
	v_mfma_f32_16x16x32_bf16 v[102:105], v[146:149], v[192:195], v[102:105]
	v_mfma_f32_16x16x32_bf16 v[98:101], v[154:157], v[192:195], v[98:101]
	v_mfma_f32_16x16x32_bf16 v[78:81], v[146:149], v[206:209], v[78:81]
	v_mfma_f32_16x16x32_bf16 v[74:77], v[154:157], v[206:209], v[74:77]
	v_mfma_f32_16x16x32_bf16 v[134:137], v[150:153], v[166:169], v[134:137]
	v_mfma_f32_16x16x32_bf16 v[130:133], v[158:161], v[166:169], v[130:133]
	v_mfma_f32_16x16x32_bf16 v[118:121], v[150:153], v[188:191], v[118:121]
	v_mfma_f32_16x16x32_bf16 v[114:117], v[158:161], v[188:191], v[114:117]
	v_mfma_f32_16x16x32_bf16 v[102:105], v[150:153], v[202:205], v[102:105]
	v_mfma_f32_16x16x32_bf16 v[98:101], v[158:161], v[202:205], v[98:101]
	v_mfma_f32_16x16x32_bf16 v[78:81], v[150:153], v[210:213], v[78:81]
	v_mfma_f32_16x16x32_bf16 v[74:77], v[158:161], v[210:213], v[74:77]
	s_barrier
	s_add_i32 s26, s74, s35
	v_lshl_add_u64 v[222:223], v[214:215], 0, s[16:17]
	s_mov_b32 m0, s26
	ds_read_b128 v[162:165], v201 offset:49152
	ds_read_b128 v[166:169], v201 offset:50176
	ds_read_b128 v[184:187], v201 offset:51200
	ds_read_b128 v[188:191], v201 offset:52224
	ds_read_b128 v[192:195], v201 offset:53248
	ds_read_b128 v[202:205], v201 offset:54272
	ds_read_b128 v[206:209], v201 offset:55296
	ds_read_b128 v[210:213], v201 offset:56320
	global_load_lds_dwordx4 v[222:223], off
	v_lshl_add_u64 v[222:223], v[214:215], 0, s[18:19]
	s_add_i32 m0, s26, 0x2000
	s_add_i32 s26, s75, s35
	global_load_lds_dwordx4 v[222:223], off
	v_lshl_add_u64 v[222:223], v[214:215], 0, s[22:23]
	s_mov_b32 m0, s26
	v_lshl_add_u64 v[214:215], v[214:215], 0, s[24:25]
	global_load_lds_dwordx4 v[222:223], off
	s_add_i32 m0, s26, 0x2000
	s_nop 0
	global_load_lds_dwordx4 v[214:215], off
	v_lshl_add_u64 v[214:215], v[216:217], 0, s[20:21]
	s_mov_b32 m0, s64
	s_nop 0
	global_load_lds_dwordx4 v[214:215], off
	v_lshl_add_u64 v[214:215], v[220:221], 0, s[20:21]
	s_mov_b32 m0, s65
	s_nop 0
	global_load_lds_dwordx4 v[214:215], off
	s_waitcnt vmcnt(8) lgkmcnt(0)
	s_barrier
	v_mfma_f32_16x16x32_bf16 v[62:65], v[66:69], v[162:165], v[62:65]
	v_mfma_f32_16x16x32_bf16 v[58:61], v[82:85], v[162:165], v[58:61]
	v_mfma_f32_16x16x32_bf16 v[46:49], v[66:69], v[184:187], v[46:49]
	v_mfma_f32_16x16x32_bf16 v[42:45], v[82:85], v[184:187], v[42:45]
	v_mfma_f32_16x16x32_bf16 v[30:33], v[66:69], v[192:195], v[30:33]
	v_mfma_f32_16x16x32_bf16 v[26:29], v[82:85], v[192:195], v[26:29]
	v_mfma_f32_16x16x32_bf16 v[14:17], v[66:69], v[206:209], v[14:17]
	v_mfma_f32_16x16x32_bf16 v[10:13], v[82:85], v[206:209], v[10:13]
	v_mfma_f32_16x16x32_bf16 v[62:65], v[70:73], v[166:169], v[62:65]
	v_mfma_f32_16x16x32_bf16 v[58:61], v[86:89], v[166:169], v[58:61]
	v_mfma_f32_16x16x32_bf16 v[46:49], v[70:73], v[188:191], v[46:49]
	v_mfma_f32_16x16x32_bf16 v[42:45], v[86:89], v[188:191], v[42:45]
	v_mfma_f32_16x16x32_bf16 v[30:33], v[70:73], v[202:205], v[30:33]
	v_mfma_f32_16x16x32_bf16 v[26:29], v[86:89], v[202:205], v[26:29]
	v_mfma_f32_16x16x32_bf16 v[14:17], v[70:73], v[210:213], v[14:17]
	v_mfma_f32_16x16x32_bf16 v[10:13], v[86:89], v[210:213], v[10:13]
	v_mfma_f32_16x16x32_bf16 v[54:57], v[146:149], v[162:165], v[54:57]
	v_mfma_f32_16x16x32_bf16 v[50:53], v[154:157], v[162:165], v[50:53]
	v_mfma_f32_16x16x32_bf16 v[38:41], v[146:149], v[184:187], v[38:41]
	v_mfma_f32_16x16x32_bf16 v[34:37], v[154:157], v[184:187], v[34:37]
	v_mfma_f32_16x16x32_bf16 v[22:25], v[146:149], v[192:195], v[22:25]
	v_mfma_f32_16x16x32_bf16 v[18:21], v[154:157], v[192:195], v[18:21]
	v_mfma_f32_16x16x32_bf16 v[6:9], v[146:149], v[206:209], v[6:9]
	v_mfma_f32_16x16x32_bf16 v[2:5], v[154:157], v[206:209], v[2:5]
	v_mfma_f32_16x16x32_bf16 v[54:57], v[150:153], v[166:169], v[54:57]
	v_mfma_f32_16x16x32_bf16 v[50:53], v[158:161], v[166:169], v[50:53]
	v_mfma_f32_16x16x32_bf16 v[38:41], v[150:153], v[188:191], v[38:41]
	v_mfma_f32_16x16x32_bf16 v[34:37], v[158:161], v[188:191], v[34:37]
	v_mfma_f32_16x16x32_bf16 v[22:25], v[150:153], v[202:205], v[22:25]
	v_mfma_f32_16x16x32_bf16 v[18:21], v[158:161], v[202:205], v[18:21]
	v_mfma_f32_16x16x32_bf16 v[6:9], v[150:153], v[210:213], v[6:9]
	v_mfma_f32_16x16x32_bf16 v[2:5], v[158:161], v[210:213], v[2:5]
	s_barrier
	s_add_i32 s73, s73, 2
	s_add_u32 s71, s71, 0x10000
	s_addc_u32 s72, s72, 0
	s_add_u32 s56, s56, 0x100
	s_addc_u32 s57, s57, 0
	s_cmp_gt_u32 s73, 13
	s_cbranch_scc0 .LBB0_1192
	s_and_b64 vcc, exec, s[36:37]
	s_cbranch_vccz .LBB0_1195
	s_barrier

.LBB0_1270:
	s_ashr_i32 s51, s50, 31
	s_lshl_b64 s[26:27], s[50:51], 20
	v_readlane_b32 s52, v254, 58
	v_readlane_b32 s53, v254, 59
	s_add_u32 s52, s52, s26
	s_addc_u32 s53, s53, s27
	s_and_b64 s[26:27], s[0:1], exec
	s_cselect_b32 s51, s53, s61
	s_cselect_b32 s57, s52, s60
	s_ashr_i32 s45, s44, 31
	s_lshl_b64 s[26:27], s[44:45], 20
	s_add_u32 s54, s3, s26
	s_addc_u32 s55, s33, s27
	s_and_b64 s[26:27], s[0:1], exec
	s_cselect_b32 s45, s55, s59
	s_cselect_b32 s73, s54, s58
	s_add_u32 s74, s58, 0x10000
	s_addc_u32 s75, s59, 0
	s_add_u32 s58, s60, 0x80080
	s_addc_u32 s59, s61, 0
	s_mov_b32 s80, -2
	ds_read_b128 v[144:147], v158
	ds_read_b128 v[148:151], v158 offset:1024
	ds_read_b128 v[152:155], v158 offset:2048
	ds_read_b128 v[162:165], v158 offset:3072
	ds_read_b128 v[166:169], v159
	ds_read_b128 v[170:173], v159 offset:1024
	ds_read_b128 v[174:177], v159 offset:2048
	ds_read_b128 v[178:181], v159 offset:3072
	s_add_u32 s26, s58, 0xfff80080
	s_addc_u32 s27, s59, -1
	s_cmp_eq_u32 s80, 28
	s_cselect_b32 s61, s51, s27
	s_cselect_b32 s60, s57, s26
	s_cselect_b32 s27, s45, s75
	s_cselect_b32 s26, s73, s74
	v_lshl_add_u64 v[214:215], s[58:59], 0, v[136:137]
	s_add_i32 m0, s63, 0xc000
	ds_read_b128 v[182:185], v160
	ds_read_b128 v[186:189], v160 offset:1024
	ds_read_b128 v[190:193], v160 offset:2048
	ds_read_b128 v[194:197], v160 offset:3072
	ds_read_b128 v[198:201], v160 offset:4096
	ds_read_b128 v[202:205], v160 offset:5120
	ds_read_b128 v[206:209], v160 offset:6144
	ds_read_b128 v[210:213], v160 offset:7168
	global_load_lds_dwordx4 v[214:215], off
	v_lshl_add_u64 v[214:215], s[58:59], 0, v[138:139]
	s_add_i32 m0, s63, 0xe000
	s_nop 0
	global_load_lds_dwordx4 v[214:215], off
	s_waitcnt vmcnt(8) lgkmcnt(0)
	s_barrier
	v_mfma_f32_16x16x32_bf16 v[126:129], v[144:147], v[182:185], 0
	v_mfma_f32_16x16x32_bf16 v[122:125], v[152:155], v[182:185], 0
	v_mfma_f32_16x16x32_bf16 v[118:121], v[144:147], v[190:193], 0
	v_mfma_f32_16x16x32_bf16 v[114:117], v[152:155], v[190:193], 0
	v_mfma_f32_16x16x32_bf16 v[106:109], v[144:147], v[198:201], 0
	v_mfma_f32_16x16x32_bf16 v[98:101], v[152:155], v[198:201], 0
	v_mfma_f32_16x16x32_bf16 v[90:93], v[144:147], v[206:209], 0
	v_mfma_f32_16x16x32_bf16 v[82:85], v[152:155], v[206:209], 0
	v_mfma_f32_16x16x32_bf16 v[126:129], v[148:151], v[186:189], v[126:129]
	v_mfma_f32_16x16x32_bf16 v[122:125], v[162:165], v[186:189], v[122:125]
	v_mfma_f32_16x16x32_bf16 v[118:121], v[148:151], v[194:197], v[118:121]
	v_mfma_f32_16x16x32_bf16 v[114:117], v[162:165], v[194:197], v[114:117]
	v_mfma_f32_16x16x32_bf16 v[106:109], v[148:151], v[202:205], v[106:109]
	v_mfma_f32_16x16x32_bf16 v[98:101], v[162:165], v[202:205], v[98:101]
	v_mfma_f32_16x16x32_bf16 v[90:93], v[148:151], v[210:213], v[90:93]
	v_mfma_f32_16x16x32_bf16 v[82:85], v[162:165], v[210:213], v[82:85]
	v_mfma_f32_16x16x32_bf16 v[110:113], v[166:169], v[182:185], 0
	v_mfma_f32_16x16x32_bf16 v[102:105], v[174:177], v[182:185], 0
	v_mfma_f32_16x16x32_bf16 v[94:97], v[166:169], v[190:193], 0
	v_mfma_f32_16x16x32_bf16 v[86:89], v[174:177], v[190:193], 0
	v_mfma_f32_16x16x32_bf16 v[78:81], v[166:169], v[198:201], 0
	v_mfma_f32_16x16x32_bf16 v[74:77], v[174:177], v[198:201], 0
	v_mfma_f32_16x16x32_bf16 v[70:73], v[166:169], v[206:209], 0
	v_mfma_f32_16x16x32_bf16 v[66:69], v[174:177], v[206:209], 0
	v_mfma_f32_16x16x32_bf16 v[110:113], v[170:173], v[186:189], v[110:113]
	v_mfma_f32_16x16x32_bf16 v[102:105], v[178:181], v[186:189], v[102:105]
	v_mfma_f32_16x16x32_bf16 v[94:97], v[170:173], v[194:197], v[94:97]
	v_mfma_f32_16x16x32_bf16 v[86:89], v[178:181], v[194:197], v[86:89]
	v_mfma_f32_16x16x32_bf16 v[78:81], v[170:173], v[202:205], v[78:81]
	v_mfma_f32_16x16x32_bf16 v[74:77], v[178:181], v[202:205], v[74:77]
	v_mfma_f32_16x16x32_bf16 v[70:73], v[170:173], v[210:213], v[70:73]
	v_mfma_f32_16x16x32_bf16 v[66:69], v[178:181], v[210:213], v[66:69]
	s_barrier
	v_lshl_add_u64 v[214:215], s[26:27], 0, v[130:131]
	s_add_i32 s26, s71, s35
	s_mov_b32 m0, s26
	ds_read_b128 v[182:185], v160 offset:16384
	ds_read_b128 v[186:189], v160 offset:17408
	ds_read_b128 v[190:193], v160 offset:18432
	ds_read_b128 v[194:197], v160 offset:19456
	ds_read_b128 v[198:201], v160 offset:20480
	ds_read_b128 v[202:205], v160 offset:21504
	ds_read_b128 v[206:209], v160 offset:22528
	ds_read_b128 v[210:213], v160 offset:23552
	global_load_lds_dwordx4 v[214:215], off
	v_lshl_add_u64 v[216:217], v[214:215], 0, s[6:7]
	s_add_i32 m0, s26, 0x2000
	s_add_i32 s26, s72, s35
	global_load_lds_dwordx4 v[216:217], off
	v_lshl_add_u64 v[216:217], v[214:215], 0, s[8:9]
	s_mov_b32 m0, s26
	v_lshl_add_u64 v[220:221], s[60:61], 0, v[134:135]
	global_load_lds_dwordx4 v[216:217], off
	v_lshl_add_u64 v[216:217], v[214:215], 0, s[10:11]
	s_add_i32 m0, s26, 0x2000
	s_nop 0
	global_load_lds_dwordx4 v[216:217], off
	v_lshl_add_u64 v[216:217], s[60:61], 0, v[132:133]
	s_mov_b32 m0, s63
	s_nop 0
	global_load_lds_dwordx4 v[216:217], off
	s_mov_b32 m0, s64
	s_nop 0
	global_load_lds_dwordx4 v[220:221], off
	s_waitcnt vmcnt(8) lgkmcnt(0)
	s_barrier
	v_mfma_f32_16x16x32_bf16 v[62:65], v[144:147], v[182:185], 0
	v_mfma_f32_16x16x32_bf16 v[58:61], v[152:155], v[182:185], 0
	v_mfma_f32_16x16x32_bf16 v[54:57], v[144:147], v[190:193], 0
	v_mfma_f32_16x16x32_bf16 v[46:49], v[152:155], v[190:193], 0
	v_mfma_f32_16x16x32_bf16 v[38:41], v[144:147], v[198:201], 0
	v_mfma_f32_16x16x32_bf16 v[30:33], v[152:155], v[198:201], 0
	v_mfma_f32_16x16x32_bf16 v[22:25], v[144:147], v[206:209], 0
	v_mfma_f32_16x16x32_bf16 v[14:17], v[152:155], v[206:209], 0
	v_mfma_f32_16x16x32_bf16 v[62:65], v[148:151], v[186:189], v[62:65]
	v_mfma_f32_16x16x32_bf16 v[58:61], v[162:165], v[186:189], v[58:61]
	v_mfma_f32_16x16x32_bf16 v[54:57], v[148:151], v[194:197], v[54:57]
	v_mfma_f32_16x16x32_bf16 v[46:49], v[162:165], v[194:197], v[46:49]
	v_mfma_f32_16x16x32_bf16 v[38:41], v[148:151], v[202:205], v[38:41]
	v_mfma_f32_16x16x32_bf16 v[30:33], v[162:165], v[202:205], v[30:33]
	v_mfma_f32_16x16x32_bf16 v[22:25], v[148:151], v[210:213], v[22:25]
	v_mfma_f32_16x16x32_bf16 v[14:17], v[162:165], v[210:213], v[14:17]
	v_mfma_f32_16x16x32_bf16 v[50:53], v[166:169], v[182:185], 0
	v_mfma_f32_16x16x32_bf16 v[42:45], v[174:177], v[182:185], 0
	v_mfma_f32_16x16x32_bf16 v[34:37], v[166:169], v[190:193], 0
	v_mfma_f32_16x16x32_bf16 v[26:29], v[174:177], v[190:193], 0
	v_mfma_f32_16x16x32_bf16 v[18:21], v[166:169], v[198:201], 0
	v_mfma_f32_16x16x32_bf16 v[10:13], v[174:177], v[198:201], 0
	v_mfma_f32_16x16x32_bf16 v[6:9], v[166:169], v[206:209], 0
	v_mfma_f32_16x16x32_bf16 v[2:5], v[174:177], v[206:209], 0
	v_mfma_f32_16x16x32_bf16 v[50:53], v[170:173], v[186:189], v[50:53]
	v_mfma_f32_16x16x32_bf16 v[42:45], v[178:181], v[186:189], v[42:45]
	v_mfma_f32_16x16x32_bf16 v[34:37], v[170:173], v[194:197], v[34:37]
	v_mfma_f32_16x16x32_bf16 v[26:29], v[178:181], v[194:197], v[26:29]
	v_mfma_f32_16x16x32_bf16 v[18:21], v[170:173], v[202:205], v[18:21]
	v_mfma_f32_16x16x32_bf16 v[10:13], v[178:181], v[202:205], v[10:13]
	v_mfma_f32_16x16x32_bf16 v[6:9], v[170:173], v[210:213], v[6:9]
	v_mfma_f32_16x16x32_bf16 v[2:5], v[178:181], v[210:213], v[2:5]
	s_barrier
	s_add_i32 s81, 0, 0x18000
	v_add_u32_e32 v161, s81, v156
	s_add_i32 s82, 0, 0x1c000
	ds_read_b128 v[144:147], v161
	ds_read_b128 v[148:151], v161 offset:1024
	ds_read_b128 v[152:155], v161 offset:2048
	ds_read_b128 v[162:165], v161 offset:3072
	v_add_u32_e32 v161, s82, v156
	ds_read_b128 v[166:169], v161
	ds_read_b128 v[170:173], v161 offset:1024
	ds_read_b128 v[174:177], v161 offset:2048
	ds_read_b128 v[178:181], v161 offset:3072
	s_add_u32 s26, s60, 0x80000
	s_addc_u32 s27, s61, 0
	s_mov_b32 m0, s65
	v_lshl_add_u64 v[222:223], s[26:27], 0, v[132:133]
	ds_read_b128 v[182:185], v160 offset:32768
	ds_read_b128 v[186:189], v160 offset:33792
	ds_read_b128 v[190:193], v160 offset:34816
	ds_read_b128 v[194:197], v160 offset:35840
	ds_read_b128 v[198:201], v160 offset:36864
	ds_read_b128 v[202:205], v160 offset:37888
	ds_read_b128 v[206:209], v160 offset:38912
	ds_read_b128 v[210:213], v160 offset:39936
	global_load_lds_dwordx4 v[222:223], off
	v_lshl_add_u64 v[222:223], s[26:27], 0, v[134:135]
	s_mov_b32 m0, s66
	s_nop 0
	global_load_lds_dwordx4 v[222:223], off
	s_waitcnt vmcnt(8) lgkmcnt(0)
	s_barrier
	v_mfma_f32_16x16x32_bf16 v[126:129], v[144:147], v[182:185], v[126:129]
	v_mfma_f32_16x16x32_bf16 v[122:125], v[152:155], v[182:185], v[122:125]
	v_mfma_f32_16x16x32_bf16 v[118:121], v[144:147], v[190:193], v[118:121]
	v_mfma_f32_16x16x32_bf16 v[114:117], v[152:155], v[190:193], v[114:117]
	v_mfma_f32_16x16x32_bf16 v[106:109], v[144:147], v[198:201], v[106:109]
	v_mfma_f32_16x16x32_bf16 v[98:101], v[152:155], v[198:201], v[98:101]
	v_mfma_f32_16x16x32_bf16 v[90:93], v[144:147], v[206:209], v[90:93]
	v_mfma_f32_16x16x32_bf16 v[82:85], v[152:155], v[206:209], v[82:85]
	v_mfma_f32_16x16x32_bf16 v[126:129], v[148:151], v[186:189], v[126:129]
	v_mfma_f32_16x16x32_bf16 v[122:125], v[162:165], v[186:189], v[122:125]
	v_mfma_f32_16x16x32_bf16 v[118:121], v[148:151], v[194:197], v[118:121]
	v_mfma_f32_16x16x32_bf16 v[114:117], v[162:165], v[194:197], v[114:117]
	v_mfma_f32_16x16x32_bf16 v[106:109], v[148:151], v[202:205], v[106:109]
	v_mfma_f32_16x16x32_bf16 v[98:101], v[162:165], v[202:205], v[98:101]
	v_mfma_f32_16x16x32_bf16 v[90:93], v[148:151], v[210:213], v[90:93]
	v_mfma_f32_16x16x32_bf16 v[82:85], v[162:165], v[210:213], v[82:85]
	v_mfma_f32_16x16x32_bf16 v[110:113], v[166:169], v[182:185], v[110:113]
	v_mfma_f32_16x16x32_bf16 v[102:105], v[174:177], v[182:185], v[102:105]
	v_mfma_f32_16x16x32_bf16 v[94:97], v[166:169], v[190:193], v[94:97]
	v_mfma_f32_16x16x32_bf16 v[86:89], v[174:177], v[190:193], v[86:89]
	v_mfma_f32_16x16x32_bf16 v[78:81], v[166:169], v[198:201], v[78:81]
	v_mfma_f32_16x16x32_bf16 v[74:77], v[174:177], v[198:201], v[74:77]
	v_mfma_f32_16x16x32_bf16 v[70:73], v[166:169], v[206:209], v[70:73]
	v_mfma_f32_16x16x32_bf16 v[66:69], v[174:177], v[206:209], v[66:69]
	v_mfma_f32_16x16x32_bf16 v[110:113], v[170:173], v[186:189], v[110:113]
	v_mfma_f32_16x16x32_bf16 v[102:105], v[178:181], v[186:189], v[102:105]
	v_mfma_f32_16x16x32_bf16 v[94:97], v[170:173], v[194:197], v[94:97]
	v_mfma_f32_16x16x32_bf16 v[86:89], v[178:181], v[194:197], v[86:89]
	v_mfma_f32_16x16x32_bf16 v[78:81], v[170:173], v[202:205], v[78:81]
	v_mfma_f32_16x16x32_bf16 v[74:77], v[178:181], v[202:205], v[74:77]
	v_mfma_f32_16x16x32_bf16 v[70:73], v[170:173], v[210:213], v[70:73]
	v_mfma_f32_16x16x32_bf16 v[66:69], v[178:181], v[210:213], v[66:69]
	s_barrier
	s_add_i32 s26, s81, s35
	v_lshl_add_u64 v[222:223], v[214:215], 0, s[14:15]
	s_mov_b32 m0, s26
	ds_read_b128 v[182:185], v160 offset:49152
	ds_read_b128 v[186:189], v160 offset:50176
	ds_read_b128 v[190:193], v160 offset:51200
	ds_read_b128 v[194:197], v160 offset:52224
	ds_read_b128 v[198:201], v160 offset:53248
	ds_read_b128 v[202:205], v160 offset:54272
	ds_read_b128 v[206:209], v160 offset:55296
	ds_read_b128 v[210:213], v160 offset:56320
	global_load_lds_dwordx4 v[222:223], off
	v_lshl_add_u64 v[222:223], v[214:215], 0, s[16:17]
	s_add_i32 m0, s26, 0x2000
	s_add_i32 s26, s82, s35
	global_load_lds_dwordx4 v[222:223], off
	v_lshl_add_u64 v[222:223], v[214:215], 0, s[20:21]
	s_mov_b32 m0, s26
	v_lshl_add_u64 v[214:215], v[214:215], 0, s[22:23]
	global_load_lds_dwordx4 v[222:223], off
	s_add_i32 m0, s26, 0x2000
	s_nop 0
	global_load_lds_dwordx4 v[214:215], off
	v_lshl_add_u64 v[214:215], v[216:217], 0, s[18:19]
	s_mov_b32 m0, s68
	s_nop 0
	global_load_lds_dwordx4 v[214:215], off
	v_lshl_add_u64 v[214:215], v[220:221], 0, s[18:19]
	s_mov_b32 m0, s69
	s_nop 0
	global_load_lds_dwordx4 v[214:215], off
	s_waitcnt vmcnt(8) lgkmcnt(0)
	s_barrier
	v_mfma_f32_16x16x32_bf16 v[62:65], v[144:147], v[182:185], v[62:65]
	v_mfma_f32_16x16x32_bf16 v[58:61], v[152:155], v[182:185], v[58:61]
	v_mfma_f32_16x16x32_bf16 v[54:57], v[144:147], v[190:193], v[54:57]
	v_mfma_f32_16x16x32_bf16 v[46:49], v[152:155], v[190:193], v[46:49]
	v_mfma_f32_16x16x32_bf16 v[38:41], v[144:147], v[198:201], v[38:41]
	v_mfma_f32_16x16x32_bf16 v[30:33], v[152:155], v[198:201], v[30:33]
	v_mfma_f32_16x16x32_bf16 v[22:25], v[144:147], v[206:209], v[22:25]
	v_mfma_f32_16x16x32_bf16 v[14:17], v[152:155], v[206:209], v[14:17]
	v_mfma_f32_16x16x32_bf16 v[62:65], v[148:151], v[186:189], v[62:65]
	v_mfma_f32_16x16x32_bf16 v[58:61], v[162:165], v[186:189], v[58:61]
	v_mfma_f32_16x16x32_bf16 v[54:57], v[148:151], v[194:197], v[54:57]
	v_mfma_f32_16x16x32_bf16 v[46:49], v[162:165], v[194:197], v[46:49]
	v_mfma_f32_16x16x32_bf16 v[38:41], v[148:151], v[202:205], v[38:41]
	v_mfma_f32_16x16x32_bf16 v[30:33], v[162:165], v[202:205], v[30:33]
	v_mfma_f32_16x16x32_bf16 v[22:25], v[148:151], v[210:213], v[22:25]
	v_mfma_f32_16x16x32_bf16 v[14:17], v[162:165], v[210:213], v[14:17]
	v_mfma_f32_16x16x32_bf16 v[50:53], v[166:169], v[182:185], v[50:53]
	v_mfma_f32_16x16x32_bf16 v[42:45], v[174:177], v[182:185], v[42:45]
	v_mfma_f32_16x16x32_bf16 v[34:37], v[166:169], v[190:193], v[34:37]
	v_mfma_f32_16x16x32_bf16 v[26:29], v[174:177], v[190:193], v[26:29]
	v_mfma_f32_16x16x32_bf16 v[18:21], v[166:169], v[198:201], v[18:21]
	v_mfma_f32_16x16x32_bf16 v[10:13], v[174:177], v[198:201], v[10:13]
	v_mfma_f32_16x16x32_bf16 v[6:9], v[166:169], v[206:209], v[6:9]
	v_mfma_f32_16x16x32_bf16 v[2:5], v[174:177], v[206:209], v[2:5]
	v_mfma_f32_16x16x32_bf16 v[50:53], v[170:173], v[186:189], v[50:53]
	v_mfma_f32_16x16x32_bf16 v[42:45], v[178:181], v[186:189], v[42:45]
	v_mfma_f32_16x16x32_bf16 v[34:37], v[170:173], v[194:197], v[34:37]
	v_mfma_f32_16x16x32_bf16 v[26:29], v[178:181], v[194:197], v[26:29]
	v_mfma_f32_16x16x32_bf16 v[18:21], v[170:173], v[202:205], v[18:21]
	v_mfma_f32_16x16x32_bf16 v[10:13], v[178:181], v[202:205], v[10:13]
	v_mfma_f32_16x16x32_bf16 v[6:9], v[170:173], v[210:213], v[6:9]
	v_mfma_f32_16x16x32_bf16 v[2:5], v[178:181], v[210:213], v[2:5]
	s_barrier
	s_add_i32 s80, s80, 2
	s_add_u32 s74, s74, 0x10000
	s_addc_u32 s75, s75, 0
	s_add_u32 s58, s58, 0x100
	s_addc_u32 s59, s59, 0
	s_cmp_gt_u32 s80, 29
.LBB0_1271:
	ds_read_b128 v[144:147], v158
	ds_read_b128 v[148:151], v158 offset:1024
	ds_read_b128 v[152:155], v158 offset:2048
	ds_read_b128 v[162:165], v158 offset:3072
	ds_read_b128 v[166:169], v159
	ds_read_b128 v[170:173], v159 offset:1024
	ds_read_b128 v[174:177], v159 offset:2048
	ds_read_b128 v[178:181], v159 offset:3072
	s_add_u32 s26, s58, 0xfff80080
	s_addc_u32 s27, s59, -1
	s_cmp_eq_u32 s80, 28
	s_cselect_b32 s61, s51, s27
	s_cselect_b32 s60, s57, s26
	s_cselect_b32 s27, s45, s75
	s_cselect_b32 s26, s73, s74
	v_lshl_add_u64 v[214:215], s[58:59], 0, v[136:137]
	s_add_i32 m0, s63, 0xc000
	ds_read_b128 v[182:185], v160
	ds_read_b128 v[186:189], v160 offset:1024
	ds_read_b128 v[190:193], v160 offset:2048
	ds_read_b128 v[194:197], v160 offset:3072
	ds_read_b128 v[198:201], v160 offset:4096
	ds_read_b128 v[202:205], v160 offset:5120
	ds_read_b128 v[206:209], v160 offset:6144
	ds_read_b128 v[210:213], v160 offset:7168
	global_load_lds_dwordx4 v[214:215], off
	v_lshl_add_u64 v[214:215], s[58:59], 0, v[138:139]
	s_add_i32 m0, s63, 0xe000
	s_nop 0
	global_load_lds_dwordx4 v[214:215], off
	s_waitcnt vmcnt(8) lgkmcnt(0)
	s_barrier
	v_mfma_f32_16x16x32_bf16 v[126:129], v[144:147], v[182:185], v[126:129]
	v_mfma_f32_16x16x32_bf16 v[122:125], v[152:155], v[182:185], v[122:125]
	v_mfma_f32_16x16x32_bf16 v[118:121], v[144:147], v[190:193], v[118:121]
	v_mfma_f32_16x16x32_bf16 v[114:117], v[152:155], v[190:193], v[114:117]
	v_mfma_f32_16x16x32_bf16 v[106:109], v[144:147], v[198:201], v[106:109]
	v_mfma_f32_16x16x32_bf16 v[98:101], v[152:155], v[198:201], v[98:101]
	v_mfma_f32_16x16x32_bf16 v[90:93], v[144:147], v[206:209], v[90:93]
	v_mfma_f32_16x16x32_bf16 v[82:85], v[152:155], v[206:209], v[82:85]
	v_mfma_f32_16x16x32_bf16 v[126:129], v[148:151], v[186:189], v[126:129]
	v_mfma_f32_16x16x32_bf16 v[122:125], v[162:165], v[186:189], v[122:125]
	v_mfma_f32_16x16x32_bf16 v[118:121], v[148:151], v[194:197], v[118:121]
	v_mfma_f32_16x16x32_bf16 v[114:117], v[162:165], v[194:197], v[114:117]
	v_mfma_f32_16x16x32_bf16 v[106:109], v[148:151], v[202:205], v[106:109]
	v_mfma_f32_16x16x32_bf16 v[98:101], v[162:165], v[202:205], v[98:101]
	v_mfma_f32_16x16x32_bf16 v[90:93], v[148:151], v[210:213], v[90:93]
	v_mfma_f32_16x16x32_bf16 v[82:85], v[162:165], v[210:213], v[82:85]
	v_mfma_f32_16x16x32_bf16 v[110:113], v[166:169], v[182:185], v[110:113]
	v_mfma_f32_16x16x32_bf16 v[102:105], v[174:177], v[182:185], v[102:105]
	v_mfma_f32_16x16x32_bf16 v[94:97], v[166:169], v[190:193], v[94:97]
	v_mfma_f32_16x16x32_bf16 v[86:89], v[174:177], v[190:193], v[86:89]
	v_mfma_f32_16x16x32_bf16 v[78:81], v[166:169], v[198:201], v[78:81]
	v_mfma_f32_16x16x32_bf16 v[74:77], v[174:177], v[198:201], v[74:77]
	v_mfma_f32_16x16x32_bf16 v[70:73], v[166:169], v[206:209], v[70:73]
	v_mfma_f32_16x16x32_bf16 v[66:69], v[174:177], v[206:209], v[66:69]
	v_mfma_f32_16x16x32_bf16 v[110:113], v[170:173], v[186:189], v[110:113]
	v_mfma_f32_16x16x32_bf16 v[102:105], v[178:181], v[186:189], v[102:105]
	v_mfma_f32_16x16x32_bf16 v[94:97], v[170:173], v[194:197], v[94:97]
	v_mfma_f32_16x16x32_bf16 v[86:89], v[178:181], v[194:197], v[86:89]
	v_mfma_f32_16x16x32_bf16 v[78:81], v[170:173], v[202:205], v[78:81]
	v_mfma_f32_16x16x32_bf16 v[74:77], v[178:181], v[202:205], v[74:77]
	v_mfma_f32_16x16x32_bf16 v[70:73], v[170:173], v[210:213], v[70:73]
	v_mfma_f32_16x16x32_bf16 v[66:69], v[178:181], v[210:213], v[66:69]
	s_barrier
	v_lshl_add_u64 v[214:215], s[26:27], 0, v[130:131]
	s_add_i32 s26, s71, s35
	s_mov_b32 m0, s26
	ds_read_b128 v[182:185], v160 offset:16384
	ds_read_b128 v[186:189], v160 offset:17408
	ds_read_b128 v[190:193], v160 offset:18432
	ds_read_b128 v[194:197], v160 offset:19456
	ds_read_b128 v[198:201], v160 offset:20480
	ds_read_b128 v[202:205], v160 offset:21504
	ds_read_b128 v[206:209], v160 offset:22528
	ds_read_b128 v[210:213], v160 offset:23552
	global_load_lds_dwordx4 v[214:215], off
	v_lshl_add_u64 v[216:217], v[214:215], 0, s[6:7]
	s_add_i32 m0, s26, 0x2000
	s_add_i32 s26, s72, s35
	global_load_lds_dwordx4 v[216:217], off
	v_lshl_add_u64 v[216:217], v[214:215], 0, s[8:9]
	s_mov_b32 m0, s26
	v_lshl_add_u64 v[220:221], s[60:61], 0, v[134:135]
	global_load_lds_dwordx4 v[216:217], off
	v_lshl_add_u64 v[216:217], v[214:215], 0, s[10:11]
	s_add_i32 m0, s26, 0x2000
	s_nop 0
	global_load_lds_dwordx4 v[216:217], off
	v_lshl_add_u64 v[216:217], s[60:61], 0, v[132:133]
	s_mov_b32 m0, s63
	s_nop 0
	global_load_lds_dwordx4 v[216:217], off
	s_mov_b32 m0, s64
	s_nop 0
	global_load_lds_dwordx4 v[220:221], off
	s_waitcnt vmcnt(8) lgkmcnt(0)
	s_barrier
	v_mfma_f32_16x16x32_bf16 v[62:65], v[144:147], v[182:185], v[62:65]
	v_mfma_f32_16x16x32_bf16 v[58:61], v[152:155], v[182:185], v[58:61]
	v_mfma_f32_16x16x32_bf16 v[54:57], v[144:147], v[190:193], v[54:57]
	v_mfma_f32_16x16x32_bf16 v[46:49], v[152:155], v[190:193], v[46:49]
	v_mfma_f32_16x16x32_bf16 v[38:41], v[144:147], v[198:201], v[38:41]
	v_mfma_f32_16x16x32_bf16 v[30:33], v[152:155], v[198:201], v[30:33]
	v_mfma_f32_16x16x32_bf16 v[22:25], v[144:147], v[206:209], v[22:25]
	v_mfma_f32_16x16x32_bf16 v[14:17], v[152:155], v[206:209], v[14:17]
	v_mfma_f32_16x16x32_bf16 v[62:65], v[148:151], v[186:189], v[62:65]
	v_mfma_f32_16x16x32_bf16 v[58:61], v[162:165], v[186:189], v[58:61]
	v_mfma_f32_16x16x32_bf16 v[54:57], v[148:151], v[194:197], v[54:57]
	v_mfma_f32_16x16x32_bf16 v[46:49], v[162:165], v[194:197], v[46:49]
	v_mfma_f32_16x16x32_bf16 v[38:41], v[148:151], v[202:205], v[38:41]
	v_mfma_f32_16x16x32_bf16 v[30:33], v[162:165], v[202:205], v[30:33]
	v_mfma_f32_16x16x32_bf16 v[22:25], v[148:151], v[210:213], v[22:25]
	v_mfma_f32_16x16x32_bf16 v[14:17], v[162:165], v[210:213], v[14:17]
	v_mfma_f32_16x16x32_bf16 v[50:53], v[166:169], v[182:185], v[50:53]
	v_mfma_f32_16x16x32_bf16 v[42:45], v[174:177], v[182:185], v[42:45]
	v_mfma_f32_16x16x32_bf16 v[34:37], v[166:169], v[190:193], v[34:37]
	v_mfma_f32_16x16x32_bf16 v[26:29], v[174:177], v[190:193], v[26:29]
	v_mfma_f32_16x16x32_bf16 v[18:21], v[166:169], v[198:201], v[18:21]
	v_mfma_f32_16x16x32_bf16 v[10:13], v[174:177], v[198:201], v[10:13]
	v_mfma_f32_16x16x32_bf16 v[6:9], v[166:169], v[206:209], v[6:9]
	v_mfma_f32_16x16x32_bf16 v[2:5], v[174:177], v[206:209], v[2:5]
	v_mfma_f32_16x16x32_bf16 v[50:53], v[170:173], v[186:189], v[50:53]
	v_mfma_f32_16x16x32_bf16 v[42:45], v[178:181], v[186:189], v[42:45]
	v_mfma_f32_16x16x32_bf16 v[34:37], v[170:173], v[194:197], v[34:37]
	v_mfma_f32_16x16x32_bf16 v[26:29], v[178:181], v[194:197], v[26:29]
	v_mfma_f32_16x16x32_bf16 v[18:21], v[170:173], v[202:205], v[18:21]
	v_mfma_f32_16x16x32_bf16 v[10:13], v[178:181], v[202:205], v[10:13]
	v_mfma_f32_16x16x32_bf16 v[6:9], v[170:173], v[210:213], v[6:9]
	v_mfma_f32_16x16x32_bf16 v[2:5], v[178:181], v[210:213], v[2:5]
	s_barrier
	s_add_i32 s81, 0, 0x18000
	v_add_u32_e32 v161, s81, v156
	s_add_i32 s82, 0, 0x1c000
	ds_read_b128 v[144:147], v161
	ds_read_b128 v[148:151], v161 offset:1024
	ds_read_b128 v[152:155], v161 offset:2048
	ds_read_b128 v[162:165], v161 offset:3072
	v_add_u32_e32 v161, s82, v156
	ds_read_b128 v[166:169], v161
	ds_read_b128 v[170:173], v161 offset:1024
	ds_read_b128 v[174:177], v161 offset:2048
	ds_read_b128 v[178:181], v161 offset:3072
	s_add_u32 s26, s60, 0x80000
	s_addc_u32 s27, s61, 0
	s_mov_b32 m0, s65
	v_lshl_add_u64 v[222:223], s[26:27], 0, v[132:133]
	ds_read_b128 v[182:185], v160 offset:32768
	ds_read_b128 v[186:189], v160 offset:33792
	ds_read_b128 v[190:193], v160 offset:34816
	ds_read_b128 v[194:197], v160 offset:35840
	ds_read_b128 v[198:201], v160 offset:36864
	ds_read_b128 v[202:205], v160 offset:37888
	ds_read_b128 v[206:209], v160 offset:38912
	ds_read_b128 v[210:213], v160 offset:39936
	global_load_lds_dwordx4 v[222:223], off
	v_lshl_add_u64 v[222:223], s[26:27], 0, v[134:135]
	s_mov_b32 m0, s66
	s_nop 0
	global_load_lds_dwordx4 v[222:223], off
	s_waitcnt vmcnt(8) lgkmcnt(0)
	s_barrier
	v_mfma_f32_16x16x32_bf16 v[126:129], v[144:147], v[182:185], v[126:129]
	v_mfma_f32_16x16x32_bf16 v[122:125], v[152:155], v[182:185], v[122:125]
	v_mfma_f32_16x16x32_bf16 v[118:121], v[144:147], v[190:193], v[118:121]
	v_mfma_f32_16x16x32_bf16 v[114:117], v[152:155], v[190:193], v[114:117]
	v_mfma_f32_16x16x32_bf16 v[106:109], v[144:147], v[198:201], v[106:109]
	v_mfma_f32_16x16x32_bf16 v[98:101], v[152:155], v[198:201], v[98:101]
	v_mfma_f32_16x16x32_bf16 v[90:93], v[144:147], v[206:209], v[90:93]
	v_mfma_f32_16x16x32_bf16 v[82:85], v[152:155], v[206:209], v[82:85]
	v_mfma_f32_16x16x32_bf16 v[126:129], v[148:151], v[186:189], v[126:129]
	v_mfma_f32_16x16x32_bf16 v[122:125], v[162:165], v[186:189], v[122:125]
	v_mfma_f32_16x16x32_bf16 v[118:121], v[148:151], v[194:197], v[118:121]
	v_mfma_f32_16x16x32_bf16 v[114:117], v[162:165], v[194:197], v[114:117]
	v_mfma_f32_16x16x32_bf16 v[106:109], v[148:151], v[202:205], v[106:109]
	v_mfma_f32_16x16x32_bf16 v[98:101], v[162:165], v[202:205], v[98:101]
	v_mfma_f32_16x16x32_bf16 v[90:93], v[148:151], v[210:213], v[90:93]
	v_mfma_f32_16x16x32_bf16 v[82:85], v[162:165], v[210:213], v[82:85]
	v_mfma_f32_16x16x32_bf16 v[110:113], v[166:169], v[182:185], v[110:113]
	v_mfma_f32_16x16x32_bf16 v[102:105], v[174:177], v[182:185], v[102:105]
	v_mfma_f32_16x16x32_bf16 v[94:97], v[166:169], v[190:193], v[94:97]
	v_mfma_f32_16x16x32_bf16 v[86:89], v[174:177], v[190:193], v[86:89]
	v_mfma_f32_16x16x32_bf16 v[78:81], v[166:169], v[198:201], v[78:81]
	v_mfma_f32_16x16x32_bf16 v[74:77], v[174:177], v[198:201], v[74:77]
	v_mfma_f32_16x16x32_bf16 v[70:73], v[166:169], v[206:209], v[70:73]
	v_mfma_f32_16x16x32_bf16 v[66:69], v[174:177], v[206:209], v[66:69]
	v_mfma_f32_16x16x32_bf16 v[110:113], v[170:173], v[186:189], v[110:113]
	v_mfma_f32_16x16x32_bf16 v[102:105], v[178:181], v[186:189], v[102:105]
	v_mfma_f32_16x16x32_bf16 v[94:97], v[170:173], v[194:197], v[94:97]
	v_mfma_f32_16x16x32_bf16 v[86:89], v[178:181], v[194:197], v[86:89]
	v_mfma_f32_16x16x32_bf16 v[78:81], v[170:173], v[202:205], v[78:81]
	v_mfma_f32_16x16x32_bf16 v[74:77], v[178:181], v[202:205], v[74:77]
	v_mfma_f32_16x16x32_bf16 v[70:73], v[170:173], v[210:213], v[70:73]
	v_mfma_f32_16x16x32_bf16 v[66:69], v[178:181], v[210:213], v[66:69]
	s_barrier
	s_add_i32 s26, s81, s35
	v_lshl_add_u64 v[222:223], v[214:215], 0, s[14:15]
	s_mov_b32 m0, s26
	ds_read_b128 v[182:185], v160 offset:49152
	ds_read_b128 v[186:189], v160 offset:50176
	ds_read_b128 v[190:193], v160 offset:51200
	ds_read_b128 v[194:197], v160 offset:52224
	ds_read_b128 v[198:201], v160 offset:53248
	ds_read_b128 v[202:205], v160 offset:54272
	ds_read_b128 v[206:209], v160 offset:55296
	ds_read_b128 v[210:213], v160 offset:56320
	global_load_lds_dwordx4 v[222:223], off
	v_lshl_add_u64 v[222:223], v[214:215], 0, s[16:17]
	s_add_i32 m0, s26, 0x2000
	s_add_i32 s26, s82, s35
	global_load_lds_dwordx4 v[222:223], off
	v_lshl_add_u64 v[222:223], v[214:215], 0, s[20:21]
	s_mov_b32 m0, s26
	v_lshl_add_u64 v[214:215], v[214:215], 0, s[22:23]
	global_load_lds_dwordx4 v[222:223], off
	s_add_i32 m0, s26, 0x2000
	s_nop 0
	global_load_lds_dwordx4 v[214:215], off
	v_lshl_add_u64 v[214:215], v[216:217], 0, s[18:19]
	s_mov_b32 m0, s68
	s_nop 0
	global_load_lds_dwordx4 v[214:215], off
	v_lshl_add_u64 v[214:215], v[220:221], 0, s[18:19]
	s_mov_b32 m0, s69
	s_nop 0
	global_load_lds_dwordx4 v[214:215], off
	s_waitcnt vmcnt(8) lgkmcnt(0)
	s_barrier
	v_mfma_f32_16x16x32_bf16 v[62:65], v[144:147], v[182:185], v[62:65]
	v_mfma_f32_16x16x32_bf16 v[58:61], v[152:155], v[182:185], v[58:61]
	v_mfma_f32_16x16x32_bf16 v[54:57], v[144:147], v[190:193], v[54:57]
	v_mfma_f32_16x16x32_bf16 v[46:49], v[152:155], v[190:193], v[46:49]
	v_mfma_f32_16x16x32_bf16 v[38:41], v[144:147], v[198:201], v[38:41]
	v_mfma_f32_16x16x32_bf16 v[30:33], v[152:155], v[198:201], v[30:33]
	v_mfma_f32_16x16x32_bf16 v[22:25], v[144:147], v[206:209], v[22:25]
	v_mfma_f32_16x16x32_bf16 v[14:17], v[152:155], v[206:209], v[14:17]
	v_mfma_f32_16x16x32_bf16 v[62:65], v[148:151], v[186:189], v[62:65]
	v_mfma_f32_16x16x32_bf16 v[58:61], v[162:165], v[186:189], v[58:61]
	v_mfma_f32_16x16x32_bf16 v[54:57], v[148:151], v[194:197], v[54:57]
	v_mfma_f32_16x16x32_bf16 v[46:49], v[162:165], v[194:197], v[46:49]
	v_mfma_f32_16x16x32_bf16 v[38:41], v[148:151], v[202:205], v[38:41]
	v_mfma_f32_16x16x32_bf16 v[30:33], v[162:165], v[202:205], v[30:33]
	v_mfma_f32_16x16x32_bf16 v[22:25], v[148:151], v[210:213], v[22:25]
	v_mfma_f32_16x16x32_bf16 v[14:17], v[162:165], v[210:213], v[14:17]
	v_mfma_f32_16x16x32_bf16 v[50:53], v[166:169], v[182:185], v[50:53]
	v_mfma_f32_16x16x32_bf16 v[42:45], v[174:177], v[182:185], v[42:45]
	v_mfma_f32_16x16x32_bf16 v[34:37], v[166:169], v[190:193], v[34:37]
	v_mfma_f32_16x16x32_bf16 v[26:29], v[174:177], v[190:193], v[26:29]
	v_mfma_f32_16x16x32_bf16 v[18:21], v[166:169], v[198:201], v[18:21]
	v_mfma_f32_16x16x32_bf16 v[10:13], v[174:177], v[198:201], v[10:13]
	v_mfma_f32_16x16x32_bf16 v[6:9], v[166:169], v[206:209], v[6:9]
	v_mfma_f32_16x16x32_bf16 v[2:5], v[174:177], v[206:209], v[2:5]
	v_mfma_f32_16x16x32_bf16 v[50:53], v[170:173], v[186:189], v[50:53]
	v_mfma_f32_16x16x32_bf16 v[42:45], v[178:181], v[186:189], v[42:45]
	v_mfma_f32_16x16x32_bf16 v[34:37], v[170:173], v[194:197], v[34:37]
	v_mfma_f32_16x16x32_bf16 v[26:29], v[178:181], v[194:197], v[26:29]
	v_mfma_f32_16x16x32_bf16 v[18:21], v[170:173], v[202:205], v[18:21]
	v_mfma_f32_16x16x32_bf16 v[10:13], v[178:181], v[202:205], v[10:13]
	v_mfma_f32_16x16x32_bf16 v[6:9], v[170:173], v[210:213], v[6:9]
	v_mfma_f32_16x16x32_bf16 v[2:5], v[178:181], v[210:213], v[2:5]
	s_barrier
	s_add_i32 s80, s80, 2
	s_add_u32 s74, s74, 0x10000
	s_addc_u32 s75, s75, 0
	s_add_u32 s58, s58, 0x100
	s_addc_u32 s59, s59, 0
	s_cmp_gt_u32 s80, 29
	s_cbranch_scc0 .LBB0_1271
	s_and_b64 vcc, exec, s[24:25]
	s_cbranch_vccz .LBB0_1274
	s_barrier

.LBB0_1496:
	s_lshl_b64 s[50:51], s[48:49], 19
	s_add_u32 s50, s59, s50
	s_addc_u32 s51, s60, s51
	s_and_b64 s[4:5], s[4:5], exec
	s_cselect_b32 s2, s51, s57
	s_cselect_b32 s47, s50, s56
	s_add_u32 s4, s56, 0x40080
	v_lshl_add_u64 v[176:177], v[2:3], 0, s[40:41]
	s_addc_u32 s5, s57, 0
	s_mov_b32 s49, -2
	ds_read_b128 v[26:29], v186
	ds_read_b128 v[30:33], v186 offset:1024
	ds_read_b128 v[18:21], v186 offset:2048
	ds_read_b128 v[22:25], v186 offset:3072
	ds_read_b128 v[10:13], v187
	ds_read_b128 v[14:17], v187 offset:1024
	ds_read_b128 v[2:5], v187 offset:2048
	ds_read_b128 v[6:9], v187 offset:3072
	s_add_u32 s56, s4, 0xfffc0080
	s_addc_u32 s57, s5, -1
	s_cmp_eq_u32 s49, 12
	s_cselect_b64 vcc, -1, 0
	s_cselect_b32 s57, s2, s57
	s_cselect_b32 s56, s47, s56
	v_cndmask_b32_e32 v179, v177, v175, vcc
	v_cndmask_b32_e32 v178, v176, v174, vcc
	v_lshl_add_u64 v[180:181], s[4:5], 0, v[168:169]
	s_add_i32 m0, s62, 0xc000
	ds_read_b128 v[192:195], v188
	ds_read_b128 v[196:199], v188 offset:1024
	ds_read_b128 v[200:203], v188 offset:2048
	ds_read_b128 v[204:207], v188 offset:3072
	ds_read_b128 v[208:211], v188 offset:4096
	ds_read_b128 v[212:215], v188 offset:5120
	ds_read_b128 v[220:223], v188 offset:6144
	ds_read_b128 v[224:227], v188 offset:7168
	global_load_lds_dwordx4 v[180:181], off
	v_lshl_add_u64 v[180:181], s[4:5], 0, v[170:171]
	s_add_i32 m0, s62, 0xe000
	s_nop 0
	global_load_lds_dwordx4 v[180:181], off
	s_waitcnt vmcnt(16) lgkmcnt(0)
	s_barrier
	v_mfma_scale_f32_16x16x128_f8f6f4 v[158:161], v[26:33], v[192:199], 0, v189, v190 op_sel_hi:[0,0,0]
	v_mfma_scale_f32_16x16x128_f8f6f4 v[150:153], v[18:25], v[192:199], 0, v189, v190 op_sel_hi:[0,0,0]
	v_mfma_scale_f32_16x16x128_f8f6f4 v[142:145], v[26:33], v[200:207], 0, v189, v190 op_sel_hi:[0,0,0]
	v_mfma_scale_f32_16x16x128_f8f6f4 v[134:137], v[18:25], v[200:207], 0, v189, v190 op_sel_hi:[0,0,0]
	v_mfma_scale_f32_16x16x128_f8f6f4 v[126:129], v[26:33], v[208:215], 0, v189, v190 op_sel_hi:[0,0,0]
	v_mfma_scale_f32_16x16x128_f8f6f4 v[118:121], v[18:25], v[208:215], 0, v189, v190 op_sel_hi:[0,0,0]
	v_mfma_scale_f32_16x16x128_f8f6f4 v[110:113], v[26:33], v[220:227], 0, v189, v190 op_sel_hi:[0,0,0]
	v_mfma_scale_f32_16x16x128_f8f6f4 v[102:105], v[18:25], v[220:227], 0, v189, v190 op_sel_hi:[0,0,0]
	v_mfma_scale_f32_16x16x128_f8f6f4 v[154:157], v[10:17], v[192:199], 0, v189, v190 op_sel_hi:[0,0,0]
	v_mfma_scale_f32_16x16x128_f8f6f4 v[146:149], v[2:9], v[192:199], 0, v189, v190 op_sel_hi:[0,0,0]
	v_mfma_scale_f32_16x16x128_f8f6f4 v[138:141], v[10:17], v[200:207], 0, v189, v190 op_sel_hi:[0,0,0]
	v_mfma_scale_f32_16x16x128_f8f6f4 v[130:133], v[2:9], v[200:207], 0, v189, v190 op_sel_hi:[0,0,0]
	v_mfma_scale_f32_16x16x128_f8f6f4 v[122:125], v[10:17], v[208:215], 0, v189, v190 op_sel_hi:[0,0,0]
	v_mfma_scale_f32_16x16x128_f8f6f4 v[114:117], v[2:9], v[208:215], 0, v189, v190 op_sel_hi:[0,0,0]
	v_mfma_scale_f32_16x16x128_f8f6f4 v[106:109], v[10:17], v[220:227], 0, v189, v190 op_sel_hi:[0,0,0]
	v_mfma_scale_f32_16x16x128_f8f6f4 v[98:101], v[2:9], v[220:227], 0, v189, v190 op_sel_hi:[0,0,0]
	s_barrier
	s_add_i32 s73, s69, s61
	v_lshl_add_u64 v[178:179], v[178:179], 0, v[162:163]
	s_mov_b32 m0, s73
	ds_read_b128 v[192:195], v188 offset:16384
	ds_read_b128 v[196:199], v188 offset:17408
	ds_read_b128 v[200:203], v188 offset:18432
	ds_read_b128 v[204:207], v188 offset:19456
	ds_read_b128 v[208:211], v188 offset:20480
	ds_read_b128 v[212:215], v188 offset:21504
	ds_read_b128 v[220:223], v188 offset:22528
	ds_read_b128 v[224:227], v188 offset:23552
	global_load_lds_dwordx4 v[178:179], off
	v_lshl_add_u64 v[180:181], v[178:179], 0, s[10:11]
	s_add_i32 m0, s73, 0x2000
	s_add_i32 s73, s70, s61
	global_load_lds_dwordx4 v[180:181], off
	v_lshl_add_u64 v[180:181], v[178:179], 0, s[12:13]
	s_mov_b32 m0, s73
	v_lshl_add_u64 v[182:183], s[56:57], 0, v[166:167]
	global_load_lds_dwordx4 v[180:181], off
	v_lshl_add_u64 v[180:181], v[178:179], 0, s[14:15]
	s_add_i32 m0, s73, 0x2000
	s_nop 0
	global_load_lds_dwordx4 v[180:181], off
	v_lshl_add_u64 v[180:181], s[56:57], 0, v[164:165]
	s_mov_b32 m0, s62
	s_nop 0
	global_load_lds_dwordx4 v[180:181], off
	s_mov_b32 m0, s53
	s_nop 0
	global_load_lds_dwordx4 v[182:183], off
	s_waitcnt vmcnt(16) lgkmcnt(0)
	s_barrier
	v_mfma_scale_f32_16x16x128_f8f6f4 v[94:97], v[26:33], v[192:199], 0, v189, v190 op_sel_hi:[0,0,0]
	v_mfma_scale_f32_16x16x128_f8f6f4 v[86:89], v[18:25], v[192:199], 0, v189, v190 op_sel_hi:[0,0,0]
	v_mfma_scale_f32_16x16x128_f8f6f4 v[78:81], v[26:33], v[200:207], 0, v189, v190 op_sel_hi:[0,0,0]
	v_mfma_scale_f32_16x16x128_f8f6f4 v[70:73], v[18:25], v[200:207], 0, v189, v190 op_sel_hi:[0,0,0]
	v_mfma_scale_f32_16x16x128_f8f6f4 v[62:65], v[26:33], v[208:215], 0, v189, v190 op_sel_hi:[0,0,0]
	v_mfma_scale_f32_16x16x128_f8f6f4 v[54:57], v[18:25], v[208:215], 0, v189, v190 op_sel_hi:[0,0,0]
	v_mfma_scale_f32_16x16x128_f8f6f4 v[46:49], v[26:33], v[220:227], 0, v189, v190 op_sel_hi:[0,0,0]
	v_mfma_scale_f32_16x16x128_f8f6f4 v[38:41], v[18:25], v[220:227], 0, v189, v190 op_sel_hi:[0,0,0]
	v_mfma_scale_f32_16x16x128_f8f6f4 v[90:93], v[10:17], v[192:199], 0, v189, v190 op_sel_hi:[0,0,0]
	v_mfma_scale_f32_16x16x128_f8f6f4 v[82:85], v[2:9], v[192:199], 0, v189, v190 op_sel_hi:[0,0,0]
	v_mfma_scale_f32_16x16x128_f8f6f4 v[74:77], v[10:17], v[200:207], 0, v189, v190 op_sel_hi:[0,0,0]
	v_mfma_scale_f32_16x16x128_f8f6f4 v[66:69], v[2:9], v[200:207], 0, v189, v190 op_sel_hi:[0,0,0]
	v_mfma_scale_f32_16x16x128_f8f6f4 v[58:61], v[10:17], v[208:215], 0, v189, v190 op_sel_hi:[0,0,0]
	v_mfma_scale_f32_16x16x128_f8f6f4 v[50:53], v[2:9], v[208:215], 0, v189, v190 op_sel_hi:[0,0,0]
	v_mfma_scale_f32_16x16x128_f8f6f4 v[42:45], v[10:17], v[220:227], 0, v189, v190 op_sel_hi:[0,0,0]
	v_mfma_scale_f32_16x16x128_f8f6f4 v[34:37], v[2:9], v[220:227], 0, v189, v190 op_sel_hi:[0,0,0]
	s_barrier
	s_add_i32 s73, 0, 0x18000
	s_add_i32 s74, 0, 0x1c000
	v_add_u32_e32 v14, s73, v184
	v_add_u32_e32 v30, s74, v184
	ds_read_b128 v[2:5], v14
	ds_read_b128 v[6:9], v14 offset:1024
	ds_read_b128 v[10:13], v14 offset:2048
	ds_read_b128 v[14:17], v14 offset:3072
	ds_read_b128 v[18:21], v30
	ds_read_b128 v[22:25], v30 offset:1024
	ds_read_b128 v[26:29], v30 offset:2048
	ds_read_b128 v[30:33], v30 offset:3072
	s_add_u32 s56, s56, 0x40000
	s_addc_u32 s57, s57, 0
	s_mov_b32 m0, s63
	v_lshl_add_u64 v[216:217], s[56:57], 0, v[164:165]
	ds_read_b128 v[192:195], v188 offset:32768
	ds_read_b128 v[196:199], v188 offset:33792
	ds_read_b128 v[200:203], v188 offset:34816
	ds_read_b128 v[204:207], v188 offset:35840
	ds_read_b128 v[208:211], v188 offset:36864
	ds_read_b128 v[212:215], v188 offset:37888
	ds_read_b128 v[220:223], v188 offset:38912
	ds_read_b128 v[224:227], v188 offset:39936
	global_load_lds_dwordx4 v[216:217], off
	v_lshl_add_u64 v[216:217], s[56:57], 0, v[166:167]
	s_mov_b32 m0, s64
	s_nop 0
	global_load_lds_dwordx4 v[216:217], off
	s_waitcnt vmcnt(8) lgkmcnt(0)
	s_barrier
	v_mfma_scale_f32_16x16x128_f8f6f4 v[158:161], v[2:9], v[192:199], v[158:161], v189, v190 op_sel_hi:[0,0,0]
	v_mfma_scale_f32_16x16x128_f8f6f4 v[150:153], v[10:17], v[192:199], v[150:153], v189, v190 op_sel_hi:[0,0,0]
	v_mfma_scale_f32_16x16x128_f8f6f4 v[142:145], v[2:9], v[200:207], v[142:145], v189, v190 op_sel_hi:[0,0,0]
	v_mfma_scale_f32_16x16x128_f8f6f4 v[134:137], v[10:17], v[200:207], v[134:137], v189, v190 op_sel_hi:[0,0,0]
	v_mfma_scale_f32_16x16x128_f8f6f4 v[126:129], v[2:9], v[208:215], v[126:129], v189, v190 op_sel_hi:[0,0,0]
	v_mfma_scale_f32_16x16x128_f8f6f4 v[118:121], v[10:17], v[208:215], v[118:121], v189, v190 op_sel_hi:[0,0,0]
	v_mfma_scale_f32_16x16x128_f8f6f4 v[110:113], v[2:9], v[220:227], v[110:113], v189, v190 op_sel_hi:[0,0,0]
	v_mfma_scale_f32_16x16x128_f8f6f4 v[102:105], v[10:17], v[220:227], v[102:105], v189, v190 op_sel_hi:[0,0,0]
	v_mfma_scale_f32_16x16x128_f8f6f4 v[154:157], v[18:25], v[192:199], v[154:157], v189, v190 op_sel_hi:[0,0,0]
	v_mfma_scale_f32_16x16x128_f8f6f4 v[146:149], v[26:33], v[192:199], v[146:149], v189, v190 op_sel_hi:[0,0,0]
	v_mfma_scale_f32_16x16x128_f8f6f4 v[138:141], v[18:25], v[200:207], v[138:141], v189, v190 op_sel_hi:[0,0,0]
	v_mfma_scale_f32_16x16x128_f8f6f4 v[130:133], v[26:33], v[200:207], v[130:133], v189, v190 op_sel_hi:[0,0,0]
	v_mfma_scale_f32_16x16x128_f8f6f4 v[122:125], v[18:25], v[208:215], v[122:125], v189, v190 op_sel_hi:[0,0,0]
	v_mfma_scale_f32_16x16x128_f8f6f4 v[114:117], v[26:33], v[208:215], v[114:117], v189, v190 op_sel_hi:[0,0,0]
	v_mfma_scale_f32_16x16x128_f8f6f4 v[106:109], v[18:25], v[220:227], v[106:109], v189, v190 op_sel_hi:[0,0,0]
	v_mfma_scale_f32_16x16x128_f8f6f4 v[98:101], v[26:33], v[220:227], v[98:101], v189, v190 op_sel_hi:[0,0,0]
	s_barrier
	s_add_i32 s56, s73, s61
	v_lshl_add_u64 v[216:217], v[178:179], 0, s[20:21]
	s_mov_b32 m0, s56
	ds_read_b128 v[192:195], v188 offset:49152
	ds_read_b128 v[196:199], v188 offset:50176
	ds_read_b128 v[200:203], v188 offset:51200
	ds_read_b128 v[204:207], v188 offset:52224
	ds_read_b128 v[208:211], v188 offset:53248
	ds_read_b128 v[212:215], v188 offset:54272
	ds_read_b128 v[220:223], v188 offset:55296
	ds_read_b128 v[224:227], v188 offset:56320
	global_load_lds_dwordx4 v[216:217], off
	v_lshl_add_u64 v[216:217], v[178:179], 0, s[22:23]
	s_add_i32 m0, s56, 0x2000
	s_add_i32 s56, s74, s61
	global_load_lds_dwordx4 v[216:217], off
	v_lshl_add_u64 v[216:217], v[178:179], 0, s[26:27]
	s_mov_b32 m0, s56
	v_lshl_add_u64 v[178:179], v[178:179], 0, s[36:37]
	global_load_lds_dwordx4 v[216:217], off
	s_add_i32 m0, s56, 0x2000
	s_nop 0
	global_load_lds_dwordx4 v[178:179], off
	v_lshl_add_u64 v[178:179], v[180:181], 0, s[24:25]
	s_mov_b32 m0, s66
	s_nop 0
	global_load_lds_dwordx4 v[178:179], off
	v_lshl_add_u64 v[178:179], v[182:183], 0, s[24:25]
	s_mov_b32 m0, s67
	s_nop 0
	global_load_lds_dwordx4 v[178:179], off
	s_waitcnt vmcnt(8) lgkmcnt(0)
	s_barrier
	v_mfma_scale_f32_16x16x128_f8f6f4 v[94:97], v[2:9], v[192:199], v[94:97], v189, v190 op_sel_hi:[0,0,0]
	v_mfma_scale_f32_16x16x128_f8f6f4 v[86:89], v[10:17], v[192:199], v[86:89], v189, v190 op_sel_hi:[0,0,0]
	v_mfma_scale_f32_16x16x128_f8f6f4 v[78:81], v[2:9], v[200:207], v[78:81], v189, v190 op_sel_hi:[0,0,0]
	v_mfma_scale_f32_16x16x128_f8f6f4 v[70:73], v[10:17], v[200:207], v[70:73], v189, v190 op_sel_hi:[0,0,0]
	v_mfma_scale_f32_16x16x128_f8f6f4 v[62:65], v[2:9], v[208:215], v[62:65], v189, v190 op_sel_hi:[0,0,0]
	v_mfma_scale_f32_16x16x128_f8f6f4 v[54:57], v[10:17], v[208:215], v[54:57], v189, v190 op_sel_hi:[0,0,0]
	v_mfma_scale_f32_16x16x128_f8f6f4 v[46:49], v[2:9], v[220:227], v[46:49], v189, v190 op_sel_hi:[0,0,0]
	v_mfma_scale_f32_16x16x128_f8f6f4 v[38:41], v[10:17], v[220:227], v[38:41], v189, v190 op_sel_hi:[0,0,0]
	v_mfma_scale_f32_16x16x128_f8f6f4 v[90:93], v[18:25], v[192:199], v[90:93], v189, v190 op_sel_hi:[0,0,0]
	v_mfma_scale_f32_16x16x128_f8f6f4 v[82:85], v[26:33], v[192:199], v[82:85], v189, v190 op_sel_hi:[0,0,0]
	v_mfma_scale_f32_16x16x128_f8f6f4 v[74:77], v[18:25], v[200:207], v[74:77], v189, v190 op_sel_hi:[0,0,0]
	v_mfma_scale_f32_16x16x128_f8f6f4 v[66:69], v[26:33], v[200:207], v[66:69], v189, v190 op_sel_hi:[0,0,0]
	v_mfma_scale_f32_16x16x128_f8f6f4 v[58:61], v[18:25], v[208:215], v[58:61], v189, v190 op_sel_hi:[0,0,0]
	v_mfma_scale_f32_16x16x128_f8f6f4 v[50:53], v[26:33], v[208:215], v[50:53], v189, v190 op_sel_hi:[0,0,0]
	v_mfma_scale_f32_16x16x128_f8f6f4 v[42:45], v[18:25], v[220:227], v[42:45], v189, v190 op_sel_hi:[0,0,0]
	v_mfma_scale_f32_16x16x128_f8f6f4 v[34:37], v[26:33], v[220:227], v[34:37], v189, v190 op_sel_hi:[0,0,0]
	s_barrier
	s_add_i32 s49, s49, 2
	s_add_u32 s4, s4, 0x100
	s_addc_u32 s5, s5, 0
	s_cmp_gt_u32 s49, 13
	v_lshl_add_u64 v[176:177], v[176:177], 0, s[40:41]
.LBB0_1497:
	ds_read_b128 v[26:29], v186
	ds_read_b128 v[30:33], v186 offset:1024
	ds_read_b128 v[18:21], v186 offset:2048
	ds_read_b128 v[22:25], v186 offset:3072
	ds_read_b128 v[10:13], v187
	ds_read_b128 v[14:17], v187 offset:1024
	ds_read_b128 v[2:5], v187 offset:2048
	ds_read_b128 v[6:9], v187 offset:3072
	s_add_u32 s56, s4, 0xfffc0080
	s_addc_u32 s57, s5, -1
	s_cmp_eq_u32 s49, 12
	s_cselect_b64 vcc, -1, 0
	s_cselect_b32 s57, s2, s57
	s_cselect_b32 s56, s47, s56
	v_cndmask_b32_e32 v179, v177, v175, vcc
	v_cndmask_b32_e32 v178, v176, v174, vcc
	v_lshl_add_u64 v[180:181], s[4:5], 0, v[168:169]
	s_add_i32 m0, s62, 0xc000
	ds_read_b128 v[192:195], v188
	ds_read_b128 v[196:199], v188 offset:1024
	ds_read_b128 v[200:203], v188 offset:2048
	ds_read_b128 v[204:207], v188 offset:3072
	ds_read_b128 v[208:211], v188 offset:4096
	ds_read_b128 v[212:215], v188 offset:5120
	ds_read_b128 v[220:223], v188 offset:6144
	ds_read_b128 v[224:227], v188 offset:7168
	global_load_lds_dwordx4 v[180:181], off
	v_lshl_add_u64 v[180:181], s[4:5], 0, v[170:171]
	s_add_i32 m0, s62, 0xe000
	s_nop 0
	global_load_lds_dwordx4 v[180:181], off
	s_waitcnt vmcnt(8) lgkmcnt(0)
	s_barrier
	v_mfma_scale_f32_16x16x128_f8f6f4 v[158:161], v[26:33], v[192:199], v[158:161], v189, v190 op_sel_hi:[0,0,0]
	v_mfma_scale_f32_16x16x128_f8f6f4 v[150:153], v[18:25], v[192:199], v[150:153], v189, v190 op_sel_hi:[0,0,0]
	v_mfma_scale_f32_16x16x128_f8f6f4 v[142:145], v[26:33], v[200:207], v[142:145], v189, v190 op_sel_hi:[0,0,0]
	v_mfma_scale_f32_16x16x128_f8f6f4 v[134:137], v[18:25], v[200:207], v[134:137], v189, v190 op_sel_hi:[0,0,0]
	v_mfma_scale_f32_16x16x128_f8f6f4 v[126:129], v[26:33], v[208:215], v[126:129], v189, v190 op_sel_hi:[0,0,0]
	v_mfma_scale_f32_16x16x128_f8f6f4 v[118:121], v[18:25], v[208:215], v[118:121], v189, v190 op_sel_hi:[0,0,0]
	v_mfma_scale_f32_16x16x128_f8f6f4 v[110:113], v[26:33], v[220:227], v[110:113], v189, v190 op_sel_hi:[0,0,0]
	v_mfma_scale_f32_16x16x128_f8f6f4 v[102:105], v[18:25], v[220:227], v[102:105], v189, v190 op_sel_hi:[0,0,0]
	v_mfma_scale_f32_16x16x128_f8f6f4 v[154:157], v[10:17], v[192:199], v[154:157], v189, v190 op_sel_hi:[0,0,0]
	v_mfma_scale_f32_16x16x128_f8f6f4 v[146:149], v[2:9], v[192:199], v[146:149], v189, v190 op_sel_hi:[0,0,0]
	v_mfma_scale_f32_16x16x128_f8f6f4 v[138:141], v[10:17], v[200:207], v[138:141], v189, v190 op_sel_hi:[0,0,0]
	v_mfma_scale_f32_16x16x128_f8f6f4 v[130:133], v[2:9], v[200:207], v[130:133], v189, v190 op_sel_hi:[0,0,0]
	v_mfma_scale_f32_16x16x128_f8f6f4 v[122:125], v[10:17], v[208:215], v[122:125], v189, v190 op_sel_hi:[0,0,0]
	v_mfma_scale_f32_16x16x128_f8f6f4 v[114:117], v[2:9], v[208:215], v[114:117], v189, v190 op_sel_hi:[0,0,0]
	v_mfma_scale_f32_16x16x128_f8f6f4 v[106:109], v[10:17], v[220:227], v[106:109], v189, v190 op_sel_hi:[0,0,0]
	v_mfma_scale_f32_16x16x128_f8f6f4 v[98:101], v[2:9], v[220:227], v[98:101], v189, v190 op_sel_hi:[0,0,0]
	s_barrier
	s_add_i32 s73, s69, s61
	v_lshl_add_u64 v[178:179], v[178:179], 0, v[162:163]
	s_mov_b32 m0, s73
	ds_read_b128 v[192:195], v188 offset:16384
	ds_read_b128 v[196:199], v188 offset:17408
	ds_read_b128 v[200:203], v188 offset:18432
	ds_read_b128 v[204:207], v188 offset:19456
	ds_read_b128 v[208:211], v188 offset:20480
	ds_read_b128 v[212:215], v188 offset:21504
	ds_read_b128 v[220:223], v188 offset:22528
	ds_read_b128 v[224:227], v188 offset:23552
	global_load_lds_dwordx4 v[178:179], off
	v_lshl_add_u64 v[180:181], v[178:179], 0, s[10:11]
	s_add_i32 m0, s73, 0x2000
	s_add_i32 s73, s70, s61
	global_load_lds_dwordx4 v[180:181], off
	v_lshl_add_u64 v[180:181], v[178:179], 0, s[12:13]
	s_mov_b32 m0, s73
	v_lshl_add_u64 v[182:183], s[56:57], 0, v[166:167]
	global_load_lds_dwordx4 v[180:181], off
	v_lshl_add_u64 v[180:181], v[178:179], 0, s[14:15]
	s_add_i32 m0, s73, 0x2000
	s_nop 0
	global_load_lds_dwordx4 v[180:181], off
	v_lshl_add_u64 v[180:181], s[56:57], 0, v[164:165]
	s_mov_b32 m0, s62
	s_nop 0
	global_load_lds_dwordx4 v[180:181], off
	s_mov_b32 m0, s53
	s_nop 0
	global_load_lds_dwordx4 v[182:183], off
	s_waitcnt vmcnt(8) lgkmcnt(0)
	s_barrier
	v_mfma_scale_f32_16x16x128_f8f6f4 v[94:97], v[26:33], v[192:199], v[94:97], v189, v190 op_sel_hi:[0,0,0]
	v_mfma_scale_f32_16x16x128_f8f6f4 v[86:89], v[18:25], v[192:199], v[86:89], v189, v190 op_sel_hi:[0,0,0]
	v_mfma_scale_f32_16x16x128_f8f6f4 v[78:81], v[26:33], v[200:207], v[78:81], v189, v190 op_sel_hi:[0,0,0]
	v_mfma_scale_f32_16x16x128_f8f6f4 v[70:73], v[18:25], v[200:207], v[70:73], v189, v190 op_sel_hi:[0,0,0]
	v_mfma_scale_f32_16x16x128_f8f6f4 v[62:65], v[26:33], v[208:215], v[62:65], v189, v190 op_sel_hi:[0,0,0]
	v_mfma_scale_f32_16x16x128_f8f6f4 v[54:57], v[18:25], v[208:215], v[54:57], v189, v190 op_sel_hi:[0,0,0]
	v_mfma_scale_f32_16x16x128_f8f6f4 v[46:49], v[26:33], v[220:227], v[46:49], v189, v190 op_sel_hi:[0,0,0]
	v_mfma_scale_f32_16x16x128_f8f6f4 v[38:41], v[18:25], v[220:227], v[38:41], v189, v190 op_sel_hi:[0,0,0]
	v_mfma_scale_f32_16x16x128_f8f6f4 v[90:93], v[10:17], v[192:199], v[90:93], v189, v190 op_sel_hi:[0,0,0]
	v_mfma_scale_f32_16x16x128_f8f6f4 v[82:85], v[2:9], v[192:199], v[82:85], v189, v190 op_sel_hi:[0,0,0]
	v_mfma_scale_f32_16x16x128_f8f6f4 v[74:77], v[10:17], v[200:207], v[74:77], v189, v190 op_sel_hi:[0,0,0]
	v_mfma_scale_f32_16x16x128_f8f6f4 v[66:69], v[2:9], v[200:207], v[66:69], v189, v190 op_sel_hi:[0,0,0]
	v_mfma_scale_f32_16x16x128_f8f6f4 v[58:61], v[10:17], v[208:215], v[58:61], v189, v190 op_sel_hi:[0,0,0]
	v_mfma_scale_f32_16x16x128_f8f6f4 v[50:53], v[2:9], v[208:215], v[50:53], v189, v190 op_sel_hi:[0,0,0]
	v_mfma_scale_f32_16x16x128_f8f6f4 v[42:45], v[10:17], v[220:227], v[42:45], v189, v190 op_sel_hi:[0,0,0]
	v_mfma_scale_f32_16x16x128_f8f6f4 v[34:37], v[2:9], v[220:227], v[34:37], v189, v190 op_sel_hi:[0,0,0]
	s_barrier
	s_add_i32 s73, 0, 0x18000
	s_add_i32 s74, 0, 0x1c000
	v_add_u32_e32 v14, s73, v184
	v_add_u32_e32 v30, s74, v184
	ds_read_b128 v[2:5], v14
	ds_read_b128 v[6:9], v14 offset:1024
	ds_read_b128 v[10:13], v14 offset:2048
	ds_read_b128 v[14:17], v14 offset:3072
	ds_read_b128 v[18:21], v30
	ds_read_b128 v[22:25], v30 offset:1024
	ds_read_b128 v[26:29], v30 offset:2048
	ds_read_b128 v[30:33], v30 offset:3072
	s_add_u32 s56, s56, 0x40000
	s_addc_u32 s57, s57, 0
	s_mov_b32 m0, s63
	v_lshl_add_u64 v[216:217], s[56:57], 0, v[164:165]
	ds_read_b128 v[192:195], v188 offset:32768
	ds_read_b128 v[196:199], v188 offset:33792
	ds_read_b128 v[200:203], v188 offset:34816
	ds_read_b128 v[204:207], v188 offset:35840
	ds_read_b128 v[208:211], v188 offset:36864
	ds_read_b128 v[212:215], v188 offset:37888
	ds_read_b128 v[220:223], v188 offset:38912
	ds_read_b128 v[224:227], v188 offset:39936
	global_load_lds_dwordx4 v[216:217], off
	v_lshl_add_u64 v[216:217], s[56:57], 0, v[166:167]
	s_mov_b32 m0, s64
	s_nop 0
	global_load_lds_dwordx4 v[216:217], off
	s_waitcnt vmcnt(8) lgkmcnt(0)
	s_barrier
	v_mfma_scale_f32_16x16x128_f8f6f4 v[158:161], v[2:9], v[192:199], v[158:161], v189, v190 op_sel_hi:[0,0,0]
	v_mfma_scale_f32_16x16x128_f8f6f4 v[150:153], v[10:17], v[192:199], v[150:153], v189, v190 op_sel_hi:[0,0,0]
	v_mfma_scale_f32_16x16x128_f8f6f4 v[142:145], v[2:9], v[200:207], v[142:145], v189, v190 op_sel_hi:[0,0,0]
	v_mfma_scale_f32_16x16x128_f8f6f4 v[134:137], v[10:17], v[200:207], v[134:137], v189, v190 op_sel_hi:[0,0,0]
	v_mfma_scale_f32_16x16x128_f8f6f4 v[126:129], v[2:9], v[208:215], v[126:129], v189, v190 op_sel_hi:[0,0,0]
	v_mfma_scale_f32_16x16x128_f8f6f4 v[118:121], v[10:17], v[208:215], v[118:121], v189, v190 op_sel_hi:[0,0,0]
	v_mfma_scale_f32_16x16x128_f8f6f4 v[110:113], v[2:9], v[220:227], v[110:113], v189, v190 op_sel_hi:[0,0,0]
	v_mfma_scale_f32_16x16x128_f8f6f4 v[102:105], v[10:17], v[220:227], v[102:105], v189, v190 op_sel_hi:[0,0,0]
	v_mfma_scale_f32_16x16x128_f8f6f4 v[154:157], v[18:25], v[192:199], v[154:157], v189, v190 op_sel_hi:[0,0,0]
	v_mfma_scale_f32_16x16x128_f8f6f4 v[146:149], v[26:33], v[192:199], v[146:149], v189, v190 op_sel_hi:[0,0,0]
	v_mfma_scale_f32_16x16x128_f8f6f4 v[138:141], v[18:25], v[200:207], v[138:141], v189, v190 op_sel_hi:[0,0,0]
	v_mfma_scale_f32_16x16x128_f8f6f4 v[130:133], v[26:33], v[200:207], v[130:133], v189, v190 op_sel_hi:[0,0,0]
	v_mfma_scale_f32_16x16x128_f8f6f4 v[122:125], v[18:25], v[208:215], v[122:125], v189, v190 op_sel_hi:[0,0,0]
	v_mfma_scale_f32_16x16x128_f8f6f4 v[114:117], v[26:33], v[208:215], v[114:117], v189, v190 op_sel_hi:[0,0,0]
	v_mfma_scale_f32_16x16x128_f8f6f4 v[106:109], v[18:25], v[220:227], v[106:109], v189, v190 op_sel_hi:[0,0,0]
	v_mfma_scale_f32_16x16x128_f8f6f4 v[98:101], v[26:33], v[220:227], v[98:101], v189, v190 op_sel_hi:[0,0,0]
	s_barrier
	s_add_i32 s56, s73, s61
	v_lshl_add_u64 v[216:217], v[178:179], 0, s[20:21]
	s_mov_b32 m0, s56
	ds_read_b128 v[192:195], v188 offset:49152
	ds_read_b128 v[196:199], v188 offset:50176
	ds_read_b128 v[200:203], v188 offset:51200
	ds_read_b128 v[204:207], v188 offset:52224
	ds_read_b128 v[208:211], v188 offset:53248
	ds_read_b128 v[212:215], v188 offset:54272
	ds_read_b128 v[220:223], v188 offset:55296
	ds_read_b128 v[224:227], v188 offset:56320
	global_load_lds_dwordx4 v[216:217], off
	v_lshl_add_u64 v[216:217], v[178:179], 0, s[22:23]
	s_add_i32 m0, s56, 0x2000
	s_add_i32 s56, s74, s61
	global_load_lds_dwordx4 v[216:217], off
	v_lshl_add_u64 v[216:217], v[178:179], 0, s[26:27]
	s_mov_b32 m0, s56
	v_lshl_add_u64 v[178:179], v[178:179], 0, s[36:37]
	global_load_lds_dwordx4 v[216:217], off
	s_add_i32 m0, s56, 0x2000
	s_nop 0
	global_load_lds_dwordx4 v[178:179], off
	v_lshl_add_u64 v[178:179], v[180:181], 0, s[24:25]
	s_mov_b32 m0, s66
	s_nop 0
	global_load_lds_dwordx4 v[178:179], off
	v_lshl_add_u64 v[178:179], v[182:183], 0, s[24:25]
	s_mov_b32 m0, s67
	s_nop 0
	global_load_lds_dwordx4 v[178:179], off
	s_waitcnt vmcnt(8) lgkmcnt(0)
	s_barrier
	v_mfma_scale_f32_16x16x128_f8f6f4 v[94:97], v[2:9], v[192:199], v[94:97], v189, v190 op_sel_hi:[0,0,0]
	v_mfma_scale_f32_16x16x128_f8f6f4 v[86:89], v[10:17], v[192:199], v[86:89], v189, v190 op_sel_hi:[0,0,0]
	v_mfma_scale_f32_16x16x128_f8f6f4 v[78:81], v[2:9], v[200:207], v[78:81], v189, v190 op_sel_hi:[0,0,0]
	v_mfma_scale_f32_16x16x128_f8f6f4 v[70:73], v[10:17], v[200:207], v[70:73], v189, v190 op_sel_hi:[0,0,0]
	v_mfma_scale_f32_16x16x128_f8f6f4 v[62:65], v[2:9], v[208:215], v[62:65], v189, v190 op_sel_hi:[0,0,0]
	v_mfma_scale_f32_16x16x128_f8f6f4 v[54:57], v[10:17], v[208:215], v[54:57], v189, v190 op_sel_hi:[0,0,0]
	v_mfma_scale_f32_16x16x128_f8f6f4 v[46:49], v[2:9], v[220:227], v[46:49], v189, v190 op_sel_hi:[0,0,0]
	v_mfma_scale_f32_16x16x128_f8f6f4 v[38:41], v[10:17], v[220:227], v[38:41], v189, v190 op_sel_hi:[0,0,0]
	v_mfma_scale_f32_16x16x128_f8f6f4 v[90:93], v[18:25], v[192:199], v[90:93], v189, v190 op_sel_hi:[0,0,0]
	v_mfma_scale_f32_16x16x128_f8f6f4 v[82:85], v[26:33], v[192:199], v[82:85], v189, v190 op_sel_hi:[0,0,0]
	v_mfma_scale_f32_16x16x128_f8f6f4 v[74:77], v[18:25], v[200:207], v[74:77], v189, v190 op_sel_hi:[0,0,0]
	v_mfma_scale_f32_16x16x128_f8f6f4 v[66:69], v[26:33], v[200:207], v[66:69], v189, v190 op_sel_hi:[0,0,0]
	v_mfma_scale_f32_16x16x128_f8f6f4 v[58:61], v[18:25], v[208:215], v[58:61], v189, v190 op_sel_hi:[0,0,0]
	v_mfma_scale_f32_16x16x128_f8f6f4 v[50:53], v[26:33], v[208:215], v[50:53], v189, v190 op_sel_hi:[0,0,0]
	v_mfma_scale_f32_16x16x128_f8f6f4 v[42:45], v[18:25], v[220:227], v[42:45], v189, v190 op_sel_hi:[0,0,0]
	v_mfma_scale_f32_16x16x128_f8f6f4 v[34:37], v[26:33], v[220:227], v[34:37], v189, v190 op_sel_hi:[0,0,0]
	s_barrier
	s_add_i32 s49, s49, 2
	s_add_u32 s4, s4, 0x100
	s_addc_u32 s5, s5, 0
	s_cmp_gt_u32 s49, 13
	v_lshl_add_u64 v[176:177], v[176:177], 0, s[40:41]
	s_cbranch_scc0 .LBB0_1497
	s_and_b64 vcc, exec, s[38:39]
	s_cbranch_vccz .LBB0_1500
	s_barrier

.LBB0_1567:
	s_add_u32 s56, s56, 0xb0080
	v_lshl_add_u64 v[176:177], v[2:3], 0, s[44:45]
	s_addc_u32 s57, s57, 0
	s_mov_b32 s53, -2
	ds_read_b128 v[26:29], v186
	ds_read_b128 v[30:33], v186 offset:1024
	ds_read_b128 v[18:21], v186 offset:2048
	ds_read_b128 v[22:25], v186 offset:3072
	ds_read_b128 v[10:13], v187
	ds_read_b128 v[14:17], v187 offset:1024
	ds_read_b128 v[2:5], v187 offset:2048
	ds_read_b128 v[6:9], v187 offset:3072
	s_add_u32 s58, s56, 0xfff50080
	s_addc_u32 s59, s57, -1
	s_cmp_eq_u32 s53, 40
	s_cselect_b64 vcc, -1, 0
	s_cselect_b32 s59, s5, s59
	s_cselect_b32 s58, s4, s58
	v_cndmask_b32_e32 v179, v177, v175, vcc
	v_cndmask_b32_e32 v178, v176, v174, vcc
	v_lshl_add_u64 v[180:181], s[56:57], 0, v[170:171]
	s_add_i32 m0, s61, 0xc000
	ds_read_b128 v[192:195], v188
	ds_read_b128 v[196:199], v188 offset:1024
	ds_read_b128 v[200:203], v188 offset:2048
	ds_read_b128 v[204:207], v188 offset:3072
	ds_read_b128 v[208:211], v188 offset:4096
	ds_read_b128 v[212:215], v188 offset:5120
	ds_read_b128 v[220:223], v188 offset:6144
	ds_read_b128 v[224:227], v188 offset:7168
	global_load_lds_dwordx4 v[180:181], off
	v_lshl_add_u64 v[180:181], s[56:57], 0, v[172:173]
	s_add_i32 m0, s61, 0xe000
	s_nop 0
	global_load_lds_dwordx4 v[180:181], off
	s_waitcnt vmcnt(24) lgkmcnt(0)
	s_barrier
	v_mfma_scale_f32_16x16x128_f8f6f4 v[158:161], v[26:33], v[192:199], 0, v189, v190 op_sel_hi:[0,0,0]
	v_mfma_scale_f32_16x16x128_f8f6f4 v[154:157], v[18:25], v[192:199], 0, v189, v190 op_sel_hi:[0,0,0]
	v_mfma_scale_f32_16x16x128_f8f6f4 v[150:153], v[26:33], v[200:207], 0, v189, v190 op_sel_hi:[0,0,0]
	v_mfma_scale_f32_16x16x128_f8f6f4 v[142:145], v[18:25], v[200:207], 0, v189, v190 op_sel_hi:[0,0,0]
	v_mfma_scale_f32_16x16x128_f8f6f4 v[134:137], v[26:33], v[208:215], 0, v189, v190 op_sel_hi:[0,0,0]
	v_mfma_scale_f32_16x16x128_f8f6f4 v[126:129], v[18:25], v[208:215], 0, v189, v190 op_sel_hi:[0,0,0]
	v_mfma_scale_f32_16x16x128_f8f6f4 v[118:121], v[26:33], v[220:227], 0, v189, v190 op_sel_hi:[0,0,0]
	v_mfma_scale_f32_16x16x128_f8f6f4 v[110:113], v[18:25], v[220:227], 0, v189, v190 op_sel_hi:[0,0,0]
	v_mfma_scale_f32_16x16x128_f8f6f4 v[146:149], v[10:17], v[192:199], 0, v189, v190 op_sel_hi:[0,0,0]
	v_mfma_scale_f32_16x16x128_f8f6f4 v[138:141], v[2:9], v[192:199], 0, v189, v190 op_sel_hi:[0,0,0]
	v_mfma_scale_f32_16x16x128_f8f6f4 v[130:133], v[10:17], v[200:207], 0, v189, v190 op_sel_hi:[0,0,0]
	v_mfma_scale_f32_16x16x128_f8f6f4 v[122:125], v[2:9], v[200:207], 0, v189, v190 op_sel_hi:[0,0,0]
	v_mfma_scale_f32_16x16x128_f8f6f4 v[114:117], v[10:17], v[208:215], 0, v189, v190 op_sel_hi:[0,0,0]
	v_mfma_scale_f32_16x16x128_f8f6f4 v[106:109], v[2:9], v[208:215], 0, v189, v190 op_sel_hi:[0,0,0]
	v_mfma_scale_f32_16x16x128_f8f6f4 v[102:105], v[10:17], v[220:227], 0, v189, v190 op_sel_hi:[0,0,0]
	v_mfma_scale_f32_16x16x128_f8f6f4 v[98:101], v[2:9], v[220:227], 0, v189, v190 op_sel_hi:[0,0,0]
	s_barrier
	s_add_i32 s80, s69, s33
	v_lshl_add_u64 v[178:179], v[178:179], 0, v[164:165]
	s_mov_b32 m0, s80
	ds_read_b128 v[192:195], v188 offset:16384
	ds_read_b128 v[196:199], v188 offset:17408
	ds_read_b128 v[200:203], v188 offset:18432
	ds_read_b128 v[204:207], v188 offset:19456
	ds_read_b128 v[208:211], v188 offset:20480
	ds_read_b128 v[212:215], v188 offset:21504
	ds_read_b128 v[220:223], v188 offset:22528
	ds_read_b128 v[224:227], v188 offset:23552
	global_load_lds_dwordx4 v[178:179], off
	v_lshl_add_u64 v[180:181], v[178:179], 0, s[10:11]
	s_add_i32 m0, s80, 0x2000
	s_add_i32 s80, s70, s33
	global_load_lds_dwordx4 v[180:181], off
	v_lshl_add_u64 v[180:181], v[178:179], 0, s[12:13]
	s_mov_b32 m0, s80
	v_lshl_add_u64 v[182:183], s[58:59], 0, v[168:169]
	global_load_lds_dwordx4 v[180:181], off
	v_lshl_add_u64 v[180:181], v[178:179], 0, s[14:15]
	s_add_i32 m0, s80, 0x2000
	s_nop 0
	global_load_lds_dwordx4 v[180:181], off
	v_lshl_add_u64 v[180:181], s[58:59], 0, v[166:167]
	s_mov_b32 m0, s61
	s_nop 0
	global_load_lds_dwordx4 v[180:181], off
	s_mov_b32 m0, s62
	s_nop 0
	global_load_lds_dwordx4 v[182:183], off
	s_waitcnt vmcnt(24) lgkmcnt(0)
	s_barrier
	v_mfma_scale_f32_16x16x128_f8f6f4 v[94:97], v[26:33], v[192:199], 0, v189, v190 op_sel_hi:[0,0,0]
	v_mfma_scale_f32_16x16x128_f8f6f4 v[90:93], v[18:25], v[192:199], 0, v189, v190 op_sel_hi:[0,0,0]
	v_mfma_scale_f32_16x16x128_f8f6f4 v[86:89], v[26:33], v[200:207], 0, v189, v190 op_sel_hi:[0,0,0]
	v_mfma_scale_f32_16x16x128_f8f6f4 v[78:81], v[18:25], v[200:207], 0, v189, v190 op_sel_hi:[0,0,0]
	v_mfma_scale_f32_16x16x128_f8f6f4 v[70:73], v[26:33], v[208:215], 0, v189, v190 op_sel_hi:[0,0,0]
	v_mfma_scale_f32_16x16x128_f8f6f4 v[62:65], v[18:25], v[208:215], 0, v189, v190 op_sel_hi:[0,0,0]
	v_mfma_scale_f32_16x16x128_f8f6f4 v[54:57], v[26:33], v[220:227], 0, v189, v190 op_sel_hi:[0,0,0]
	v_mfma_scale_f32_16x16x128_f8f6f4 v[46:49], v[18:25], v[220:227], 0, v189, v190 op_sel_hi:[0,0,0]
	v_mfma_scale_f32_16x16x128_f8f6f4 v[82:85], v[10:17], v[192:199], 0, v189, v190 op_sel_hi:[0,0,0]
	v_mfma_scale_f32_16x16x128_f8f6f4 v[74:77], v[2:9], v[192:199], 0, v189, v190 op_sel_hi:[0,0,0]
	v_mfma_scale_f32_16x16x128_f8f6f4 v[66:69], v[10:17], v[200:207], 0, v189, v190 op_sel_hi:[0,0,0]
	v_mfma_scale_f32_16x16x128_f8f6f4 v[58:61], v[2:9], v[200:207], 0, v189, v190 op_sel_hi:[0,0,0]
	v_mfma_scale_f32_16x16x128_f8f6f4 v[50:53], v[10:17], v[208:215], 0, v189, v190 op_sel_hi:[0,0,0]
	v_mfma_scale_f32_16x16x128_f8f6f4 v[42:45], v[2:9], v[208:215], 0, v189, v190 op_sel_hi:[0,0,0]
	v_mfma_scale_f32_16x16x128_f8f6f4 v[38:41], v[10:17], v[220:227], 0, v189, v190 op_sel_hi:[0,0,0]
	v_mfma_scale_f32_16x16x128_f8f6f4 v[34:37], v[2:9], v[220:227], 0, v189, v190 op_sel_hi:[0,0,0]
	s_barrier
	s_add_i32 s80, 0, 0x18000
	s_add_i32 s81, 0, 0x1c000
	v_add_u32_e32 v14, s80, v184
	v_add_u32_e32 v30, s81, v184
	ds_read_b128 v[2:5], v14
	ds_read_b128 v[6:9], v14 offset:1024
	ds_read_b128 v[10:13], v14 offset:2048
	ds_read_b128 v[14:17], v14 offset:3072
	ds_read_b128 v[18:21], v30
	ds_read_b128 v[22:25], v30 offset:1024
	ds_read_b128 v[26:29], v30 offset:2048
	ds_read_b128 v[30:33], v30 offset:3072
	s_add_u32 s58, s58, 0xb0000
	s_addc_u32 s59, s59, 0
	s_mov_b32 m0, s63
	v_lshl_add_u64 v[216:217], s[58:59], 0, v[166:167]
	ds_read_b128 v[192:195], v188 offset:32768
	ds_read_b128 v[196:199], v188 offset:33792
	ds_read_b128 v[200:203], v188 offset:34816
	ds_read_b128 v[204:207], v188 offset:35840
	ds_read_b128 v[208:211], v188 offset:36864
	ds_read_b128 v[212:215], v188 offset:37888
	ds_read_b128 v[220:223], v188 offset:38912
	ds_read_b128 v[224:227], v188 offset:39936
	global_load_lds_dwordx4 v[216:217], off
	v_lshl_add_u64 v[216:217], s[58:59], 0, v[168:169]
	s_mov_b32 m0, s64
	s_nop 0
	global_load_lds_dwordx4 v[216:217], off
	s_waitcnt vmcnt(8) lgkmcnt(0)
	s_barrier
	v_mfma_scale_f32_16x16x128_f8f6f4 v[158:161], v[2:9], v[192:199], v[158:161], v189, v190 op_sel_hi:[0,0,0]
	v_mfma_scale_f32_16x16x128_f8f6f4 v[154:157], v[10:17], v[192:199], v[154:157], v189, v190 op_sel_hi:[0,0,0]
	v_mfma_scale_f32_16x16x128_f8f6f4 v[150:153], v[2:9], v[200:207], v[150:153], v189, v190 op_sel_hi:[0,0,0]
	v_mfma_scale_f32_16x16x128_f8f6f4 v[142:145], v[10:17], v[200:207], v[142:145], v189, v190 op_sel_hi:[0,0,0]
	v_mfma_scale_f32_16x16x128_f8f6f4 v[134:137], v[2:9], v[208:215], v[134:137], v189, v190 op_sel_hi:[0,0,0]
	v_mfma_scale_f32_16x16x128_f8f6f4 v[126:129], v[10:17], v[208:215], v[126:129], v189, v190 op_sel_hi:[0,0,0]
	v_mfma_scale_f32_16x16x128_f8f6f4 v[118:121], v[2:9], v[220:227], v[118:121], v189, v190 op_sel_hi:[0,0,0]
	v_mfma_scale_f32_16x16x128_f8f6f4 v[110:113], v[10:17], v[220:227], v[110:113], v189, v190 op_sel_hi:[0,0,0]
	v_mfma_scale_f32_16x16x128_f8f6f4 v[146:149], v[18:25], v[192:199], v[146:149], v189, v190 op_sel_hi:[0,0,0]
	v_mfma_scale_f32_16x16x128_f8f6f4 v[138:141], v[26:33], v[192:199], v[138:141], v189, v190 op_sel_hi:[0,0,0]
	v_mfma_scale_f32_16x16x128_f8f6f4 v[130:133], v[18:25], v[200:207], v[130:133], v189, v190 op_sel_hi:[0,0,0]
	v_mfma_scale_f32_16x16x128_f8f6f4 v[122:125], v[26:33], v[200:207], v[122:125], v189, v190 op_sel_hi:[0,0,0]
	v_mfma_scale_f32_16x16x128_f8f6f4 v[114:117], v[18:25], v[208:215], v[114:117], v189, v190 op_sel_hi:[0,0,0]
	v_mfma_scale_f32_16x16x128_f8f6f4 v[106:109], v[26:33], v[208:215], v[106:109], v189, v190 op_sel_hi:[0,0,0]
	v_mfma_scale_f32_16x16x128_f8f6f4 v[102:105], v[18:25], v[220:227], v[102:105], v189, v190 op_sel_hi:[0,0,0]
	v_mfma_scale_f32_16x16x128_f8f6f4 v[98:101], v[26:33], v[220:227], v[98:101], v189, v190 op_sel_hi:[0,0,0]
	s_barrier
	s_add_i32 s58, s80, s33
	v_lshl_add_u64 v[216:217], v[178:179], 0, s[24:25]
	s_mov_b32 m0, s58
	ds_read_b128 v[192:195], v188 offset:49152
	ds_read_b128 v[196:199], v188 offset:50176
	ds_read_b128 v[200:203], v188 offset:51200
	ds_read_b128 v[204:207], v188 offset:52224
	ds_read_b128 v[208:211], v188 offset:53248
	ds_read_b128 v[212:215], v188 offset:54272
	ds_read_b128 v[220:223], v188 offset:55296
	ds_read_b128 v[224:227], v188 offset:56320
	global_load_lds_dwordx4 v[216:217], off
	v_lshl_add_u64 v[216:217], v[178:179], 0, s[26:27]
	s_add_i32 m0, s58, 0x2000
	s_add_i32 s58, s81, s33
	global_load_lds_dwordx4 v[216:217], off
	v_lshl_add_u64 v[216:217], v[178:179], 0, s[38:39]
	s_mov_b32 m0, s58
	v_lshl_add_u64 v[178:179], v[178:179], 0, s[40:41]
	global_load_lds_dwordx4 v[216:217], off
	s_add_i32 m0, s58, 0x2000
	s_nop 0
	global_load_lds_dwordx4 v[178:179], off
	v_lshl_add_u64 v[178:179], v[180:181], 0, s[36:37]
	s_mov_b32 m0, s66
	s_nop 0
	global_load_lds_dwordx4 v[178:179], off
	v_lshl_add_u64 v[178:179], v[182:183], 0, s[36:37]
	s_mov_b32 m0, s67
	s_nop 0
	global_load_lds_dwordx4 v[178:179], off
	s_waitcnt vmcnt(8) lgkmcnt(0)
	s_barrier
	v_mfma_scale_f32_16x16x128_f8f6f4 v[94:97], v[2:9], v[192:199], v[94:97], v189, v190 op_sel_hi:[0,0,0]
	v_mfma_scale_f32_16x16x128_f8f6f4 v[90:93], v[10:17], v[192:199], v[90:93], v189, v190 op_sel_hi:[0,0,0]
	v_mfma_scale_f32_16x16x128_f8f6f4 v[86:89], v[2:9], v[200:207], v[86:89], v189, v190 op_sel_hi:[0,0,0]
	v_mfma_scale_f32_16x16x128_f8f6f4 v[78:81], v[10:17], v[200:207], v[78:81], v189, v190 op_sel_hi:[0,0,0]
	v_mfma_scale_f32_16x16x128_f8f6f4 v[70:73], v[2:9], v[208:215], v[70:73], v189, v190 op_sel_hi:[0,0,0]
	v_mfma_scale_f32_16x16x128_f8f6f4 v[62:65], v[10:17], v[208:215], v[62:65], v189, v190 op_sel_hi:[0,0,0]
	v_mfma_scale_f32_16x16x128_f8f6f4 v[54:57], v[2:9], v[220:227], v[54:57], v189, v190 op_sel_hi:[0,0,0]
	v_mfma_scale_f32_16x16x128_f8f6f4 v[46:49], v[10:17], v[220:227], v[46:49], v189, v190 op_sel_hi:[0,0,0]
	v_mfma_scale_f32_16x16x128_f8f6f4 v[82:85], v[18:25], v[192:199], v[82:85], v189, v190 op_sel_hi:[0,0,0]
	v_mfma_scale_f32_16x16x128_f8f6f4 v[74:77], v[26:33], v[192:199], v[74:77], v189, v190 op_sel_hi:[0,0,0]
	v_mfma_scale_f32_16x16x128_f8f6f4 v[66:69], v[18:25], v[200:207], v[66:69], v189, v190 op_sel_hi:[0,0,0]
	v_mfma_scale_f32_16x16x128_f8f6f4 v[58:61], v[26:33], v[200:207], v[58:61], v189, v190 op_sel_hi:[0,0,0]
	v_mfma_scale_f32_16x16x128_f8f6f4 v[50:53], v[18:25], v[208:215], v[50:53], v189, v190 op_sel_hi:[0,0,0]
	v_mfma_scale_f32_16x16x128_f8f6f4 v[42:45], v[26:33], v[208:215], v[42:45], v189, v190 op_sel_hi:[0,0,0]
	v_mfma_scale_f32_16x16x128_f8f6f4 v[38:41], v[18:25], v[220:227], v[38:41], v189, v190 op_sel_hi:[0,0,0]
	v_mfma_scale_f32_16x16x128_f8f6f4 v[34:37], v[26:33], v[220:227], v[34:37], v189, v190 op_sel_hi:[0,0,0]
	s_barrier
	s_add_i32 s53, s53, 2
	s_add_u32 s56, s56, 0x100
	s_addc_u32 s57, s57, 0
	s_cmp_gt_u32 s53, 41
	v_lshl_add_u64 v[176:177], v[176:177], 0, s[44:45]
.LBB0_1568:
	ds_read_b128 v[26:29], v186
	ds_read_b128 v[30:33], v186 offset:1024
	ds_read_b128 v[18:21], v186 offset:2048
	ds_read_b128 v[22:25], v186 offset:3072
	ds_read_b128 v[10:13], v187
	ds_read_b128 v[14:17], v187 offset:1024
	ds_read_b128 v[2:5], v187 offset:2048
	ds_read_b128 v[6:9], v187 offset:3072
	s_add_u32 s58, s56, 0xfff50080
	s_addc_u32 s59, s57, -1
	s_cmp_eq_u32 s53, 40
	s_cselect_b64 vcc, -1, 0
	s_cselect_b32 s59, s5, s59
	s_cselect_b32 s58, s4, s58
	v_cndmask_b32_e32 v179, v177, v175, vcc
	v_cndmask_b32_e32 v178, v176, v174, vcc
	v_lshl_add_u64 v[180:181], s[56:57], 0, v[170:171]
	s_add_i32 m0, s61, 0xc000
	ds_read_b128 v[192:195], v188
	ds_read_b128 v[196:199], v188 offset:1024
	ds_read_b128 v[200:203], v188 offset:2048
	ds_read_b128 v[204:207], v188 offset:3072
	ds_read_b128 v[208:211], v188 offset:4096
	ds_read_b128 v[212:215], v188 offset:5120
	ds_read_b128 v[220:223], v188 offset:6144
	ds_read_b128 v[224:227], v188 offset:7168
	global_load_lds_dwordx4 v[180:181], off
	v_lshl_add_u64 v[180:181], s[56:57], 0, v[172:173]
	s_add_i32 m0, s61, 0xe000
	s_nop 0
	global_load_lds_dwordx4 v[180:181], off
	s_waitcnt vmcnt(8) lgkmcnt(0)
	s_barrier
	v_mfma_scale_f32_16x16x128_f8f6f4 v[158:161], v[26:33], v[192:199], v[158:161], v189, v190 op_sel_hi:[0,0,0]
	v_mfma_scale_f32_16x16x128_f8f6f4 v[154:157], v[18:25], v[192:199], v[154:157], v189, v190 op_sel_hi:[0,0,0]
	v_mfma_scale_f32_16x16x128_f8f6f4 v[150:153], v[26:33], v[200:207], v[150:153], v189, v190 op_sel_hi:[0,0,0]
	v_mfma_scale_f32_16x16x128_f8f6f4 v[142:145], v[18:25], v[200:207], v[142:145], v189, v190 op_sel_hi:[0,0,0]
	v_mfma_scale_f32_16x16x128_f8f6f4 v[134:137], v[26:33], v[208:215], v[134:137], v189, v190 op_sel_hi:[0,0,0]
	v_mfma_scale_f32_16x16x128_f8f6f4 v[126:129], v[18:25], v[208:215], v[126:129], v189, v190 op_sel_hi:[0,0,0]
	v_mfma_scale_f32_16x16x128_f8f6f4 v[118:121], v[26:33], v[220:227], v[118:121], v189, v190 op_sel_hi:[0,0,0]
	v_mfma_scale_f32_16x16x128_f8f6f4 v[110:113], v[18:25], v[220:227], v[110:113], v189, v190 op_sel_hi:[0,0,0]
	v_mfma_scale_f32_16x16x128_f8f6f4 v[146:149], v[10:17], v[192:199], v[146:149], v189, v190 op_sel_hi:[0,0,0]
	v_mfma_scale_f32_16x16x128_f8f6f4 v[138:141], v[2:9], v[192:199], v[138:141], v189, v190 op_sel_hi:[0,0,0]
	v_mfma_scale_f32_16x16x128_f8f6f4 v[130:133], v[10:17], v[200:207], v[130:133], v189, v190 op_sel_hi:[0,0,0]
	v_mfma_scale_f32_16x16x128_f8f6f4 v[122:125], v[2:9], v[200:207], v[122:125], v189, v190 op_sel_hi:[0,0,0]
	v_mfma_scale_f32_16x16x128_f8f6f4 v[114:117], v[10:17], v[208:215], v[114:117], v189, v190 op_sel_hi:[0,0,0]
	v_mfma_scale_f32_16x16x128_f8f6f4 v[106:109], v[2:9], v[208:215], v[106:109], v189, v190 op_sel_hi:[0,0,0]
	v_mfma_scale_f32_16x16x128_f8f6f4 v[102:105], v[10:17], v[220:227], v[102:105], v189, v190 op_sel_hi:[0,0,0]
	v_mfma_scale_f32_16x16x128_f8f6f4 v[98:101], v[2:9], v[220:227], v[98:101], v189, v190 op_sel_hi:[0,0,0]
	s_barrier
	s_add_i32 s80, s69, s33
	v_lshl_add_u64 v[178:179], v[178:179], 0, v[164:165]
	s_mov_b32 m0, s80
	ds_read_b128 v[192:195], v188 offset:16384
	ds_read_b128 v[196:199], v188 offset:17408
	ds_read_b128 v[200:203], v188 offset:18432
	ds_read_b128 v[204:207], v188 offset:19456
	ds_read_b128 v[208:211], v188 offset:20480
	ds_read_b128 v[212:215], v188 offset:21504
	ds_read_b128 v[220:223], v188 offset:22528
	ds_read_b128 v[224:227], v188 offset:23552
	global_load_lds_dwordx4 v[178:179], off
	v_lshl_add_u64 v[180:181], v[178:179], 0, s[10:11]
	s_add_i32 m0, s80, 0x2000
	s_add_i32 s80, s70, s33
	global_load_lds_dwordx4 v[180:181], off
	v_lshl_add_u64 v[180:181], v[178:179], 0, s[12:13]
	s_mov_b32 m0, s80
	v_lshl_add_u64 v[182:183], s[58:59], 0, v[168:169]
	global_load_lds_dwordx4 v[180:181], off
	v_lshl_add_u64 v[180:181], v[178:179], 0, s[14:15]
	s_add_i32 m0, s80, 0x2000
	s_nop 0
	global_load_lds_dwordx4 v[180:181], off
	v_lshl_add_u64 v[180:181], s[58:59], 0, v[166:167]
	s_mov_b32 m0, s61
	s_nop 0
	global_load_lds_dwordx4 v[180:181], off
	s_mov_b32 m0, s62
	s_nop 0
	global_load_lds_dwordx4 v[182:183], off
	s_waitcnt vmcnt(8) lgkmcnt(0)
	s_barrier
	v_mfma_scale_f32_16x16x128_f8f6f4 v[94:97], v[26:33], v[192:199], v[94:97], v189, v190 op_sel_hi:[0,0,0]
	v_mfma_scale_f32_16x16x128_f8f6f4 v[90:93], v[18:25], v[192:199], v[90:93], v189, v190 op_sel_hi:[0,0,0]
	v_mfma_scale_f32_16x16x128_f8f6f4 v[86:89], v[26:33], v[200:207], v[86:89], v189, v190 op_sel_hi:[0,0,0]
	v_mfma_scale_f32_16x16x128_f8f6f4 v[78:81], v[18:25], v[200:207], v[78:81], v189, v190 op_sel_hi:[0,0,0]
	v_mfma_scale_f32_16x16x128_f8f6f4 v[70:73], v[26:33], v[208:215], v[70:73], v189, v190 op_sel_hi:[0,0,0]
	v_mfma_scale_f32_16x16x128_f8f6f4 v[62:65], v[18:25], v[208:215], v[62:65], v189, v190 op_sel_hi:[0,0,0]
	v_mfma_scale_f32_16x16x128_f8f6f4 v[54:57], v[26:33], v[220:227], v[54:57], v189, v190 op_sel_hi:[0,0,0]
	v_mfma_scale_f32_16x16x128_f8f6f4 v[46:49], v[18:25], v[220:227], v[46:49], v189, v190 op_sel_hi:[0,0,0]
	v_mfma_scale_f32_16x16x128_f8f6f4 v[82:85], v[10:17], v[192:199], v[82:85], v189, v190 op_sel_hi:[0,0,0]
	v_mfma_scale_f32_16x16x128_f8f6f4 v[74:77], v[2:9], v[192:199], v[74:77], v189, v190 op_sel_hi:[0,0,0]
	v_mfma_scale_f32_16x16x128_f8f6f4 v[66:69], v[10:17], v[200:207], v[66:69], v189, v190 op_sel_hi:[0,0,0]
	v_mfma_scale_f32_16x16x128_f8f6f4 v[58:61], v[2:9], v[200:207], v[58:61], v189, v190 op_sel_hi:[0,0,0]
	v_mfma_scale_f32_16x16x128_f8f6f4 v[50:53], v[10:17], v[208:215], v[50:53], v189, v190 op_sel_hi:[0,0,0]
	v_mfma_scale_f32_16x16x128_f8f6f4 v[42:45], v[2:9], v[208:215], v[42:45], v189, v190 op_sel_hi:[0,0,0]
	v_mfma_scale_f32_16x16x128_f8f6f4 v[38:41], v[10:17], v[220:227], v[38:41], v189, v190 op_sel_hi:[0,0,0]
	v_mfma_scale_f32_16x16x128_f8f6f4 v[34:37], v[2:9], v[220:227], v[34:37], v189, v190 op_sel_hi:[0,0,0]
	s_barrier
	s_add_i32 s80, 0, 0x18000
	s_add_i32 s81, 0, 0x1c000
	v_add_u32_e32 v14, s80, v184
	v_add_u32_e32 v30, s81, v184
	ds_read_b128 v[2:5], v14
	ds_read_b128 v[6:9], v14 offset:1024
	ds_read_b128 v[10:13], v14 offset:2048
	ds_read_b128 v[14:17], v14 offset:3072
	ds_read_b128 v[18:21], v30
	ds_read_b128 v[22:25], v30 offset:1024
	ds_read_b128 v[26:29], v30 offset:2048
	ds_read_b128 v[30:33], v30 offset:3072
	s_add_u32 s58, s58, 0xb0000
	s_addc_u32 s59, s59, 0
	s_mov_b32 m0, s63
	v_lshl_add_u64 v[216:217], s[58:59], 0, v[166:167]
	ds_read_b128 v[192:195], v188 offset:32768
	ds_read_b128 v[196:199], v188 offset:33792
	ds_read_b128 v[200:203], v188 offset:34816
	ds_read_b128 v[204:207], v188 offset:35840
	ds_read_b128 v[208:211], v188 offset:36864
	ds_read_b128 v[212:215], v188 offset:37888
	ds_read_b128 v[220:223], v188 offset:38912
	ds_read_b128 v[224:227], v188 offset:39936
	global_load_lds_dwordx4 v[216:217], off
	v_lshl_add_u64 v[216:217], s[58:59], 0, v[168:169]
	s_mov_b32 m0, s64
	s_nop 0
	global_load_lds_dwordx4 v[216:217], off
	s_waitcnt vmcnt(8) lgkmcnt(0)
	s_barrier
	v_mfma_scale_f32_16x16x128_f8f6f4 v[158:161], v[2:9], v[192:199], v[158:161], v189, v190 op_sel_hi:[0,0,0]
	v_mfma_scale_f32_16x16x128_f8f6f4 v[154:157], v[10:17], v[192:199], v[154:157], v189, v190 op_sel_hi:[0,0,0]
	v_mfma_scale_f32_16x16x128_f8f6f4 v[150:153], v[2:9], v[200:207], v[150:153], v189, v190 op_sel_hi:[0,0,0]
	v_mfma_scale_f32_16x16x128_f8f6f4 v[142:145], v[10:17], v[200:207], v[142:145], v189, v190 op_sel_hi:[0,0,0]
	v_mfma_scale_f32_16x16x128_f8f6f4 v[134:137], v[2:9], v[208:215], v[134:137], v189, v190 op_sel_hi:[0,0,0]
	v_mfma_scale_f32_16x16x128_f8f6f4 v[126:129], v[10:17], v[208:215], v[126:129], v189, v190 op_sel_hi:[0,0,0]
	v_mfma_scale_f32_16x16x128_f8f6f4 v[118:121], v[2:9], v[220:227], v[118:121], v189, v190 op_sel_hi:[0,0,0]
	v_mfma_scale_f32_16x16x128_f8f6f4 v[110:113], v[10:17], v[220:227], v[110:113], v189, v190 op_sel_hi:[0,0,0]
	v_mfma_scale_f32_16x16x128_f8f6f4 v[146:149], v[18:25], v[192:199], v[146:149], v189, v190 op_sel_hi:[0,0,0]
	v_mfma_scale_f32_16x16x128_f8f6f4 v[138:141], v[26:33], v[192:199], v[138:141], v189, v190 op_sel_hi:[0,0,0]
	v_mfma_scale_f32_16x16x128_f8f6f4 v[130:133], v[18:25], v[200:207], v[130:133], v189, v190 op_sel_hi:[0,0,0]
	v_mfma_scale_f32_16x16x128_f8f6f4 v[122:125], v[26:33], v[200:207], v[122:125], v189, v190 op_sel_hi:[0,0,0]
	v_mfma_scale_f32_16x16x128_f8f6f4 v[114:117], v[18:25], v[208:215], v[114:117], v189, v190 op_sel_hi:[0,0,0]
	v_mfma_scale_f32_16x16x128_f8f6f4 v[106:109], v[26:33], v[208:215], v[106:109], v189, v190 op_sel_hi:[0,0,0]
	v_mfma_scale_f32_16x16x128_f8f6f4 v[102:105], v[18:25], v[220:227], v[102:105], v189, v190 op_sel_hi:[0,0,0]
	v_mfma_scale_f32_16x16x128_f8f6f4 v[98:101], v[26:33], v[220:227], v[98:101], v189, v190 op_sel_hi:[0,0,0]
	s_barrier
	s_add_i32 s58, s80, s33
	v_lshl_add_u64 v[216:217], v[178:179], 0, s[24:25]
	s_mov_b32 m0, s58
	ds_read_b128 v[192:195], v188 offset:49152
	ds_read_b128 v[196:199], v188 offset:50176
	ds_read_b128 v[200:203], v188 offset:51200
	ds_read_b128 v[204:207], v188 offset:52224
	ds_read_b128 v[208:211], v188 offset:53248
	ds_read_b128 v[212:215], v188 offset:54272
	ds_read_b128 v[220:223], v188 offset:55296
	ds_read_b128 v[224:227], v188 offset:56320
	global_load_lds_dwordx4 v[216:217], off
	v_lshl_add_u64 v[216:217], v[178:179], 0, s[26:27]
	s_add_i32 m0, s58, 0x2000
	s_add_i32 s58, s81, s33
	global_load_lds_dwordx4 v[216:217], off
	v_lshl_add_u64 v[216:217], v[178:179], 0, s[38:39]
	s_mov_b32 m0, s58
	v_lshl_add_u64 v[178:179], v[178:179], 0, s[40:41]
	global_load_lds_dwordx4 v[216:217], off
	s_add_i32 m0, s58, 0x2000
	s_nop 0
	global_load_lds_dwordx4 v[178:179], off
	v_lshl_add_u64 v[178:179], v[180:181], 0, s[36:37]
	s_mov_b32 m0, s66
	s_nop 0
	global_load_lds_dwordx4 v[178:179], off
	v_lshl_add_u64 v[178:179], v[182:183], 0, s[36:37]
	s_mov_b32 m0, s67
	s_nop 0
	global_load_lds_dwordx4 v[178:179], off
	s_waitcnt vmcnt(8) lgkmcnt(0)
	s_barrier
	v_mfma_scale_f32_16x16x128_f8f6f4 v[94:97], v[2:9], v[192:199], v[94:97], v189, v190 op_sel_hi:[0,0,0]
	v_mfma_scale_f32_16x16x128_f8f6f4 v[90:93], v[10:17], v[192:199], v[90:93], v189, v190 op_sel_hi:[0,0,0]
	v_mfma_scale_f32_16x16x128_f8f6f4 v[86:89], v[2:9], v[200:207], v[86:89], v189, v190 op_sel_hi:[0,0,0]
	v_mfma_scale_f32_16x16x128_f8f6f4 v[78:81], v[10:17], v[200:207], v[78:81], v189, v190 op_sel_hi:[0,0,0]
	v_mfma_scale_f32_16x16x128_f8f6f4 v[70:73], v[2:9], v[208:215], v[70:73], v189, v190 op_sel_hi:[0,0,0]
	v_mfma_scale_f32_16x16x128_f8f6f4 v[62:65], v[10:17], v[208:215], v[62:65], v189, v190 op_sel_hi:[0,0,0]
	v_mfma_scale_f32_16x16x128_f8f6f4 v[54:57], v[2:9], v[220:227], v[54:57], v189, v190 op_sel_hi:[0,0,0]
	v_mfma_scale_f32_16x16x128_f8f6f4 v[46:49], v[10:17], v[220:227], v[46:49], v189, v190 op_sel_hi:[0,0,0]
	v_mfma_scale_f32_16x16x128_f8f6f4 v[82:85], v[18:25], v[192:199], v[82:85], v189, v190 op_sel_hi:[0,0,0]
	v_mfma_scale_f32_16x16x128_f8f6f4 v[74:77], v[26:33], v[192:199], v[74:77], v189, v190 op_sel_hi:[0,0,0]
	v_mfma_scale_f32_16x16x128_f8f6f4 v[66:69], v[18:25], v[200:207], v[66:69], v189, v190 op_sel_hi:[0,0,0]
	v_mfma_scale_f32_16x16x128_f8f6f4 v[58:61], v[26:33], v[200:207], v[58:61], v189, v190 op_sel_hi:[0,0,0]
	v_mfma_scale_f32_16x16x128_f8f6f4 v[50:53], v[18:25], v[208:215], v[50:53], v189, v190 op_sel_hi:[0,0,0]
	v_mfma_scale_f32_16x16x128_f8f6f4 v[42:45], v[26:33], v[208:215], v[42:45], v189, v190 op_sel_hi:[0,0,0]
	v_mfma_scale_f32_16x16x128_f8f6f4 v[38:41], v[18:25], v[220:227], v[38:41], v189, v190 op_sel_hi:[0,0,0]
	v_mfma_scale_f32_16x16x128_f8f6f4 v[34:37], v[26:33], v[220:227], v[34:37], v189, v190 op_sel_hi:[0,0,0]
	s_barrier
	s_add_i32 s53, s53, 2
	s_add_u32 s56, s56, 0x100
	s_addc_u32 s57, s57, 0
	s_cmp_gt_u32 s53, 41
	v_lshl_add_u64 v[176:177], v[176:177], 0, s[44:45]
	s_cbranch_scc0 .LBB0_1568
	s_and_b64 vcc, exec, s[42:43]
	s_cbranch_vccz .LBB0_1571
	s_barrier
